# c3 + fp8 GEMMs use v_mfma_f32_16x16x128_f8f6f4 (no scale prefix, unit scale) instead of the MX-scaled form
# speedup vs baseline: 1.0063x; 1.0063x over previous
; #define GAS __attribute__((address_space(1)))
; #define LAS __attribute__((address_space(3)))
; #define LDS_WAIT() asm volatile("s_waitcnt lgkmcnt(0)" ::: "memory")
; __device__ __forceinline__ void p0_transpose_item_f8(const float* W, int K, int N, unsigned char* WT, int drow0, int k0, int n0, float scale, LAS float* scr, int lane, const float* gain = nullptr) {
; #pragma unroll 8
;     for (int i = 0; i < 32; ++i) { const int kk = 2 * i + (lane >> 5); scr[kk * 33 + (lane & 31)] = __builtin_nontemporal_load(W + (size_t)(k0 + kk) * N + n0 + (lane & 31)); }
;     LDS_WAIT(); asm volatile("" ::: "memory");
;     const int c = lane & 7;
;     f32x4 ga = {scale, scale, scale, scale}, gb = ga;
;     if (gain) { ga = *(const GAS f32x4*)(gain + k0 + 8 * c) * scale; gb = *(const GAS f32x4*)(gain + k0 + 8 * c + 4) * scale; }
.LBB0_57:
	v_add_u32_e32 v6, s91, v2
	v_mad_u64_u32 v[4:5], s[92:93], v6, s97, 0
	v_add_u32_e32 v8, 2, v6
	v_add_u32_e32 v17, 4, v6
	v_add_u32_e32 v37, 6, v6
	v_ashrrev_i32_e32 v7, 31, v6
	v_add_u32_e32 v40, 8, v6
	v_add_u32_e32 v42, 10, v6
	v_add_u32_e32 v44, 12, v6
	v_add_u32_e32 v46, 14, v6
	v_mov_b32_e32 v6, v5
	v_ashrrev_i32_e32 v49, 31, v8
	v_mad_u64_u32 v[8:9], s[92:93], v8, s97, 0
	v_mad_u64_u32 v[28:29], s[92:93], v17, s97, 0
	v_mad_u64_u32 v[38:39], s[92:93], v37, s97, 0
	v_ashrrev_i32_e32 v51, 31, v17
	v_ashrrev_i32_e32 v17, 31, v37
	v_ashrrev_i32_e32 v37, 31, v40
	v_mad_u64_u32 v[40:41], s[92:93], v40, s97, 0
	v_ashrrev_i32_e32 v55, 31, v42
	v_mad_u64_u32 v[42:43], s[92:93], v42, s97, 0
	v_ashrrev_i32_e32 v57, 31, v44
	v_mad_u64_u32 v[44:45], s[92:93], v44, s97, 0
	v_ashrrev_i32_e32 v59, 31, v46
	v_mad_u64_u32 v[46:47], s[92:93], v46, s97, 0
	v_mad_u64_u32 v[6:7], s[92:93], v7, s97, v[6:7]
	v_mov_b32_e32 v48, v9
	v_mov_b32_e32 v50, v29
	v_mov_b32_e32 v52, v39
	v_mov_b32_e32 v54, v41
	v_mov_b32_e32 v56, v43
	v_mov_b32_e32 v58, v45
	v_mov_b32_e32 v60, v47
	v_mov_b32_e32 v5, v6
	v_mad_u64_u32 v[6:7], s[92:93], v49, s97, v[48:49]
	v_mad_u64_u32 v[48:49], s[92:93], v51, s97, v[50:51]
	v_mad_u64_u32 v[50:51], s[92:93], v17, s97, v[52:53]
	v_mad_u64_u32 v[52:53], s[92:93], v37, s97, v[54:55]
	v_mad_u64_u32 v[54:55], s[92:93], v55, s97, v[56:57]
	v_mad_u64_u32 v[56:57], s[92:93], v57, s97, v[58:59]
	v_mad_u64_u32 v[58:59], s[92:93], v59, s97, v[60:61]
	v_mov_b32_e32 v9, v6
	v_mov_b32_e32 v29, v48
	v_mov_b32_e32 v39, v50
	v_lshl_add_u64 v[4:5], v[4:5], 2, v[26:27]
	v_mov_b32_e32 v41, v52
	v_mov_b32_e32 v43, v54
	v_mov_b32_e32 v45, v56
	v_mov_b32_e32 v47, v58
	v_lshl_add_u64 v[6:7], v[8:9], 2, v[26:27]
	v_lshl_add_u64 v[8:9], v[28:29], 2, v[26:27]
	v_lshl_add_u64 v[28:29], v[38:39], 2, v[26:27]
	v_lshl_add_u64 v[38:39], v[40:41], 2, v[26:27]
	v_lshl_add_u64 v[40:41], v[42:43], 2, v[26:27]
	v_lshl_add_u64 v[42:43], v[44:45], 2, v[26:27]
	v_lshl_add_u64 v[44:45], v[46:47], 2, v[26:27]
	global_load_dword v64, v[4:5], off nt
	global_load_dword v65, v[6:7], off nt
	global_load_dword v66, v[8:9], off nt
	global_load_dword v67, v[28:29], off nt
	global_load_dword v68, v[38:39], off nt
	global_load_dword v69, v[40:41], off nt
	global_load_dword v70, v[42:43], off nt
	global_load_dword v71, v[44:45], off nt
	s_lshl_b32 s92, s97, 6
	s_mov_b32 s93, 0
	v_lshl_add_u64 v[4:5], v[4:5], 0, s[92:93]
	v_lshl_add_u64 v[6:7], v[6:7], 0, s[92:93]
	v_lshl_add_u64 v[8:9], v[8:9], 0, s[92:93]
	v_lshl_add_u64 v[28:29], v[28:29], 0, s[92:93]
	v_lshl_add_u64 v[38:39], v[38:39], 0, s[92:93]
	v_lshl_add_u64 v[40:41], v[40:41], 0, s[92:93]
	v_lshl_add_u64 v[42:43], v[42:43], 0, s[92:93]
	v_lshl_add_u64 v[44:45], v[44:45], 0, s[92:93]
	global_load_dword v72, v[4:5], off nt
	global_load_dword v73, v[6:7], off nt
	global_load_dword v74, v[8:9], off nt
	global_load_dword v75, v[28:29], off nt
	global_load_dword v76, v[38:39], off nt
	global_load_dword v77, v[40:41], off nt
	global_load_dword v78, v[42:43], off nt
	global_load_dword v79, v[44:45], off nt
	v_lshl_add_u64 v[4:5], v[4:5], 0, s[92:93]
	v_lshl_add_u64 v[6:7], v[6:7], 0, s[92:93]
	v_lshl_add_u64 v[8:9], v[8:9], 0, s[92:93]
	v_lshl_add_u64 v[28:29], v[28:29], 0, s[92:93]
	v_lshl_add_u64 v[38:39], v[38:39], 0, s[92:93]
	v_lshl_add_u64 v[40:41], v[40:41], 0, s[92:93]
	v_lshl_add_u64 v[42:43], v[42:43], 0, s[92:93]
	v_lshl_add_u64 v[44:45], v[44:45], 0, s[92:93]
	global_load_dword v80, v[4:5], off nt
	global_load_dword v81, v[6:7], off nt
	global_load_dword v82, v[8:9], off nt
	global_load_dword v83, v[28:29], off nt
	global_load_dword v84, v[38:39], off nt
	global_load_dword v85, v[40:41], off nt
	global_load_dword v86, v[42:43], off nt
	global_load_dword v87, v[44:45], off nt
	v_lshl_add_u64 v[4:5], v[4:5], 0, s[92:93]
	v_lshl_add_u64 v[6:7], v[6:7], 0, s[92:93]
	v_lshl_add_u64 v[8:9], v[8:9], 0, s[92:93]
	v_lshl_add_u64 v[28:29], v[28:29], 0, s[92:93]
	v_lshl_add_u64 v[38:39], v[38:39], 0, s[92:93]
	v_lshl_add_u64 v[40:41], v[40:41], 0, s[92:93]
	v_lshl_add_u64 v[42:43], v[42:43], 0, s[92:93]
	v_lshl_add_u64 v[44:45], v[44:45], 0, s[92:93]
	global_load_dword v88, v[4:5], off nt
	global_load_dword v89, v[6:7], off nt
	global_load_dword v90, v[8:9], off nt
	global_load_dword v91, v[28:29], off nt
	global_load_dword v92, v[38:39], off nt
	global_load_dword v93, v[40:41], off nt
	global_load_dword v94, v[42:43], off nt
	global_load_dword v95, v[44:45], off nt
	v_add_u32_e32 v29, 0x400, v3
	s_waitcnt vmcnt(30)
	ds_write2_b32 v3, v64, v65 offset1:66
	s_waitcnt vmcnt(28)
	ds_write2_b32 v3, v66, v67 offset0:132 offset1:198
	s_waitcnt vmcnt(26)
	ds_write2_b32 v29, v68, v69 offset0:8 offset1:74
	s_waitcnt vmcnt(24)
	ds_write2_b32 v29, v70, v71 offset0:140 offset1:206
	v_add_u32_e32 v3, 0x840, v3
	v_add_u32_e32 v29, 0x400, v3
	s_waitcnt vmcnt(22)
	ds_write2_b32 v3, v72, v73 offset1:66
	s_waitcnt vmcnt(20)
	ds_write2_b32 v3, v74, v75 offset0:132 offset1:198
	s_waitcnt vmcnt(18)
	ds_write2_b32 v29, v76, v77 offset0:8 offset1:74
	s_waitcnt vmcnt(16)
	ds_write2_b32 v29, v78, v79 offset0:140 offset1:206
	v_add_u32_e32 v3, 0x840, v3
	v_add_u32_e32 v29, 0x400, v3
	s_waitcnt vmcnt(14)
	ds_write2_b32 v3, v80, v81 offset1:66
	s_waitcnt vmcnt(12)
	ds_write2_b32 v3, v82, v83 offset0:132 offset1:198
	s_waitcnt vmcnt(10)
	ds_write2_b32 v29, v84, v85 offset0:8 offset1:74
	s_waitcnt vmcnt(8)
	ds_write2_b32 v29, v86, v87 offset0:140 offset1:206
	v_add_u32_e32 v3, 0x840, v3
	v_add_u32_e32 v29, 0x400, v3
	s_waitcnt vmcnt(6)
	ds_write2_b32 v3, v88, v89 offset1:66
	s_waitcnt vmcnt(4)
	ds_write2_b32 v3, v90, v91 offset0:132 offset1:198
	s_waitcnt vmcnt(2)
	ds_write2_b32 v29, v92, v93 offset0:8 offset1:74
	s_waitcnt vmcnt(0)
	ds_write2_b32 v29, v94, v95 offset0:140 offset1:206
	v_add_u32_e32 v3, 0x840, v3
	s_waitcnt lgkmcnt(0)
	s_ashr_i32 s91, s90, 31
	s_and_b64 vcc, exec, s[88:89]
	s_cbranch_vccz .LBB0_61
	v_lshl_add_u64 v[6:7], s[90:91], 2, v[20:21]
	global_load_dwordx4 v[2:5], v[6:7], off offset:16
	s_nop 0
	global_load_dwordx4 v[6:9], v[6:7], off
	s_waitcnt vmcnt(1)
	v_mov_b32_e32 v28, v3
	v_mov_b32_e32 v3, v4
	v_mov_b32_e32 v29, v5
	s_waitcnt vmcnt(0)
	v_mov_b32_e32 v4, v7
	v_mov_b32_e32 v7, v8
	v_mov_b32_e32 v5, v9
	s_branch .LBB0_62

; #define PG8_STAGE(bufoff, gbase, voff) do { _Pragma("unroll") for (int _i = 0; _i < 2; ++_i) \
;         __builtin_amdgcn_global_load_lds((const unsigned*)((const char*)(gbase) + (voff)[_i]), (PG8_LAS unsigned*)(lds + (bufoff) + ldsw + _i * 8192), 16, 0, 0); } while (0)
; #define PG8_LDA(dst, b, h) do { _Pragma("unroll") for (int m = 0; m < 4; ++m) Frag<F8>::load(dst[m], lds + PG8_SA(b, h) + aoff + m * 2048); } while (0)
; #define PG8_LDB(dst, b, h) do { _Pragma("unroll") for (int n = 0; n < 2; ++n) Frag<F8>::load(dst[n], lds + PG8_SB(b, h) + boff + n * 2048); } while (0)
; #define PG8_MMA(ai, bj, At, Bt) do { __builtin_amdgcn_s_setprio(3); _Pragma("unroll") for (int m = 0; m < 4; ++m) _Pragma("unroll") for (int n = 0; n < 2; ++n) Frag<F8>::mma(acc[ai][bj][m][n], Bt[n], At[m]); \
;         __builtin_amdgcn_s_setprio(0); } while (0)
; #define PG8_WAIT_V(n) asm volatile("s_waitcnt vmcnt(" #n ")" ::: "memory")
; #define PG8_WAIT_L(n) asm volatile("s_waitcnt lgkmcnt(" #n ")" ::: "memory")
; #define PG8_BAR __builtin_amdgcn_s_barrier()
; #define PG8_SCHED __builtin_amdgcn_sched_barrier(0)
; template <class Epi, class Sched, bool ALIGN_EPI = false, bool SP2 = false, bool F8 = false>
; __device__ __forceinline__ void gemm_phase(PG8_LAS unsigned char* lds, const Gemm g, const Sched& S, const Epi& E) {
;     ...
;             const bool last = (t == nt - 2);
;             const char* a1 = cA + (size_t)(t + 1) * kstep;
;             const char* a2 = last ? nA : cA + (size_t)(t + 2) * kstep; const char* b2 = last ? nB : cB + (size_t)(t + 2) * kstep;
;             const char* a3 = a2 + kstep; const char* b3 = b2 + kstep;
;             if (last && has_next) S.a_ready(nxt);
;             if constexpr (SP2) {
;             PG8_LDB(B0, 0, 0); PG8_LDB(B1, 0, 1); PG8_SCHED; PG8_LDA(At, 0, 0); PG8_STAGE(PG8_SA(1, 1), a1 + hstep, voffA);
;             PG8_WAIT_V(8); PG8_WAIT_L(0); PG8_BAR; PG8_MMA(0, 0, At, B0); PG8_MMA(0, 1, At, B1); PG8_BAR; PG8_SCHED;
;             PG8_LDA(At, 0, 1); PG8_STAGE(PG8_SB(0, 0), b2, voffB); PG8_STAGE(PG8_SB(0, 1), b2 + hstep, voffB); PG8_STAGE(PG8_SA(0, 0), a2, voffA);
;             PG8_WAIT_V(8); PG8_WAIT_L(0); PG8_BAR; PG8_MMA(1, 0, At, B0); PG8_MMA(1, 1, At, B1); PG8_BAR; PG8_SCHED;
.LBB0_150:
	s_ashr_i32 s25, s24, 31
	s_lshl_b64 s[4:5], s[24:25], 18
	s_add_u32 s38, s77, s4
	s_addc_u32 s39, s78, s5
	s_and_b64 s[4:5], s[8:9], exec
	s_cselect_b32 s25, s39, s71
	s_cselect_b32 s91, s38, s70
	s_ashr_i32 s31, s30, 31
	s_lshl_b64 s[4:5], s[30:31], 18
	s_add_u32 s42, s79, s4
	s_addc_u32 s43, s80, s5
	s_and_b64 s[4:5], s[8:9], exec
	s_cselect_b32 s31, s43, s73
	s_cselect_b32 s92, s42, s72
	s_add_u32 s70, s70, 0x20080
	s_addc_u32 s71, s71, 0
	s_add_u32 s93, s72, 0x100
	s_addc_u32 s95, s73, 0
	s_mov_b32 s96, -2
	ds_read_b128 v[18:21], v194
	ds_read_b128 v[22:25], v194 offset:1024
	ds_read_b128 v[26:29], v194 offset:2048
	ds_read_b128 v[30:33], v194 offset:3072
	ds_read_b128 v[2:5], v195
	ds_read_b128 v[6:9], v195 offset:1024
	ds_read_b128 v[10:13], v195 offset:2048
	ds_read_b128 v[14:17], v195 offset:3072
	s_add_u32 s0, s70, 0xfffe0080
	s_addc_u32 s1, s71, -1
	s_cmp_eq_u32 s96, 4
	s_cselect_b32 s75, s25, s1
	s_cselect_b32 s74, s91, s0
	s_cselect_b32 s73, s31, s95
	s_cselect_b32 s72, s92, s93
	v_lshl_add_u64 v[224:225], s[70:71], 0, v[174:175]
	s_add_i32 m0, s45, 0xc000
	ds_read_b128 v[182:185], v196
	ds_read_b128 v[186:189], v196 offset:1024
	ds_read_b128 v[200:203], v196 offset:2048
	ds_read_b128 v[204:207], v196 offset:3072
	ds_read_b128 v[208:211], v196 offset:4096
	ds_read_b128 v[212:215], v196 offset:5120
	ds_read_b128 v[216:219], v196 offset:6144
	ds_read_b128 v[220:223], v196 offset:7168
	global_load_lds_dwordx4 v[224:225], off
	v_lshl_add_u64 v[224:225], s[70:71], 0, v[176:177]
	s_add_i32 m0, s45, 0xe000
	s_nop 0
	global_load_lds_dwordx4 v[224:225], off
	s_waitcnt vmcnt(8)
	s_waitcnt lgkmcnt(0)
	s_barrier
	s_setprio 3
	s_waitcnt lgkmcnt(0)
	v_mfma_f32_16x16x128_f8f6f4 v[158:161], v[18:25], v[182:189], 0
	v_mfma_f32_16x16x128_f8f6f4 v[154:157], v[26:33], v[182:189], 0
	v_mfma_f32_16x16x128_f8f6f4 v[150:153], v[18:25], v[200:207], 0
	v_mfma_f32_16x16x128_f8f6f4 v[142:145], v[26:33], v[200:207], 0
	v_mfma_f32_16x16x128_f8f6f4 v[130:133], v[18:25], v[208:215], 0
	v_mfma_f32_16x16x128_f8f6f4 v[122:125], v[26:33], v[208:215], 0
	v_mfma_f32_16x16x128_f8f6f4 v[118:121], v[18:25], v[216:223], 0
	v_mfma_f32_16x16x128_f8f6f4 v[110:113], v[26:33], v[216:223], 0
	s_setprio 0
	s_setprio 3
	v_mfma_f32_16x16x128_f8f6f4 v[146:149], v[2:9], v[182:189], 0
	v_mfma_f32_16x16x128_f8f6f4 v[138:141], v[10:17], v[182:189], 0
	v_mfma_f32_16x16x128_f8f6f4 v[134:137], v[2:9], v[200:207], 0
	v_mfma_f32_16x16x128_f8f6f4 v[126:129], v[10:17], v[200:207], 0
	v_mfma_f32_16x16x128_f8f6f4 v[114:117], v[2:9], v[208:215], 0
	v_mfma_f32_16x16x128_f8f6f4 v[106:109], v[10:17], v[208:215], 0
	v_mfma_f32_16x16x128_f8f6f4 v[102:105], v[2:9], v[216:223], 0
	v_mfma_f32_16x16x128_f8f6f4 v[98:101], v[10:17], v[216:223], 0
	s_setprio 0
	s_barrier
	s_add_i32 s0, s87, s76
	v_lshl_add_u64 v[182:183], s[72:73], 0, v[170:171]
	s_mov_b32 m0, s0
	ds_read_b128 v[200:203], v196 offset:16384
	ds_read_b128 v[204:207], v196 offset:17408
	ds_read_b128 v[208:211], v196 offset:18432
	ds_read_b128 v[212:215], v196 offset:19456
	ds_read_b128 v[216:219], v196 offset:20480
	ds_read_b128 v[220:223], v196 offset:21504
	ds_read_b128 v[224:227], v196 offset:22528
	ds_read_b128 v[228:231], v196 offset:23552
	global_load_lds_dwordx4 v[182:183], off
	s_add_i32 m0, s0, 0x2000
	s_add_u32 s4, s72, 0x20000
	v_lshl_add_u64 v[184:185], s[72:73], 0, v[166:167]
	s_addc_u32 s5, s73, 0
	s_add_i32 s0, s88, s76
	global_load_lds_dwordx4 v[184:185], off
	v_lshl_add_u64 v[186:187], s[4:5], 0, v[170:171]
	s_mov_b32 m0, s0
	v_lshl_add_u64 v[188:189], s[74:75], 0, v[168:169]
	global_load_lds_dwordx4 v[186:187], off
	v_lshl_add_u64 v[186:187], s[4:5], 0, v[166:167]
	s_add_i32 m0, s0, 0x2000
	s_nop 0
	global_load_lds_dwordx4 v[186:187], off
	v_lshl_add_u64 v[186:187], s[74:75], 0, v[172:173]
	s_mov_b32 m0, s45
	s_nop 0
	global_load_lds_dwordx4 v[186:187], off
	s_mov_b32 m0, s82
	s_nop 0
	global_load_lds_dwordx4 v[188:189], off
	s_waitcnt vmcnt(8)
	s_waitcnt lgkmcnt(0)
	s_barrier
	s_setprio 3
	s_waitcnt lgkmcnt(0)
	v_mfma_f32_16x16x128_f8f6f4 v[94:97], v[18:25], v[200:207], 0
	v_mfma_f32_16x16x128_f8f6f4 v[90:93], v[26:33], v[200:207], 0
	v_mfma_f32_16x16x128_f8f6f4 v[86:89], v[18:25], v[208:215], 0
	v_mfma_f32_16x16x128_f8f6f4 v[82:85], v[26:33], v[208:215], 0
	v_mfma_f32_16x16x128_f8f6f4 v[70:73], v[18:25], v[216:223], 0
	v_mfma_f32_16x16x128_f8f6f4 v[66:69], v[26:33], v[216:223], 0
	v_mfma_f32_16x16x128_f8f6f4 v[54:57], v[18:25], v[224:231], 0
	v_mfma_f32_16x16x128_f8f6f4 v[50:53], v[26:33], v[224:231], 0
	s_setprio 0
	s_setprio 3
	v_mfma_f32_16x16x128_f8f6f4 v[78:81], v[2:9], v[200:207], 0
	v_mfma_f32_16x16x128_f8f6f4 v[74:77], v[10:17], v[200:207], 0
	v_mfma_f32_16x16x128_f8f6f4 v[62:65], v[2:9], v[208:215], 0
	v_mfma_f32_16x16x128_f8f6f4 v[58:61], v[10:17], v[208:215], 0
	v_mfma_f32_16x16x128_f8f6f4 v[46:49], v[2:9], v[216:223], 0
	v_mfma_f32_16x16x128_f8f6f4 v[42:45], v[10:17], v[216:223], 0
	v_mfma_f32_16x16x128_f8f6f4 v[38:41], v[2:9], v[224:231], 0
	v_mfma_f32_16x16x128_f8f6f4 v[34:37], v[10:17], v[224:231], 0
	s_setprio 0
	s_barrier
	s_add_i32 s0, 0, 0x18000
	s_add_i32 s1, 0, 0x1c000
	v_add_u32_e32 v14, s0, v190
	v_add_u32_e32 v30, s1, v190
	ds_read_b128 v[2:5], v14
	ds_read_b128 v[6:9], v14 offset:1024
	ds_read_b128 v[10:13], v14 offset:2048
	ds_read_b128 v[14:17], v14 offset:3072
	ds_read_b128 v[18:21], v30
	ds_read_b128 v[22:25], v30 offset:1024
	ds_read_b128 v[26:29], v30 offset:2048
	ds_read_b128 v[30:33], v30 offset:3072
	s_add_u32 s4, s74, 0x20000
	s_addc_u32 s5, s75, 0
	s_mov_b32 m0, s83
	v_lshl_add_u64 v[232:233], s[4:5], 0, v[172:173]
	ds_read_b128 v[200:203], v196 offset:32768
	ds_read_b128 v[204:207], v196 offset:33792
	ds_read_b128 v[208:211], v196 offset:34816
	ds_read_b128 v[212:215], v196 offset:35840
	ds_read_b128 v[216:219], v196 offset:36864
	ds_read_b128 v[220:223], v196 offset:37888
	ds_read_b128 v[224:227], v196 offset:38912
	ds_read_b128 v[228:231], v196 offset:39936
	global_load_lds_dwordx4 v[232:233], off
	v_lshl_add_u64 v[232:233], s[4:5], 0, v[168:169]
	s_mov_b32 m0, s84
	s_nop 0
	global_load_lds_dwordx4 v[232:233], off
	s_waitcnt vmcnt(8)
	s_waitcnt lgkmcnt(0)
	s_barrier
; #define PG8_STAGE(bufoff, gbase, voff) do { _Pragma("unroll") for (int _i = 0; _i < 2; ++_i) \
;         __builtin_amdgcn_global_load_lds((const unsigned*)((const char*)(gbase) + (voff)[_i]), (PG8_LAS unsigned*)(lds + (bufoff) + ldsw + _i * 8192), 16, 0, 0); } while (0)
; #define PG8_LDA(dst, b, h) do { _Pragma("unroll") for (int m = 0; m < 4; ++m) Frag<F8>::load(dst[m], lds + PG8_SA(b, h) + aoff + m * 2048); } while (0)
; #define PG8_LDB(dst, b, h) do { _Pragma("unroll") for (int n = 0; n < 2; ++n) Frag<F8>::load(dst[n], lds + PG8_SB(b, h) + boff + n * 2048); } while (0)
; #define PG8_MMA(ai, bj, At, Bt) do { __builtin_amdgcn_s_setprio(3); _Pragma("unroll") for (int m = 0; m < 4; ++m) _Pragma("unroll") for (int n = 0; n < 2; ++n) Frag<F8>::mma(acc[ai][bj][m][n], Bt[n], At[m]); \
;         __builtin_amdgcn_s_setprio(0); } while (0)
; #define PG8_WAIT_V(n) asm volatile("s_waitcnt vmcnt(" #n ")" ::: "memory")
; #define PG8_WAIT_L(n) asm volatile("s_waitcnt lgkmcnt(" #n ")" ::: "memory")
; #define PG8_BAR __builtin_amdgcn_s_barrier()
; #define PG8_SCHED __builtin_amdgcn_sched_barrier(0)
; template <class Epi, class Sched, bool ALIGN_EPI = false, bool SP2 = false, bool F8 = false>
; __device__ __forceinline__ void gemm_phase(PG8_LAS unsigned char* lds, const Gemm g, const Sched& S, const Epi& E) {
;     ...
;             PG8_LDB(B0, 0, 0); PG8_LDB(B1, 0, 1); PG8_SCHED; PG8_LDA(At, 0, 0); PG8_STAGE(PG8_SA(1, 1), a1 + hstep, voffA);
;             PG8_WAIT_V(8); PG8_WAIT_L(0); PG8_BAR; PG8_MMA(0, 0, At, B0); PG8_MMA(0, 1, At, B1); PG8_BAR; PG8_SCHED;
;             PG8_LDA(At, 0, 1); PG8_STAGE(PG8_SB(0, 0), b2, voffB); PG8_STAGE(PG8_SB(0, 1), b2 + hstep, voffB); PG8_STAGE(PG8_SA(0, 0), a2, voffA);
;             PG8_WAIT_V(8); PG8_WAIT_L(0); PG8_BAR; PG8_MMA(1, 0, At, B0); PG8_MMA(1, 1, At, B1); PG8_BAR; PG8_SCHED;
;             PG8_LDB(B0, 1, 0); PG8_LDB(B1, 1, 1); PG8_SCHED; PG8_LDA(At, 1, 0); PG8_STAGE(PG8_SA(0, 1), a2 + hstep, voffA);
;             PG8_WAIT_V(8); PG8_WAIT_L(0); PG8_BAR; PG8_MMA(0, 0, At, B0); PG8_MMA(0, 1, At, B1); PG8_BAR; PG8_SCHED;
;             PG8_LDA(At, 1, 1); PG8_STAGE(PG8_SB(1, 0), b3, voffB); PG8_STAGE(PG8_SB(1, 1), b3 + hstep, voffB); PG8_STAGE(PG8_SA(1, 0), a3, voffA);
;             PG8_WAIT_V(8); PG8_WAIT_L(0); PG8_BAR; PG8_MMA(1, 0, At, B0); PG8_MMA(1, 1, At, B1); PG8_BAR; PG8_SCHED;
	s_setprio 3
	s_waitcnt lgkmcnt(0)
	v_mfma_f32_16x16x128_f8f6f4 v[158:161], v[2:9], v[200:207], v[158:161]
	v_mfma_f32_16x16x128_f8f6f4 v[154:157], v[10:17], v[200:207], v[154:157]
	v_mfma_f32_16x16x128_f8f6f4 v[150:153], v[2:9], v[208:215], v[150:153]
	v_mfma_f32_16x16x128_f8f6f4 v[142:145], v[10:17], v[208:215], v[142:145]
	v_mfma_f32_16x16x128_f8f6f4 v[130:133], v[2:9], v[216:223], v[130:133]
	v_mfma_f32_16x16x128_f8f6f4 v[122:125], v[10:17], v[216:223], v[122:125]
	v_mfma_f32_16x16x128_f8f6f4 v[118:121], v[2:9], v[224:231], v[118:121]
	v_mfma_f32_16x16x128_f8f6f4 v[110:113], v[10:17], v[224:231], v[110:113]
	s_setprio 0
	s_setprio 3
	v_mfma_f32_16x16x128_f8f6f4 v[146:149], v[18:25], v[200:207], v[146:149]
	v_mfma_f32_16x16x128_f8f6f4 v[138:141], v[26:33], v[200:207], v[138:141]
	v_mfma_f32_16x16x128_f8f6f4 v[134:137], v[18:25], v[208:215], v[134:137]
	v_mfma_f32_16x16x128_f8f6f4 v[126:129], v[26:33], v[208:215], v[126:129]
	v_mfma_f32_16x16x128_f8f6f4 v[114:117], v[18:25], v[216:223], v[114:117]
	v_mfma_f32_16x16x128_f8f6f4 v[106:109], v[26:33], v[216:223], v[106:109]
	v_mfma_f32_16x16x128_f8f6f4 v[102:105], v[18:25], v[224:231], v[102:105]
	v_mfma_f32_16x16x128_f8f6f4 v[98:101], v[26:33], v[224:231], v[98:101]
	s_setprio 0
	s_barrier
	s_add_i32 s0, s0, s76
	v_lshl_add_u64 v[182:183], v[182:183], 0, s[18:19]
	s_mov_b32 m0, s0
	ds_read_b128 v[200:203], v196 offset:49152
	ds_read_b128 v[204:207], v196 offset:50176
	ds_read_b128 v[208:211], v196 offset:51200
	ds_read_b128 v[212:215], v196 offset:52224
	ds_read_b128 v[216:219], v196 offset:53248
	ds_read_b128 v[220:223], v196 offset:54272
	ds_read_b128 v[224:227], v196 offset:55296
	ds_read_b128 v[228:231], v196 offset:56320
	global_load_lds_dwordx4 v[182:183], off
	s_add_i32 m0, s0, 0x2000
	s_add_u32 s4, s72, 0x20080
	v_lshl_add_u64 v[182:183], v[184:185], 0, s[18:19]
	s_addc_u32 s5, s73, 0
	s_add_i32 s0, s1, s76
	global_load_lds_dwordx4 v[182:183], off
	v_lshl_add_u64 v[182:183], s[4:5], 0, v[170:171]
	s_mov_b32 m0, s0
	s_nop 0
	global_load_lds_dwordx4 v[182:183], off
	v_lshl_add_u64 v[182:183], s[4:5], 0, v[166:167]
	s_add_i32 m0, s0, 0x2000
	s_nop 0
	global_load_lds_dwordx4 v[182:183], off
	v_lshl_add_u64 v[182:183], v[186:187], 0, s[18:19]
	s_mov_b32 m0, s85
	s_nop 0
	global_load_lds_dwordx4 v[182:183], off
	v_lshl_add_u64 v[182:183], v[188:189], 0, s[18:19]
	s_mov_b32 m0, s86
	s_nop 0
	global_load_lds_dwordx4 v[182:183], off
	s_waitcnt vmcnt(8)
	s_waitcnt lgkmcnt(0)
	s_barrier
	s_setprio 3
	s_waitcnt lgkmcnt(0)
	v_mfma_f32_16x16x128_f8f6f4 v[94:97], v[2:9], v[200:207], v[94:97]
	v_mfma_f32_16x16x128_f8f6f4 v[90:93], v[10:17], v[200:207], v[90:93]
	v_mfma_f32_16x16x128_f8f6f4 v[86:89], v[2:9], v[208:215], v[86:89]
	v_mfma_f32_16x16x128_f8f6f4 v[82:85], v[10:17], v[208:215], v[82:85]
	v_mfma_f32_16x16x128_f8f6f4 v[70:73], v[2:9], v[216:223], v[70:73]
	v_mfma_f32_16x16x128_f8f6f4 v[66:69], v[10:17], v[216:223], v[66:69]
	v_mfma_f32_16x16x128_f8f6f4 v[54:57], v[2:9], v[224:231], v[54:57]
	v_mfma_f32_16x16x128_f8f6f4 v[50:53], v[10:17], v[224:231], v[50:53]
	s_setprio 0
	s_setprio 3
	v_mfma_f32_16x16x128_f8f6f4 v[78:81], v[18:25], v[200:207], v[78:81]
	v_mfma_f32_16x16x128_f8f6f4 v[74:77], v[26:33], v[200:207], v[74:77]
	v_mfma_f32_16x16x128_f8f6f4 v[62:65], v[18:25], v[208:215], v[62:65]
	v_mfma_f32_16x16x128_f8f6f4 v[58:61], v[26:33], v[208:215], v[58:61]
	v_mfma_f32_16x16x128_f8f6f4 v[46:49], v[18:25], v[216:223], v[46:49]
	v_mfma_f32_16x16x128_f8f6f4 v[42:45], v[26:33], v[216:223], v[42:45]
	v_mfma_f32_16x16x128_f8f6f4 v[38:41], v[18:25], v[224:231], v[38:41]
	v_mfma_f32_16x16x128_f8f6f4 v[34:37], v[26:33], v[224:231], v[34:37]
	s_setprio 0
	s_barrier
	s_add_i32 s96, s96, 2
	s_add_u32 s70, s70, 0x100
	s_addc_u32 s71, s71, 0
	s_add_u32 s93, s93, 0x100
	s_addc_u32 s95, s95, 0
	s_cmp_gt_u32 s96, 5
	s_cbranch_scc1 .Lpeel_exit_0
.LBB0_151:
	ds_read_b128 v[18:21], v194
	ds_read_b128 v[22:25], v194 offset:1024
	ds_read_b128 v[26:29], v194 offset:2048
	ds_read_b128 v[30:33], v194 offset:3072
	ds_read_b128 v[2:5], v195
	ds_read_b128 v[6:9], v195 offset:1024
	ds_read_b128 v[10:13], v195 offset:2048
	ds_read_b128 v[14:17], v195 offset:3072
	s_add_u32 s0, s70, 0xfffe0080
	s_addc_u32 s1, s71, -1
	s_cmp_eq_u32 s96, 4
	s_cselect_b32 s75, s25, s1
	s_cselect_b32 s74, s91, s0
	s_cselect_b32 s73, s31, s95
	s_cselect_b32 s72, s92, s93
	v_lshl_add_u64 v[224:225], s[70:71], 0, v[174:175]
	s_add_i32 m0, s45, 0xc000
	ds_read_b128 v[182:185], v196
	ds_read_b128 v[186:189], v196 offset:1024
	ds_read_b128 v[200:203], v196 offset:2048
	ds_read_b128 v[204:207], v196 offset:3072
	ds_read_b128 v[208:211], v196 offset:4096
	ds_read_b128 v[212:215], v196 offset:5120
	ds_read_b128 v[216:219], v196 offset:6144
	ds_read_b128 v[220:223], v196 offset:7168
	global_load_lds_dwordx4 v[224:225], off
	v_lshl_add_u64 v[224:225], s[70:71], 0, v[176:177]
	s_add_i32 m0, s45, 0xe000
	s_nop 0
	global_load_lds_dwordx4 v[224:225], off
	s_waitcnt vmcnt(8)
	s_waitcnt lgkmcnt(0)
	s_barrier
	s_setprio 3
	s_waitcnt lgkmcnt(0)
	v_mfma_f32_16x16x128_f8f6f4 v[158:161], v[18:25], v[182:189], v[158:161]
	v_mfma_f32_16x16x128_f8f6f4 v[154:157], v[26:33], v[182:189], v[154:157]
	v_mfma_f32_16x16x128_f8f6f4 v[150:153], v[18:25], v[200:207], v[150:153]
	v_mfma_f32_16x16x128_f8f6f4 v[142:145], v[26:33], v[200:207], v[142:145]
	v_mfma_f32_16x16x128_f8f6f4 v[130:133], v[18:25], v[208:215], v[130:133]
	v_mfma_f32_16x16x128_f8f6f4 v[122:125], v[26:33], v[208:215], v[122:125]
	v_mfma_f32_16x16x128_f8f6f4 v[118:121], v[18:25], v[216:223], v[118:121]
	v_mfma_f32_16x16x128_f8f6f4 v[110:113], v[26:33], v[216:223], v[110:113]
	s_setprio 0
	s_setprio 3
	v_mfma_f32_16x16x128_f8f6f4 v[146:149], v[2:9], v[182:189], v[146:149]
	v_mfma_f32_16x16x128_f8f6f4 v[138:141], v[10:17], v[182:189], v[138:141]
	v_mfma_f32_16x16x128_f8f6f4 v[134:137], v[2:9], v[200:207], v[134:137]
	v_mfma_f32_16x16x128_f8f6f4 v[126:129], v[10:17], v[200:207], v[126:129]
	v_mfma_f32_16x16x128_f8f6f4 v[114:117], v[2:9], v[208:215], v[114:117]
	v_mfma_f32_16x16x128_f8f6f4 v[106:109], v[10:17], v[208:215], v[106:109]
	v_mfma_f32_16x16x128_f8f6f4 v[102:105], v[2:9], v[216:223], v[102:105]
	v_mfma_f32_16x16x128_f8f6f4 v[98:101], v[10:17], v[216:223], v[98:101]
	s_setprio 0
	s_barrier
; #define PG8_STAGE(bufoff, gbase, voff) do { _Pragma("unroll") for (int _i = 0; _i < 2; ++_i) \
;         __builtin_amdgcn_global_load_lds((const unsigned*)((const char*)(gbase) + (voff)[_i]), (PG8_LAS unsigned*)(lds + (bufoff) + ldsw + _i * 8192), 16, 0, 0); } while (0)
; #define PG8_LDA(dst, b, h) do { _Pragma("unroll") for (int m = 0; m < 4; ++m) Frag<F8>::load(dst[m], lds + PG8_SA(b, h) + aoff + m * 2048); } while (0)
; #define PG8_LDB(dst, b, h) do { _Pragma("unroll") for (int n = 0; n < 2; ++n) Frag<F8>::load(dst[n], lds + PG8_SB(b, h) + boff + n * 2048); } while (0)
; #define PG8_MMA(ai, bj, At, Bt) do { __builtin_amdgcn_s_setprio(3); _Pragma("unroll") for (int m = 0; m < 4; ++m) _Pragma("unroll") for (int n = 0; n < 2; ++n) Frag<F8>::mma(acc[ai][bj][m][n], Bt[n], At[m]); \
;         __builtin_amdgcn_s_setprio(0); } while (0)
; #define PG8_WAIT_V(n) asm volatile("s_waitcnt vmcnt(" #n ")" ::: "memory")
; #define PG8_WAIT_L(n) asm volatile("s_waitcnt lgkmcnt(" #n ")" ::: "memory")
; #define PG8_BAR __builtin_amdgcn_s_barrier()
; #define PG8_SCHED __builtin_amdgcn_sched_barrier(0)
; template <class Epi, class Sched, bool ALIGN_EPI = false, bool SP2 = false, bool F8 = false>
; __device__ __forceinline__ void gemm_phase(PG8_LAS unsigned char* lds, const Gemm g, const Sched& S, const Epi& E) {
;     ...
;             PG8_LDA(At, 0, 1); PG8_STAGE(PG8_SB(0, 0), b2, voffB); PG8_STAGE(PG8_SB(0, 1), b2 + hstep, voffB); PG8_STAGE(PG8_SA(0, 0), a2, voffA);
;             PG8_WAIT_V(8); PG8_WAIT_L(0); PG8_BAR; PG8_MMA(1, 0, At, B0); PG8_MMA(1, 1, At, B1); PG8_BAR; PG8_SCHED;
;             PG8_LDB(B0, 1, 0); PG8_LDB(B1, 1, 1); PG8_SCHED; PG8_LDA(At, 1, 0); PG8_STAGE(PG8_SA(0, 1), a2 + hstep, voffA);
;             PG8_WAIT_V(8); PG8_WAIT_L(0); PG8_BAR; PG8_MMA(0, 0, At, B0); PG8_MMA(0, 1, At, B1); PG8_BAR; PG8_SCHED;
;             PG8_LDA(At, 1, 1); PG8_STAGE(PG8_SB(1, 0), b3, voffB); PG8_STAGE(PG8_SB(1, 1), b3 + hstep, voffB); PG8_STAGE(PG8_SA(1, 0), a3, voffA);
	s_add_i32 s0, s87, s76
	v_lshl_add_u64 v[182:183], s[72:73], 0, v[170:171]
	s_mov_b32 m0, s0
	ds_read_b128 v[200:203], v196 offset:16384
	ds_read_b128 v[204:207], v196 offset:17408
	ds_read_b128 v[208:211], v196 offset:18432
	ds_read_b128 v[212:215], v196 offset:19456
	ds_read_b128 v[216:219], v196 offset:20480
	ds_read_b128 v[220:223], v196 offset:21504
	ds_read_b128 v[224:227], v196 offset:22528
	ds_read_b128 v[228:231], v196 offset:23552
	global_load_lds_dwordx4 v[182:183], off
	s_add_i32 m0, s0, 0x2000
	s_add_u32 s4, s72, 0x20000
	v_lshl_add_u64 v[184:185], s[72:73], 0, v[166:167]
	s_addc_u32 s5, s73, 0
	s_add_i32 s0, s88, s76
	global_load_lds_dwordx4 v[184:185], off
	v_lshl_add_u64 v[186:187], s[4:5], 0, v[170:171]
	s_mov_b32 m0, s0
	v_lshl_add_u64 v[188:189], s[74:75], 0, v[168:169]
	global_load_lds_dwordx4 v[186:187], off
	v_lshl_add_u64 v[186:187], s[4:5], 0, v[166:167]
	s_add_i32 m0, s0, 0x2000
	s_nop 0
	global_load_lds_dwordx4 v[186:187], off
	v_lshl_add_u64 v[186:187], s[74:75], 0, v[172:173]
	s_mov_b32 m0, s45
	s_nop 0
	global_load_lds_dwordx4 v[186:187], off
	s_mov_b32 m0, s82
	s_nop 0
	global_load_lds_dwordx4 v[188:189], off
	s_waitcnt vmcnt(8)
	s_waitcnt lgkmcnt(0)
	s_barrier
	s_setprio 3
	s_waitcnt lgkmcnt(0)
	v_mfma_f32_16x16x128_f8f6f4 v[94:97], v[18:25], v[200:207], v[94:97]
	v_mfma_f32_16x16x128_f8f6f4 v[90:93], v[26:33], v[200:207], v[90:93]
	v_mfma_f32_16x16x128_f8f6f4 v[86:89], v[18:25], v[208:215], v[86:89]
	v_mfma_f32_16x16x128_f8f6f4 v[82:85], v[26:33], v[208:215], v[82:85]
	v_mfma_f32_16x16x128_f8f6f4 v[70:73], v[18:25], v[216:223], v[70:73]
	v_mfma_f32_16x16x128_f8f6f4 v[66:69], v[26:33], v[216:223], v[66:69]
	v_mfma_f32_16x16x128_f8f6f4 v[54:57], v[18:25], v[224:231], v[54:57]
	v_mfma_f32_16x16x128_f8f6f4 v[50:53], v[26:33], v[224:231], v[50:53]
	s_setprio 0
	s_setprio 3
	v_mfma_f32_16x16x128_f8f6f4 v[78:81], v[2:9], v[200:207], v[78:81]
	v_mfma_f32_16x16x128_f8f6f4 v[74:77], v[10:17], v[200:207], v[74:77]
	v_mfma_f32_16x16x128_f8f6f4 v[62:65], v[2:9], v[208:215], v[62:65]
	v_mfma_f32_16x16x128_f8f6f4 v[58:61], v[10:17], v[208:215], v[58:61]
	v_mfma_f32_16x16x128_f8f6f4 v[46:49], v[2:9], v[216:223], v[46:49]
	v_mfma_f32_16x16x128_f8f6f4 v[42:45], v[10:17], v[216:223], v[42:45]
	v_mfma_f32_16x16x128_f8f6f4 v[38:41], v[2:9], v[224:231], v[38:41]
	v_mfma_f32_16x16x128_f8f6f4 v[34:37], v[10:17], v[224:231], v[34:37]
	s_setprio 0
	s_barrier
	s_add_i32 s0, 0, 0x18000
	s_add_i32 s1, 0, 0x1c000
	v_add_u32_e32 v14, s0, v190
	v_add_u32_e32 v30, s1, v190
	ds_read_b128 v[2:5], v14
	ds_read_b128 v[6:9], v14 offset:1024
	ds_read_b128 v[10:13], v14 offset:2048
	ds_read_b128 v[14:17], v14 offset:3072
	ds_read_b128 v[18:21], v30
	ds_read_b128 v[22:25], v30 offset:1024
	ds_read_b128 v[26:29], v30 offset:2048
	ds_read_b128 v[30:33], v30 offset:3072
	s_add_u32 s4, s74, 0x20000
	s_addc_u32 s5, s75, 0
	s_mov_b32 m0, s83
	v_lshl_add_u64 v[232:233], s[4:5], 0, v[172:173]
	ds_read_b128 v[200:203], v196 offset:32768
	ds_read_b128 v[204:207], v196 offset:33792
	ds_read_b128 v[208:211], v196 offset:34816
	ds_read_b128 v[212:215], v196 offset:35840
	ds_read_b128 v[216:219], v196 offset:36864
	ds_read_b128 v[220:223], v196 offset:37888
	ds_read_b128 v[224:227], v196 offset:38912
	ds_read_b128 v[228:231], v196 offset:39936
	global_load_lds_dwordx4 v[232:233], off
	v_lshl_add_u64 v[232:233], s[4:5], 0, v[168:169]
	s_mov_b32 m0, s84
	s_nop 0
	global_load_lds_dwordx4 v[232:233], off
	s_waitcnt vmcnt(8)
	s_waitcnt lgkmcnt(0)
	s_barrier
; #define PG8_STAGE(bufoff, gbase, voff) do { _Pragma("unroll") for (int _i = 0; _i < 2; ++_i) \
;         __builtin_amdgcn_global_load_lds((const unsigned*)((const char*)(gbase) + (voff)[_i]), (PG8_LAS unsigned*)(lds + (bufoff) + ldsw + _i * 8192), 16, 0, 0); } while (0)
; #define PG8_LDA(dst, b, h) do { _Pragma("unroll") for (int m = 0; m < 4; ++m) Frag<F8>::load(dst[m], lds + PG8_SA(b, h) + aoff + m * 2048); } while (0)
; #define PG8_MMA(ai, bj, At, Bt) do { __builtin_amdgcn_s_setprio(3); _Pragma("unroll") for (int m = 0; m < 4; ++m) _Pragma("unroll") for (int n = 0; n < 2; ++n) Frag<F8>::mma(acc[ai][bj][m][n], Bt[n], At[m]); \
;         __builtin_amdgcn_s_setprio(0); } while (0)
; #define PG8_WAIT_V(n) asm volatile("s_waitcnt vmcnt(" #n ")" ::: "memory")
; #define PG8_WAIT_L(n) asm volatile("s_waitcnt lgkmcnt(" #n ")" ::: "memory")
; #define PG8_BAR __builtin_amdgcn_s_barrier()
; #define PG8_SCHED __builtin_amdgcn_sched_barrier(0)
; template <class Epi, class Sched, bool ALIGN_EPI = false, bool SP2 = false, bool F8 = false>
; __device__ __forceinline__ void gemm_phase(PG8_LAS unsigned char* lds, const Gemm g, const Sched& S, const Epi& E) {
;     ...
;             PG8_LDA(At, 1, 1); PG8_STAGE(PG8_SB(1, 0), b3, voffB); PG8_STAGE(PG8_SB(1, 1), b3 + hstep, voffB); PG8_STAGE(PG8_SA(1, 0), a3, voffA);
;             PG8_WAIT_V(8); PG8_WAIT_L(0); PG8_BAR; PG8_MMA(1, 0, At, B0); PG8_MMA(1, 1, At, B1); PG8_BAR; PG8_SCHED;
	s_setprio 3
	s_waitcnt lgkmcnt(0)
	v_mfma_f32_16x16x128_f8f6f4 v[158:161], v[2:9], v[200:207], v[158:161]
	v_mfma_f32_16x16x128_f8f6f4 v[154:157], v[10:17], v[200:207], v[154:157]
	v_mfma_f32_16x16x128_f8f6f4 v[150:153], v[2:9], v[208:215], v[150:153]
	v_mfma_f32_16x16x128_f8f6f4 v[142:145], v[10:17], v[208:215], v[142:145]
	v_mfma_f32_16x16x128_f8f6f4 v[130:133], v[2:9], v[216:223], v[130:133]
	v_mfma_f32_16x16x128_f8f6f4 v[122:125], v[10:17], v[216:223], v[122:125]
	v_mfma_f32_16x16x128_f8f6f4 v[118:121], v[2:9], v[224:231], v[118:121]
	v_mfma_f32_16x16x128_f8f6f4 v[110:113], v[10:17], v[224:231], v[110:113]
	s_setprio 0
	s_setprio 3
	v_mfma_f32_16x16x128_f8f6f4 v[146:149], v[18:25], v[200:207], v[146:149]
	v_mfma_f32_16x16x128_f8f6f4 v[138:141], v[26:33], v[200:207], v[138:141]
	v_mfma_f32_16x16x128_f8f6f4 v[134:137], v[18:25], v[208:215], v[134:137]
	v_mfma_f32_16x16x128_f8f6f4 v[126:129], v[26:33], v[208:215], v[126:129]
	v_mfma_f32_16x16x128_f8f6f4 v[114:117], v[18:25], v[216:223], v[114:117]
	v_mfma_f32_16x16x128_f8f6f4 v[106:109], v[26:33], v[216:223], v[106:109]
	v_mfma_f32_16x16x128_f8f6f4 v[102:105], v[18:25], v[224:231], v[102:105]
	v_mfma_f32_16x16x128_f8f6f4 v[98:101], v[26:33], v[224:231], v[98:101]
	s_setprio 0
	s_barrier
	s_add_i32 s0, s0, s76
	v_lshl_add_u64 v[182:183], v[182:183], 0, s[18:19]
	s_mov_b32 m0, s0
	ds_read_b128 v[200:203], v196 offset:49152
	ds_read_b128 v[204:207], v196 offset:50176
	ds_read_b128 v[208:211], v196 offset:51200
	ds_read_b128 v[212:215], v196 offset:52224
	ds_read_b128 v[216:219], v196 offset:53248
	ds_read_b128 v[220:223], v196 offset:54272
	ds_read_b128 v[224:227], v196 offset:55296
	ds_read_b128 v[228:231], v196 offset:56320
	global_load_lds_dwordx4 v[182:183], off
	s_add_i32 m0, s0, 0x2000
	s_add_u32 s4, s72, 0x20080
	v_lshl_add_u64 v[182:183], v[184:185], 0, s[18:19]
	s_addc_u32 s5, s73, 0
	s_add_i32 s0, s1, s76
	global_load_lds_dwordx4 v[182:183], off
	v_lshl_add_u64 v[182:183], s[4:5], 0, v[170:171]
	s_mov_b32 m0, s0
	s_nop 0
	global_load_lds_dwordx4 v[182:183], off
	v_lshl_add_u64 v[182:183], s[4:5], 0, v[166:167]
	s_add_i32 m0, s0, 0x2000
	s_nop 0
	global_load_lds_dwordx4 v[182:183], off
	v_lshl_add_u64 v[182:183], v[186:187], 0, s[18:19]
	s_mov_b32 m0, s85
	s_nop 0
	global_load_lds_dwordx4 v[182:183], off
	v_lshl_add_u64 v[182:183], v[188:189], 0, s[18:19]
	s_mov_b32 m0, s86
	s_nop 0
	global_load_lds_dwordx4 v[182:183], off
	s_waitcnt vmcnt(8)
	s_waitcnt lgkmcnt(0)
	s_barrier
	s_setprio 3
	s_waitcnt lgkmcnt(0)
	v_mfma_f32_16x16x128_f8f6f4 v[94:97], v[2:9], v[200:207], v[94:97]
	v_mfma_f32_16x16x128_f8f6f4 v[90:93], v[10:17], v[200:207], v[90:93]
	v_mfma_f32_16x16x128_f8f6f4 v[86:89], v[2:9], v[208:215], v[86:89]
	v_mfma_f32_16x16x128_f8f6f4 v[82:85], v[10:17], v[208:215], v[82:85]
	v_mfma_f32_16x16x128_f8f6f4 v[70:73], v[2:9], v[216:223], v[70:73]
	v_mfma_f32_16x16x128_f8f6f4 v[66:69], v[10:17], v[216:223], v[66:69]
	v_mfma_f32_16x16x128_f8f6f4 v[54:57], v[2:9], v[224:231], v[54:57]
	v_mfma_f32_16x16x128_f8f6f4 v[50:53], v[10:17], v[224:231], v[50:53]
	s_setprio 0
	s_setprio 3
	v_mfma_f32_16x16x128_f8f6f4 v[78:81], v[18:25], v[200:207], v[78:81]
	v_mfma_f32_16x16x128_f8f6f4 v[74:77], v[26:33], v[200:207], v[74:77]
	v_mfma_f32_16x16x128_f8f6f4 v[62:65], v[18:25], v[208:215], v[62:65]
	v_mfma_f32_16x16x128_f8f6f4 v[58:61], v[26:33], v[208:215], v[58:61]
	v_mfma_f32_16x16x128_f8f6f4 v[46:49], v[18:25], v[216:223], v[46:49]
	v_mfma_f32_16x16x128_f8f6f4 v[42:45], v[26:33], v[216:223], v[42:45]
	v_mfma_f32_16x16x128_f8f6f4 v[38:41], v[18:25], v[224:231], v[38:41]
	v_mfma_f32_16x16x128_f8f6f4 v[34:37], v[26:33], v[224:231], v[34:37]
	s_setprio 0
	s_barrier
	s_add_i32 s96, s96, 2
	s_add_u32 s70, s70, 0x100
	s_addc_u32 s71, s71, 0
	s_add_u32 s93, s93, 0x100
	s_addc_u32 s95, s95, 0
	s_cmp_gt_u32 s96, 5
	s_cbranch_scc0 .LBB0_151

; #define PG8_STAGE(bufoff, gbase, voff) do { _Pragma("unroll") for (int _i = 0; _i < 2; ++_i) \
;         __builtin_amdgcn_global_load_lds((const unsigned*)((const char*)(gbase) + (voff)[_i]), (PG8_LAS unsigned*)(lds + (bufoff) + ldsw + _i * 8192), 16, 0, 0); } while (0)
; #define PG8_LDA(dst, b, h) do { _Pragma("unroll") for (int m = 0; m < 4; ++m) Frag<F8>::load(dst[m], lds + PG8_SA(b, h) + aoff + m * 2048); } while (0)
; #define PG8_LDB(dst, b, h) do { _Pragma("unroll") for (int n = 0; n < 2; ++n) Frag<F8>::load(dst[n], lds + PG8_SB(b, h) + boff + n * 2048); } while (0)
; #define PG8_MMA(ai, bj, At, Bt) do { __builtin_amdgcn_s_setprio(3); _Pragma("unroll") for (int m = 0; m < 4; ++m) _Pragma("unroll") for (int n = 0; n < 2; ++n) Frag<F8>::mma(acc[ai][bj][m][n], Bt[n], At[m]); \
;         __builtin_amdgcn_s_setprio(0); } while (0)
; #define PG8_WAIT_V(n) asm volatile("s_waitcnt vmcnt(" #n ")" ::: "memory")
; #define PG8_WAIT_L(n) asm volatile("s_waitcnt lgkmcnt(" #n ")" ::: "memory")
; #define PG8_BAR __builtin_amdgcn_s_barrier()
; #define PG8_SCHED __builtin_amdgcn_sched_barrier(0)
; template <class Epi, class Sched, bool ALIGN_EPI = false, bool SP2 = false, bool F8 = false>
; __device__ __forceinline__ void gemm_phase(PG8_LAS unsigned char* lds, const Gemm g, const Sched& S, const Epi& E) {
;     ...
;             if constexpr (SP2) {
;             PG8_LDB(B0, 0, 0); PG8_LDB(B1, 0, 1); PG8_SCHED; PG8_LDA(At, 0, 0); PG8_STAGE(PG8_SA(1, 1), a1 + hstep, voffA);
;             PG8_WAIT_V(8); PG8_WAIT_L(0); PG8_BAR; PG8_MMA(0, 0, At, B0); PG8_MMA(0, 1, At, B1); PG8_BAR; PG8_SCHED;
;             PG8_LDA(At, 0, 1); PG8_STAGE(PG8_SB(0, 0), b2, voffB); PG8_STAGE(PG8_SB(0, 1), b2 + hstep, voffB); PG8_STAGE(PG8_SA(0, 0), a2, voffA);
;             PG8_WAIT_V(8); PG8_WAIT_L(0); PG8_BAR; PG8_MMA(1, 0, At, B0); PG8_MMA(1, 1, At, B1); PG8_BAR; PG8_SCHED;
.LBB0_162:
	ds_read_b128 v[18:21], v167
	ds_read_b128 v[22:25], v167 offset:1024
	ds_read_b128 v[26:29], v167 offset:2048
	ds_read_b128 v[30:33], v167 offset:3072
	ds_read_b128 v[2:5], v188
	ds_read_b128 v[6:9], v188 offset:1024
	ds_read_b128 v[10:13], v188 offset:2048
	ds_read_b128 v[14:17], v188 offset:3072
	s_add_u32 s0, s16, 0x100100
	s_addc_u32 s1, s17, 0
	s_add_u32 s3, s16, s45
	s_addc_u32 s4, s17, s70
	s_cmp_eq_u32 s71, 4
	s_cselect_b32 s23, s9, s1
	s_cselect_b32 s22, s8, s0
	s_cselect_b32 s19, s13, s4
	s_cselect_b32 s18, s12, s3
	s_mov_b32 m0, s72
	v_lshl_add_u64 v[218:219], s[16:17], 0, v[176:177]
	ds_read_b128 v[180:183], v189
	ds_read_b128 v[184:187], v189 offset:1024
	ds_read_b128 v[194:197], v189 offset:2048
	ds_read_b128 v[198:201], v189 offset:3072
	ds_read_b128 v[202:205], v189 offset:4096
	ds_read_b128 v[206:209], v189 offset:5120
	ds_read_b128 v[210:213], v189 offset:6144
	ds_read_b128 v[214:217], v189 offset:7168
	global_load_lds_dwordx4 v[218:219], off
	v_lshl_add_u64 v[218:219], s[16:17], 0, v[178:179]
	s_mov_b32 m0, s73
	s_nop 0
	global_load_lds_dwordx4 v[218:219], off
	s_waitcnt vmcnt(8)
	s_waitcnt lgkmcnt(0)
	s_barrier
	s_setprio 3
	s_waitcnt lgkmcnt(0)
	v_mfma_f32_16x16x128_f8f6f4 v[158:161], v[18:25], v[180:187], v[158:161]
	v_mfma_f32_16x16x128_f8f6f4 v[154:157], v[26:33], v[180:187], v[154:157]
	v_mfma_f32_16x16x128_f8f6f4 v[150:153], v[18:25], v[194:201], v[150:153]
	v_mfma_f32_16x16x128_f8f6f4 v[142:145], v[26:33], v[194:201], v[142:145]
	v_mfma_f32_16x16x128_f8f6f4 v[134:137], v[18:25], v[202:209], v[134:137]
	v_mfma_f32_16x16x128_f8f6f4 v[126:129], v[26:33], v[202:209], v[126:129]
	v_mfma_f32_16x16x128_f8f6f4 v[118:121], v[18:25], v[210:217], v[118:121]
	v_mfma_f32_16x16x128_f8f6f4 v[110:113], v[26:33], v[210:217], v[110:113]
	s_setprio 0
	s_setprio 3
	v_mfma_f32_16x16x128_f8f6f4 v[146:149], v[2:9], v[180:187], v[146:149]
	v_mfma_f32_16x16x128_f8f6f4 v[138:141], v[10:17], v[180:187], v[138:141]
	v_mfma_f32_16x16x128_f8f6f4 v[130:133], v[2:9], v[194:201], v[130:133]
	v_mfma_f32_16x16x128_f8f6f4 v[122:125], v[10:17], v[194:201], v[122:125]
	v_mfma_f32_16x16x128_f8f6f4 v[114:117], v[2:9], v[202:209], v[114:117]
	v_mfma_f32_16x16x128_f8f6f4 v[106:109], v[10:17], v[202:209], v[106:109]
	v_mfma_f32_16x16x128_f8f6f4 v[102:105], v[2:9], v[210:217], v[102:105]
	v_mfma_f32_16x16x128_f8f6f4 v[98:101], v[10:17], v[210:217], v[98:101]
	s_setprio 0
	s_barrier
	s_mov_b32 m0, s74
	v_lshl_add_u64 v[180:181], s[18:19], 0, v[172:173]
	s_add_u32 s4, s18, 0x20000
	ds_read_b128 v[194:197], v189 offset:16384
	ds_read_b128 v[198:201], v189 offset:17408
	ds_read_b128 v[202:205], v189 offset:18432
	ds_read_b128 v[206:209], v189 offset:19456
	ds_read_b128 v[210:213], v189 offset:20480
	ds_read_b128 v[214:217], v189 offset:21504
	ds_read_b128 v[218:221], v189 offset:22528
	ds_read_b128 v[222:225], v189 offset:23552
	global_load_lds_dwordx4 v[180:181], off
	v_lshl_add_u64 v[182:183], s[18:19], 0, v[168:169]
	s_mov_b32 m0, s75
	s_addc_u32 s5, s19, 0
	global_load_lds_dwordx4 v[182:183], off
	v_lshl_add_u64 v[184:185], s[4:5], 0, v[172:173]
	s_mov_b32 m0, s76
	v_lshl_add_u64 v[186:187], s[22:23], 0, v[170:171]
	global_load_lds_dwordx4 v[184:185], off
	v_lshl_add_u64 v[184:185], s[4:5], 0, v[168:169]
	s_mov_b32 m0, s77
	s_nop 0
	global_load_lds_dwordx4 v[184:185], off
	v_lshl_add_u64 v[184:185], s[22:23], 0, v[174:175]
	s_mov_b32 m0, s30
	s_nop 0
	global_load_lds_dwordx4 v[184:185], off
	s_mov_b32 m0, s31
	s_nop 0
	global_load_lds_dwordx4 v[186:187], off
	s_waitcnt vmcnt(8)
	s_waitcnt lgkmcnt(0)
	s_barrier
	s_setprio 3
	s_waitcnt lgkmcnt(0)
	v_mfma_f32_16x16x128_f8f6f4 v[94:97], v[18:25], v[194:201], v[94:97]
	v_mfma_f32_16x16x128_f8f6f4 v[90:93], v[26:33], v[194:201], v[90:93]
	v_mfma_f32_16x16x128_f8f6f4 v[86:89], v[18:25], v[202:209], v[86:89]
	v_mfma_f32_16x16x128_f8f6f4 v[78:81], v[26:33], v[202:209], v[78:81]
	v_mfma_f32_16x16x128_f8f6f4 v[70:73], v[18:25], v[210:217], v[70:73]
	v_mfma_f32_16x16x128_f8f6f4 v[62:65], v[26:33], v[210:217], v[62:65]
	v_mfma_f32_16x16x128_f8f6f4 v[54:57], v[18:25], v[218:225], v[54:57]
	v_mfma_f32_16x16x128_f8f6f4 v[46:49], v[26:33], v[218:225], v[46:49]
	s_setprio 0
	s_setprio 3
	v_mfma_f32_16x16x128_f8f6f4 v[82:85], v[2:9], v[194:201], v[82:85]
	v_mfma_f32_16x16x128_f8f6f4 v[74:77], v[10:17], v[194:201], v[74:77]
	v_mfma_f32_16x16x128_f8f6f4 v[66:69], v[2:9], v[202:209], v[66:69]
	v_mfma_f32_16x16x128_f8f6f4 v[58:61], v[10:17], v[202:209], v[58:61]
	v_mfma_f32_16x16x128_f8f6f4 v[50:53], v[2:9], v[210:217], v[50:53]
	v_mfma_f32_16x16x128_f8f6f4 v[42:45], v[10:17], v[210:217], v[42:45]
	v_mfma_f32_16x16x128_f8f6f4 v[38:41], v[2:9], v[218:225], v[38:41]
	v_mfma_f32_16x16x128_f8f6f4 v[34:37], v[10:17], v[218:225], v[34:37]
	s_setprio 0
	s_barrier
; #define PG8_STAGE(bufoff, gbase, voff) do { _Pragma("unroll") for (int _i = 0; _i < 2; ++_i) \
;         __builtin_amdgcn_global_load_lds((const unsigned*)((const char*)(gbase) + (voff)[_i]), (PG8_LAS unsigned*)(lds + (bufoff) + ldsw + _i * 8192), 16, 0, 0); } while (0)
; #define PG8_LDA(dst, b, h) do { _Pragma("unroll") for (int m = 0; m < 4; ++m) Frag<F8>::load(dst[m], lds + PG8_SA(b, h) + aoff + m * 2048); } while (0)
; #define PG8_LDB(dst, b, h) do { _Pragma("unroll") for (int n = 0; n < 2; ++n) Frag<F8>::load(dst[n], lds + PG8_SB(b, h) + boff + n * 2048); } while (0)
; #define PG8_MMA(ai, bj, At, Bt) do { __builtin_amdgcn_s_setprio(3); _Pragma("unroll") for (int m = 0; m < 4; ++m) _Pragma("unroll") for (int n = 0; n < 2; ++n) Frag<F8>::mma(acc[ai][bj][m][n], Bt[n], At[m]); \
;         __builtin_amdgcn_s_setprio(0); } while (0)
; #define PG8_WAIT_V(n) asm volatile("s_waitcnt vmcnt(" #n ")" ::: "memory")
; #define PG8_WAIT_L(n) asm volatile("s_waitcnt lgkmcnt(" #n ")" ::: "memory")
; #define PG8_BAR __builtin_amdgcn_s_barrier()
; #define PG8_SCHED __builtin_amdgcn_sched_barrier(0)
; template <class Epi, class Sched, bool ALIGN_EPI = false, bool SP2 = false, bool F8 = false>
; __device__ __forceinline__ void gemm_phase(PG8_LAS unsigned char* lds, const Gemm g, const Sched& S, const Epi& E) {
;     ...
;             PG8_LDB(B0, 1, 0); PG8_LDB(B1, 1, 1); PG8_SCHED; PG8_LDA(At, 1, 0); PG8_STAGE(PG8_SA(0, 1), a2 + hstep, voffA);
;             PG8_WAIT_V(8); PG8_WAIT_L(0); PG8_BAR; PG8_MMA(0, 0, At, B0); PG8_MMA(0, 1, At, B1); PG8_BAR; PG8_SCHED;
;             PG8_LDA(At, 1, 1); PG8_STAGE(PG8_SB(1, 0), b3, voffB); PG8_STAGE(PG8_SB(1, 1), b3 + hstep, voffB); PG8_STAGE(PG8_SA(1, 0), a3, voffA);
;             PG8_WAIT_V(8); PG8_WAIT_L(0); PG8_BAR; PG8_MMA(1, 0, At, B0); PG8_MMA(1, 1, At, B1); PG8_BAR; PG8_SCHED;
	ds_read_b128 v[2:5], v191
	ds_read_b128 v[6:9], v191 offset:1024
	ds_read_b128 v[10:13], v191 offset:2048
	ds_read_b128 v[14:17], v191 offset:3072
	ds_read_b128 v[18:21], v192
	ds_read_b128 v[22:25], v192 offset:1024
	ds_read_b128 v[26:29], v192 offset:2048
	ds_read_b128 v[30:33], v192 offset:3072
	s_add_u32 s4, s22, 0x20000
	s_addc_u32 s5, s23, 0
	s_mov_b32 m0, s38
	v_lshl_add_u64 v[226:227], s[4:5], 0, v[174:175]
	ds_read_b128 v[194:197], v189 offset:32768
	ds_read_b128 v[198:201], v189 offset:33792
	ds_read_b128 v[202:205], v189 offset:34816
	ds_read_b128 v[206:209], v189 offset:35840
	ds_read_b128 v[210:213], v189 offset:36864
	ds_read_b128 v[214:217], v189 offset:37888
	ds_read_b128 v[218:221], v189 offset:38912
	ds_read_b128 v[222:225], v189 offset:39936
	global_load_lds_dwordx4 v[226:227], off
	v_lshl_add_u64 v[226:227], s[4:5], 0, v[170:171]
	s_mov_b32 m0, s39
	s_nop 0
	global_load_lds_dwordx4 v[226:227], off
	s_waitcnt vmcnt(8)
	s_waitcnt lgkmcnt(0)
	s_barrier
	s_setprio 3
	s_waitcnt lgkmcnt(0)
	v_mfma_f32_16x16x128_f8f6f4 v[158:161], v[2:9], v[194:201], v[158:161]
	v_mfma_f32_16x16x128_f8f6f4 v[154:157], v[10:17], v[194:201], v[154:157]
	v_mfma_f32_16x16x128_f8f6f4 v[150:153], v[2:9], v[202:209], v[150:153]
	v_mfma_f32_16x16x128_f8f6f4 v[142:145], v[10:17], v[202:209], v[142:145]
	v_mfma_f32_16x16x128_f8f6f4 v[134:137], v[2:9], v[210:217], v[134:137]
	v_mfma_f32_16x16x128_f8f6f4 v[126:129], v[10:17], v[210:217], v[126:129]
	v_mfma_f32_16x16x128_f8f6f4 v[118:121], v[2:9], v[218:225], v[118:121]
	v_mfma_f32_16x16x128_f8f6f4 v[110:113], v[10:17], v[218:225], v[110:113]
	s_setprio 0
	s_setprio 3
	v_mfma_f32_16x16x128_f8f6f4 v[146:149], v[18:25], v[194:201], v[146:149]
	v_mfma_f32_16x16x128_f8f6f4 v[138:141], v[26:33], v[194:201], v[138:141]
	v_mfma_f32_16x16x128_f8f6f4 v[130:133], v[18:25], v[202:209], v[130:133]
	v_mfma_f32_16x16x128_f8f6f4 v[122:125], v[26:33], v[202:209], v[122:125]
	v_mfma_f32_16x16x128_f8f6f4 v[114:117], v[18:25], v[210:217], v[114:117]
	v_mfma_f32_16x16x128_f8f6f4 v[106:109], v[26:33], v[210:217], v[106:109]
	v_mfma_f32_16x16x128_f8f6f4 v[102:105], v[18:25], v[218:225], v[102:105]
	v_mfma_f32_16x16x128_f8f6f4 v[98:101], v[26:33], v[218:225], v[98:101]
	s_setprio 0
	s_barrier
	s_mov_b32 m0, s78
	v_lshl_add_u64 v[180:181], v[180:181], 0, s[14:15]
	s_add_u32 s4, s18, 0x20080
	ds_read_b128 v[194:197], v189 offset:49152
	ds_read_b128 v[198:201], v189 offset:50176
	ds_read_b128 v[202:205], v189 offset:51200
	ds_read_b128 v[206:209], v189 offset:52224
	ds_read_b128 v[210:213], v189 offset:53248
	ds_read_b128 v[214:217], v189 offset:54272
	ds_read_b128 v[218:221], v189 offset:55296
	ds_read_b128 v[222:225], v189 offset:56320
	global_load_lds_dwordx4 v[180:181], off
	v_lshl_add_u64 v[180:181], v[182:183], 0, s[14:15]
	s_mov_b32 m0, s79
	s_addc_u32 s5, s19, 0
	global_load_lds_dwordx4 v[180:181], off
	v_lshl_add_u64 v[180:181], s[4:5], 0, v[172:173]
	s_mov_b32 m0, s80
	s_nop 0
	global_load_lds_dwordx4 v[180:181], off
	v_lshl_add_u64 v[180:181], s[4:5], 0, v[168:169]
	s_mov_b32 m0, s81
	s_nop 0
	global_load_lds_dwordx4 v[180:181], off
	v_lshl_add_u64 v[180:181], v[184:185], 0, s[14:15]
	s_mov_b32 m0, s43
	s_nop 0
	global_load_lds_dwordx4 v[180:181], off
	v_lshl_add_u64 v[180:181], v[186:187], 0, s[14:15]
	s_mov_b32 m0, s44
	s_nop 0
	global_load_lds_dwordx4 v[180:181], off
	s_waitcnt vmcnt(8)
	s_waitcnt lgkmcnt(0)
	s_barrier
	s_setprio 3
	s_waitcnt lgkmcnt(0)
	v_mfma_f32_16x16x128_f8f6f4 v[94:97], v[2:9], v[194:201], v[94:97]
	v_mfma_f32_16x16x128_f8f6f4 v[90:93], v[10:17], v[194:201], v[90:93]
	v_mfma_f32_16x16x128_f8f6f4 v[86:89], v[2:9], v[202:209], v[86:89]
	v_mfma_f32_16x16x128_f8f6f4 v[78:81], v[10:17], v[202:209], v[78:81]
	v_mfma_f32_16x16x128_f8f6f4 v[70:73], v[2:9], v[210:217], v[70:73]
	v_mfma_f32_16x16x128_f8f6f4 v[62:65], v[10:17], v[210:217], v[62:65]
	v_mfma_f32_16x16x128_f8f6f4 v[54:57], v[2:9], v[218:225], v[54:57]
	v_mfma_f32_16x16x128_f8f6f4 v[46:49], v[10:17], v[218:225], v[46:49]
	s_setprio 0
	s_setprio 3
	v_mfma_f32_16x16x128_f8f6f4 v[82:85], v[18:25], v[194:201], v[82:85]
	v_mfma_f32_16x16x128_f8f6f4 v[74:77], v[26:33], v[194:201], v[74:77]
	v_mfma_f32_16x16x128_f8f6f4 v[66:69], v[18:25], v[202:209], v[66:69]
	v_mfma_f32_16x16x128_f8f6f4 v[58:61], v[26:33], v[202:209], v[58:61]
	v_mfma_f32_16x16x128_f8f6f4 v[50:53], v[18:25], v[210:217], v[50:53]
	v_mfma_f32_16x16x128_f8f6f4 v[42:45], v[26:33], v[210:217], v[42:45]
	v_mfma_f32_16x16x128_f8f6f4 v[38:41], v[18:25], v[218:225], v[38:41]
	v_mfma_f32_16x16x128_f8f6f4 v[34:37], v[26:33], v[218:225], v[34:37]
	s_setprio 0
	s_barrier
	s_add_i32 s71, s71, 2
	s_add_u32 s16, s16, 0x100
	s_addc_u32 s17, s17, 0
	s_cmp_gt_u32 s71, 5
	s_cbranch_scc0 .LBB0_162
	s_cmpk_lt_u32 s25, 0x100
	s_cbranch_scc0 .LBB0_165
	s_barrier

; #define PG8_STAGE(bufoff, gbase, voff) do { _Pragma("unroll") for (int _i = 0; _i < 2; ++_i) \
;         __builtin_amdgcn_global_load_lds((const unsigned*)((const char*)(gbase) + (voff)[_i]), (PG8_LAS unsigned*)(lds + (bufoff) + ldsw + _i * 8192), 16, 0, 0); } while (0)
; #define PG8_LDA(dst, b, h) do { _Pragma("unroll") for (int m = 0; m < 4; ++m) Frag<F8>::load(dst[m], lds + PG8_SA(b, h) + aoff + m * 2048); } while (0)
; #define PG8_LDB(dst, b, h) do { _Pragma("unroll") for (int n = 0; n < 2; ++n) Frag<F8>::load(dst[n], lds + PG8_SB(b, h) + boff + n * 2048); } while (0)
; #define PG8_MMA(ai, bj, At, Bt) do { __builtin_amdgcn_s_setprio(3); _Pragma("unroll") for (int m = 0; m < 4; ++m) _Pragma("unroll") for (int n = 0; n < 2; ++n) Frag<F8>::mma(acc[ai][bj][m][n], Bt[n], At[m]); \
;         __builtin_amdgcn_s_setprio(0); } while (0)
; #define PG8_WAIT_V(n) asm volatile("s_waitcnt vmcnt(" #n ")" ::: "memory")
; #define PG8_WAIT_L(n) asm volatile("s_waitcnt lgkmcnt(" #n ")" ::: "memory")
; #define PG8_BAR __builtin_amdgcn_s_barrier()
; #define PG8_SCHED __builtin_amdgcn_sched_barrier(0)
; template <class Epi, class Sched, bool ALIGN_EPI = false, bool SP2 = false, bool F8 = false>
; __device__ __forceinline__ void gemm_phase(PG8_LAS unsigned char* lds, const Gemm g, const Sched& S, const Epi& E) {
;     ...
;             const bool last = (t == nt - 2);
;             const char* a1 = cA + (size_t)(t + 1) * kstep;
;             const char* a2 = last ? nA : cA + (size_t)(t + 2) * kstep; const char* b2 = last ? nB : cB + (size_t)(t + 2) * kstep;
;             const char* a3 = a2 + kstep; const char* b3 = b2 + kstep;
;             if (last && has_next) S.a_ready(nxt);
;             if constexpr (SP2) {
;             PG8_LDB(B0, 0, 0); PG8_LDB(B1, 0, 1); PG8_SCHED; PG8_LDA(At, 0, 0); PG8_STAGE(PG8_SA(1, 1), a1 + hstep, voffA);
;             PG8_WAIT_V(8); PG8_WAIT_L(0); PG8_BAR; PG8_MMA(0, 0, At, B0); PG8_MMA(0, 1, At, B1); PG8_BAR; PG8_SCHED;
;             PG8_LDA(At, 0, 1); PG8_STAGE(PG8_SB(0, 0), b2, voffB); PG8_STAGE(PG8_SB(0, 1), b2 + hstep, voffB); PG8_STAGE(PG8_SA(0, 0), a2, voffA);
;             PG8_WAIT_V(8); PG8_WAIT_L(0); PG8_BAR; PG8_MMA(1, 0, At, B0); PG8_MMA(1, 1, At, B1); PG8_BAR; PG8_SCHED;
.LBB0_801:
	s_ashr_i32 s25, s24, 31
	s_lshl_b64 s[4:5], s[24:25], 18
	s_add_u32 s36, s49, s4
	s_addc_u32 s37, s50, s5
	s_and_b64 s[4:5], s[8:9], exec
	s_cselect_b32 s25, s37, s43
	s_cselect_b32 s83, s36, s42
	s_ashr_i32 s31, s30, 31
	s_lshl_b64 s[4:5], s[30:31], 18
	s_add_u32 s38, s51, s4
	s_addc_u32 s39, s52, s5
	s_and_b64 s[4:5], s[8:9], exec
	s_cselect_b32 s31, s39, s45
	s_cselect_b32 s84, s38, s44
	s_add_u32 s42, s42, 0x20080
	s_addc_u32 s43, s43, 0
	s_add_u32 s85, s44, 0x100
	s_addc_u32 s86, s45, 0
	s_mov_b32 s87, -2
	ds_read_b128 v[18:21], v194
	ds_read_b128 v[22:25], v194 offset:1024
	ds_read_b128 v[26:29], v194 offset:2048
	ds_read_b128 v[30:33], v194 offset:3072
	ds_read_b128 v[2:5], v195
	ds_read_b128 v[6:9], v195 offset:1024
	ds_read_b128 v[10:13], v195 offset:2048
	ds_read_b128 v[14:17], v195 offset:3072
	s_add_u32 s0, s42, 0xfffe0080
	s_addc_u32 s1, s43, -1
	s_cmp_eq_u32 s87, 4
	s_cselect_b32 s47, s25, s1
	s_cselect_b32 s46, s83, s0
	s_cselect_b32 s45, s31, s86
	s_cselect_b32 s44, s84, s85
	v_lshl_add_u64 v[224:225], s[42:43], 0, v[174:175]
	s_add_i32 m0, s41, 0xc000
	ds_read_b128 v[182:185], v196
	ds_read_b128 v[186:189], v196 offset:1024
	ds_read_b128 v[200:203], v196 offset:2048
	ds_read_b128 v[204:207], v196 offset:3072
	ds_read_b128 v[208:211], v196 offset:4096
	ds_read_b128 v[212:215], v196 offset:5120
	ds_read_b128 v[216:219], v196 offset:6144
	ds_read_b128 v[220:223], v196 offset:7168
	global_load_lds_dwordx4 v[224:225], off
	v_lshl_add_u64 v[224:225], s[42:43], 0, v[176:177]
	s_add_i32 m0, s41, 0xe000
	s_nop 0
	global_load_lds_dwordx4 v[224:225], off
	s_waitcnt vmcnt(8)
	s_waitcnt lgkmcnt(0)
	s_barrier
	s_setprio 3
	s_waitcnt lgkmcnt(0)
	v_mfma_f32_16x16x128_f8f6f4 v[158:161], v[18:25], v[182:189], 0
	v_mfma_f32_16x16x128_f8f6f4 v[154:157], v[26:33], v[182:189], 0
	v_mfma_f32_16x16x128_f8f6f4 v[150:153], v[18:25], v[200:207], 0
	v_mfma_f32_16x16x128_f8f6f4 v[142:145], v[26:33], v[200:207], 0
	v_mfma_f32_16x16x128_f8f6f4 v[130:133], v[18:25], v[208:215], 0
	v_mfma_f32_16x16x128_f8f6f4 v[122:125], v[26:33], v[208:215], 0
	v_mfma_f32_16x16x128_f8f6f4 v[118:121], v[18:25], v[216:223], 0
	v_mfma_f32_16x16x128_f8f6f4 v[110:113], v[26:33], v[216:223], 0
	s_setprio 0
	s_setprio 3
	v_mfma_f32_16x16x128_f8f6f4 v[146:149], v[2:9], v[182:189], 0
	v_mfma_f32_16x16x128_f8f6f4 v[138:141], v[10:17], v[182:189], 0
	v_mfma_f32_16x16x128_f8f6f4 v[134:137], v[2:9], v[200:207], 0
	v_mfma_f32_16x16x128_f8f6f4 v[126:129], v[10:17], v[200:207], 0
	v_mfma_f32_16x16x128_f8f6f4 v[114:117], v[2:9], v[208:215], 0
	v_mfma_f32_16x16x128_f8f6f4 v[106:109], v[10:17], v[208:215], 0
	v_mfma_f32_16x16x128_f8f6f4 v[102:105], v[2:9], v[216:223], 0
	v_mfma_f32_16x16x128_f8f6f4 v[98:101], v[10:17], v[216:223], 0
	s_setprio 0
	s_barrier
	s_add_i32 s0, s79, s48
	v_lshl_add_u64 v[182:183], s[44:45], 0, v[170:171]
	s_mov_b32 m0, s0
	ds_read_b128 v[200:203], v196 offset:16384
	ds_read_b128 v[204:207], v196 offset:17408
	ds_read_b128 v[208:211], v196 offset:18432
	ds_read_b128 v[212:215], v196 offset:19456
	ds_read_b128 v[216:219], v196 offset:20480
	ds_read_b128 v[220:223], v196 offset:21504
	ds_read_b128 v[224:227], v196 offset:22528
	ds_read_b128 v[228:231], v196 offset:23552
	global_load_lds_dwordx4 v[182:183], off
	s_add_i32 m0, s0, 0x2000
	s_add_u32 s4, s44, 0x20000
	v_lshl_add_u64 v[184:185], s[44:45], 0, v[166:167]
	s_addc_u32 s5, s45, 0
	s_add_i32 s0, s80, s48
	global_load_lds_dwordx4 v[184:185], off
	v_lshl_add_u64 v[186:187], s[4:5], 0, v[170:171]
	s_mov_b32 m0, s0
	v_lshl_add_u64 v[188:189], s[46:47], 0, v[168:169]
	global_load_lds_dwordx4 v[186:187], off
	v_lshl_add_u64 v[186:187], s[4:5], 0, v[166:167]
	s_add_i32 m0, s0, 0x2000
	s_nop 0
	global_load_lds_dwordx4 v[186:187], off
	v_lshl_add_u64 v[186:187], s[46:47], 0, v[172:173]
	s_mov_b32 m0, s41
	s_nop 0
	global_load_lds_dwordx4 v[186:187], off
	s_mov_b32 m0, s71
	s_nop 0
	global_load_lds_dwordx4 v[188:189], off
	s_waitcnt vmcnt(8)
	s_waitcnt lgkmcnt(0)
	s_barrier
	s_setprio 3
	s_waitcnt lgkmcnt(0)
	v_mfma_f32_16x16x128_f8f6f4 v[94:97], v[18:25], v[200:207], 0
	v_mfma_f32_16x16x128_f8f6f4 v[90:93], v[26:33], v[200:207], 0
	v_mfma_f32_16x16x128_f8f6f4 v[86:89], v[18:25], v[208:215], 0
	v_mfma_f32_16x16x128_f8f6f4 v[82:85], v[26:33], v[208:215], 0
	v_mfma_f32_16x16x128_f8f6f4 v[70:73], v[18:25], v[216:223], 0
	v_mfma_f32_16x16x128_f8f6f4 v[66:69], v[26:33], v[216:223], 0
	v_mfma_f32_16x16x128_f8f6f4 v[54:57], v[18:25], v[224:231], 0
	v_mfma_f32_16x16x128_f8f6f4 v[50:53], v[26:33], v[224:231], 0
	s_setprio 0
	s_setprio 3
	v_mfma_f32_16x16x128_f8f6f4 v[78:81], v[2:9], v[200:207], 0
	v_mfma_f32_16x16x128_f8f6f4 v[74:77], v[10:17], v[200:207], 0
	v_mfma_f32_16x16x128_f8f6f4 v[62:65], v[2:9], v[208:215], 0
	v_mfma_f32_16x16x128_f8f6f4 v[58:61], v[10:17], v[208:215], 0
	v_mfma_f32_16x16x128_f8f6f4 v[46:49], v[2:9], v[216:223], 0
	v_mfma_f32_16x16x128_f8f6f4 v[42:45], v[10:17], v[216:223], 0
	v_mfma_f32_16x16x128_f8f6f4 v[38:41], v[2:9], v[224:231], 0
	v_mfma_f32_16x16x128_f8f6f4 v[34:37], v[10:17], v[224:231], 0
	s_setprio 0
	s_barrier
	s_add_i32 s0, 0, 0x18000
	s_add_i32 s1, 0, 0x1c000
	v_add_u32_e32 v14, s0, v190
	v_add_u32_e32 v30, s1, v190
	ds_read_b128 v[2:5], v14
	ds_read_b128 v[6:9], v14 offset:1024
	ds_read_b128 v[10:13], v14 offset:2048
	ds_read_b128 v[14:17], v14 offset:3072
	ds_read_b128 v[18:21], v30
	ds_read_b128 v[22:25], v30 offset:1024
	ds_read_b128 v[26:29], v30 offset:2048
	ds_read_b128 v[30:33], v30 offset:3072
	s_add_u32 s4, s46, 0x20000
	s_addc_u32 s5, s47, 0
	s_mov_b32 m0, s72
	v_lshl_add_u64 v[232:233], s[4:5], 0, v[172:173]
	ds_read_b128 v[200:203], v196 offset:32768
	ds_read_b128 v[204:207], v196 offset:33792
	ds_read_b128 v[208:211], v196 offset:34816
	ds_read_b128 v[212:215], v196 offset:35840
	ds_read_b128 v[216:219], v196 offset:36864
	ds_read_b128 v[220:223], v196 offset:37888
	ds_read_b128 v[224:227], v196 offset:38912
	ds_read_b128 v[228:231], v196 offset:39936
	global_load_lds_dwordx4 v[232:233], off
	v_lshl_add_u64 v[232:233], s[4:5], 0, v[168:169]
	s_mov_b32 m0, s73
	s_nop 0
	global_load_lds_dwordx4 v[232:233], off
	s_waitcnt vmcnt(8)
	s_waitcnt lgkmcnt(0)
	s_barrier
; #define PG8_STAGE(bufoff, gbase, voff) do { _Pragma("unroll") for (int _i = 0; _i < 2; ++_i) \
;         __builtin_amdgcn_global_load_lds((const unsigned*)((const char*)(gbase) + (voff)[_i]), (PG8_LAS unsigned*)(lds + (bufoff) + ldsw + _i * 8192), 16, 0, 0); } while (0)
; #define PG8_LDA(dst, b, h) do { _Pragma("unroll") for (int m = 0; m < 4; ++m) Frag<F8>::load(dst[m], lds + PG8_SA(b, h) + aoff + m * 2048); } while (0)
; #define PG8_LDB(dst, b, h) do { _Pragma("unroll") for (int n = 0; n < 2; ++n) Frag<F8>::load(dst[n], lds + PG8_SB(b, h) + boff + n * 2048); } while (0)
; #define PG8_MMA(ai, bj, At, Bt) do { __builtin_amdgcn_s_setprio(3); _Pragma("unroll") for (int m = 0; m < 4; ++m) _Pragma("unroll") for (int n = 0; n < 2; ++n) Frag<F8>::mma(acc[ai][bj][m][n], Bt[n], At[m]); \
;         __builtin_amdgcn_s_setprio(0); } while (0)
; #define PG8_WAIT_V(n) asm volatile("s_waitcnt vmcnt(" #n ")" ::: "memory")
; #define PG8_WAIT_L(n) asm volatile("s_waitcnt lgkmcnt(" #n ")" ::: "memory")
; #define PG8_BAR __builtin_amdgcn_s_barrier()
; #define PG8_SCHED __builtin_amdgcn_sched_barrier(0)
; template <class Epi, class Sched, bool ALIGN_EPI = false, bool SP2 = false, bool F8 = false>
; __device__ __forceinline__ void gemm_phase(PG8_LAS unsigned char* lds, const Gemm g, const Sched& S, const Epi& E) {
;     ...
;             PG8_LDB(B0, 0, 0); PG8_LDB(B1, 0, 1); PG8_SCHED; PG8_LDA(At, 0, 0); PG8_STAGE(PG8_SA(1, 1), a1 + hstep, voffA);
;             PG8_WAIT_V(8); PG8_WAIT_L(0); PG8_BAR; PG8_MMA(0, 0, At, B0); PG8_MMA(0, 1, At, B1); PG8_BAR; PG8_SCHED;
;             PG8_LDA(At, 0, 1); PG8_STAGE(PG8_SB(0, 0), b2, voffB); PG8_STAGE(PG8_SB(0, 1), b2 + hstep, voffB); PG8_STAGE(PG8_SA(0, 0), a2, voffA);
;             PG8_WAIT_V(8); PG8_WAIT_L(0); PG8_BAR; PG8_MMA(1, 0, At, B0); PG8_MMA(1, 1, At, B1); PG8_BAR; PG8_SCHED;
;             PG8_LDB(B0, 1, 0); PG8_LDB(B1, 1, 1); PG8_SCHED; PG8_LDA(At, 1, 0); PG8_STAGE(PG8_SA(0, 1), a2 + hstep, voffA);
;             PG8_WAIT_V(8); PG8_WAIT_L(0); PG8_BAR; PG8_MMA(0, 0, At, B0); PG8_MMA(0, 1, At, B1); PG8_BAR; PG8_SCHED;
;             PG8_LDA(At, 1, 1); PG8_STAGE(PG8_SB(1, 0), b3, voffB); PG8_STAGE(PG8_SB(1, 1), b3 + hstep, voffB); PG8_STAGE(PG8_SA(1, 0), a3, voffA);
;             PG8_WAIT_V(8); PG8_WAIT_L(0); PG8_BAR; PG8_MMA(1, 0, At, B0); PG8_MMA(1, 1, At, B1); PG8_BAR; PG8_SCHED;
	s_setprio 3
	s_waitcnt lgkmcnt(0)
	v_mfma_f32_16x16x128_f8f6f4 v[158:161], v[2:9], v[200:207], v[158:161]
	v_mfma_f32_16x16x128_f8f6f4 v[154:157], v[10:17], v[200:207], v[154:157]
	v_mfma_f32_16x16x128_f8f6f4 v[150:153], v[2:9], v[208:215], v[150:153]
	v_mfma_f32_16x16x128_f8f6f4 v[142:145], v[10:17], v[208:215], v[142:145]
	v_mfma_f32_16x16x128_f8f6f4 v[130:133], v[2:9], v[216:223], v[130:133]
	v_mfma_f32_16x16x128_f8f6f4 v[122:125], v[10:17], v[216:223], v[122:125]
	v_mfma_f32_16x16x128_f8f6f4 v[118:121], v[2:9], v[224:231], v[118:121]
	v_mfma_f32_16x16x128_f8f6f4 v[110:113], v[10:17], v[224:231], v[110:113]
	s_setprio 0
	s_setprio 3
	v_mfma_f32_16x16x128_f8f6f4 v[146:149], v[18:25], v[200:207], v[146:149]
	v_mfma_f32_16x16x128_f8f6f4 v[138:141], v[26:33], v[200:207], v[138:141]
	v_mfma_f32_16x16x128_f8f6f4 v[134:137], v[18:25], v[208:215], v[134:137]
	v_mfma_f32_16x16x128_f8f6f4 v[126:129], v[26:33], v[208:215], v[126:129]
	v_mfma_f32_16x16x128_f8f6f4 v[114:117], v[18:25], v[216:223], v[114:117]
	v_mfma_f32_16x16x128_f8f6f4 v[106:109], v[26:33], v[216:223], v[106:109]
	v_mfma_f32_16x16x128_f8f6f4 v[102:105], v[18:25], v[224:231], v[102:105]
	v_mfma_f32_16x16x128_f8f6f4 v[98:101], v[26:33], v[224:231], v[98:101]
	s_setprio 0
	s_barrier
	s_add_i32 s0, s0, s48
	v_lshl_add_u64 v[182:183], v[182:183], 0, s[18:19]
	s_mov_b32 m0, s0
	ds_read_b128 v[200:203], v196 offset:49152
	ds_read_b128 v[204:207], v196 offset:50176
	ds_read_b128 v[208:211], v196 offset:51200
	ds_read_b128 v[212:215], v196 offset:52224
	ds_read_b128 v[216:219], v196 offset:53248
	ds_read_b128 v[220:223], v196 offset:54272
	ds_read_b128 v[224:227], v196 offset:55296
	ds_read_b128 v[228:231], v196 offset:56320
	global_load_lds_dwordx4 v[182:183], off
	s_add_i32 m0, s0, 0x2000
	s_add_u32 s4, s44, 0x20080
	v_lshl_add_u64 v[182:183], v[184:185], 0, s[18:19]
	s_addc_u32 s5, s45, 0
	s_add_i32 s0, s1, s48
	global_load_lds_dwordx4 v[182:183], off
	v_lshl_add_u64 v[182:183], s[4:5], 0, v[170:171]
	s_mov_b32 m0, s0
	s_nop 0
	global_load_lds_dwordx4 v[182:183], off
	v_lshl_add_u64 v[182:183], s[4:5], 0, v[166:167]
	s_add_i32 m0, s0, 0x2000
	s_nop 0
	global_load_lds_dwordx4 v[182:183], off
	v_lshl_add_u64 v[182:183], v[186:187], 0, s[18:19]
	s_mov_b32 m0, s74
	s_nop 0
	global_load_lds_dwordx4 v[182:183], off
	v_lshl_add_u64 v[182:183], v[188:189], 0, s[18:19]
	s_mov_b32 m0, s75
	s_nop 0
	global_load_lds_dwordx4 v[182:183], off
	s_waitcnt vmcnt(8)
	s_waitcnt lgkmcnt(0)
	s_barrier
	s_setprio 3
	s_waitcnt lgkmcnt(0)
	v_mfma_f32_16x16x128_f8f6f4 v[94:97], v[2:9], v[200:207], v[94:97]
	v_mfma_f32_16x16x128_f8f6f4 v[90:93], v[10:17], v[200:207], v[90:93]
	v_mfma_f32_16x16x128_f8f6f4 v[86:89], v[2:9], v[208:215], v[86:89]
	v_mfma_f32_16x16x128_f8f6f4 v[82:85], v[10:17], v[208:215], v[82:85]
	v_mfma_f32_16x16x128_f8f6f4 v[70:73], v[2:9], v[216:223], v[70:73]
	v_mfma_f32_16x16x128_f8f6f4 v[66:69], v[10:17], v[216:223], v[66:69]
	v_mfma_f32_16x16x128_f8f6f4 v[54:57], v[2:9], v[224:231], v[54:57]
	v_mfma_f32_16x16x128_f8f6f4 v[50:53], v[10:17], v[224:231], v[50:53]
	s_setprio 0
	s_setprio 3
	v_mfma_f32_16x16x128_f8f6f4 v[78:81], v[18:25], v[200:207], v[78:81]
	v_mfma_f32_16x16x128_f8f6f4 v[74:77], v[26:33], v[200:207], v[74:77]
	v_mfma_f32_16x16x128_f8f6f4 v[62:65], v[18:25], v[208:215], v[62:65]
	v_mfma_f32_16x16x128_f8f6f4 v[58:61], v[26:33], v[208:215], v[58:61]
	v_mfma_f32_16x16x128_f8f6f4 v[46:49], v[18:25], v[216:223], v[46:49]
	v_mfma_f32_16x16x128_f8f6f4 v[42:45], v[26:33], v[216:223], v[42:45]
	v_mfma_f32_16x16x128_f8f6f4 v[38:41], v[18:25], v[224:231], v[38:41]
	v_mfma_f32_16x16x128_f8f6f4 v[34:37], v[26:33], v[224:231], v[34:37]
	s_setprio 0
	s_barrier
	s_add_i32 s87, s87, 2
	s_add_u32 s42, s42, 0x100
	s_addc_u32 s43, s43, 0
	s_add_u32 s85, s85, 0x100
	s_addc_u32 s86, s86, 0
	s_cmp_gt_u32 s87, 5
	s_cbranch_scc1 .Lpeel_exit_2
.LBB0_802:
	ds_read_b128 v[18:21], v194
	ds_read_b128 v[22:25], v194 offset:1024
	ds_read_b128 v[26:29], v194 offset:2048
	ds_read_b128 v[30:33], v194 offset:3072
	ds_read_b128 v[2:5], v195
	ds_read_b128 v[6:9], v195 offset:1024
	ds_read_b128 v[10:13], v195 offset:2048
	ds_read_b128 v[14:17], v195 offset:3072
	s_add_u32 s0, s42, 0xfffe0080
	s_addc_u32 s1, s43, -1
	s_cmp_eq_u32 s87, 4
	s_cselect_b32 s47, s25, s1
	s_cselect_b32 s46, s83, s0
	s_cselect_b32 s45, s31, s86
	s_cselect_b32 s44, s84, s85
	v_lshl_add_u64 v[224:225], s[42:43], 0, v[174:175]
	s_add_i32 m0, s41, 0xc000
	ds_read_b128 v[182:185], v196
	ds_read_b128 v[186:189], v196 offset:1024
	ds_read_b128 v[200:203], v196 offset:2048
	ds_read_b128 v[204:207], v196 offset:3072
	ds_read_b128 v[208:211], v196 offset:4096
	ds_read_b128 v[212:215], v196 offset:5120
	ds_read_b128 v[216:219], v196 offset:6144
	ds_read_b128 v[220:223], v196 offset:7168
	global_load_lds_dwordx4 v[224:225], off
	v_lshl_add_u64 v[224:225], s[42:43], 0, v[176:177]
	s_add_i32 m0, s41, 0xe000
	s_nop 0
	global_load_lds_dwordx4 v[224:225], off
	s_waitcnt vmcnt(8)
	s_waitcnt lgkmcnt(0)
	s_barrier
	s_setprio 3
	s_waitcnt lgkmcnt(0)
	v_mfma_f32_16x16x128_f8f6f4 v[158:161], v[18:25], v[182:189], v[158:161]
	v_mfma_f32_16x16x128_f8f6f4 v[154:157], v[26:33], v[182:189], v[154:157]
	v_mfma_f32_16x16x128_f8f6f4 v[150:153], v[18:25], v[200:207], v[150:153]
	v_mfma_f32_16x16x128_f8f6f4 v[142:145], v[26:33], v[200:207], v[142:145]
	v_mfma_f32_16x16x128_f8f6f4 v[130:133], v[18:25], v[208:215], v[130:133]
	v_mfma_f32_16x16x128_f8f6f4 v[122:125], v[26:33], v[208:215], v[122:125]
	v_mfma_f32_16x16x128_f8f6f4 v[118:121], v[18:25], v[216:223], v[118:121]
	v_mfma_f32_16x16x128_f8f6f4 v[110:113], v[26:33], v[216:223], v[110:113]
	s_setprio 0
	s_setprio 3
	v_mfma_f32_16x16x128_f8f6f4 v[146:149], v[2:9], v[182:189], v[146:149]
	v_mfma_f32_16x16x128_f8f6f4 v[138:141], v[10:17], v[182:189], v[138:141]
	v_mfma_f32_16x16x128_f8f6f4 v[134:137], v[2:9], v[200:207], v[134:137]
	v_mfma_f32_16x16x128_f8f6f4 v[126:129], v[10:17], v[200:207], v[126:129]
	v_mfma_f32_16x16x128_f8f6f4 v[114:117], v[2:9], v[208:215], v[114:117]
	v_mfma_f32_16x16x128_f8f6f4 v[106:109], v[10:17], v[208:215], v[106:109]
	v_mfma_f32_16x16x128_f8f6f4 v[102:105], v[2:9], v[216:223], v[102:105]
	v_mfma_f32_16x16x128_f8f6f4 v[98:101], v[10:17], v[216:223], v[98:101]
	s_setprio 0
	s_barrier
; #define PG8_STAGE(bufoff, gbase, voff) do { _Pragma("unroll") for (int _i = 0; _i < 2; ++_i) \
;         __builtin_amdgcn_global_load_lds((const unsigned*)((const char*)(gbase) + (voff)[_i]), (PG8_LAS unsigned*)(lds + (bufoff) + ldsw + _i * 8192), 16, 0, 0); } while (0)
; #define PG8_LDA(dst, b, h) do { _Pragma("unroll") for (int m = 0; m < 4; ++m) Frag<F8>::load(dst[m], lds + PG8_SA(b, h) + aoff + m * 2048); } while (0)
; #define PG8_LDB(dst, b, h) do { _Pragma("unroll") for (int n = 0; n < 2; ++n) Frag<F8>::load(dst[n], lds + PG8_SB(b, h) + boff + n * 2048); } while (0)
; #define PG8_MMA(ai, bj, At, Bt) do { __builtin_amdgcn_s_setprio(3); _Pragma("unroll") for (int m = 0; m < 4; ++m) _Pragma("unroll") for (int n = 0; n < 2; ++n) Frag<F8>::mma(acc[ai][bj][m][n], Bt[n], At[m]); \
;         __builtin_amdgcn_s_setprio(0); } while (0)
; #define PG8_WAIT_V(n) asm volatile("s_waitcnt vmcnt(" #n ")" ::: "memory")
; #define PG8_WAIT_L(n) asm volatile("s_waitcnt lgkmcnt(" #n ")" ::: "memory")
; #define PG8_BAR __builtin_amdgcn_s_barrier()
; #define PG8_SCHED __builtin_amdgcn_sched_barrier(0)
; template <class Epi, class Sched, bool ALIGN_EPI = false, bool SP2 = false, bool F8 = false>
; __device__ __forceinline__ void gemm_phase(PG8_LAS unsigned char* lds, const Gemm g, const Sched& S, const Epi& E) {
;     ...
;             PG8_LDA(At, 0, 1); PG8_STAGE(PG8_SB(0, 0), b2, voffB); PG8_STAGE(PG8_SB(0, 1), b2 + hstep, voffB); PG8_STAGE(PG8_SA(0, 0), a2, voffA);
;             PG8_WAIT_V(8); PG8_WAIT_L(0); PG8_BAR; PG8_MMA(1, 0, At, B0); PG8_MMA(1, 1, At, B1); PG8_BAR; PG8_SCHED;
;             PG8_LDB(B0, 1, 0); PG8_LDB(B1, 1, 1); PG8_SCHED; PG8_LDA(At, 1, 0); PG8_STAGE(PG8_SA(0, 1), a2 + hstep, voffA);
;             PG8_WAIT_V(8); PG8_WAIT_L(0); PG8_BAR; PG8_MMA(0, 0, At, B0); PG8_MMA(0, 1, At, B1); PG8_BAR; PG8_SCHED;
;             PG8_LDA(At, 1, 1); PG8_STAGE(PG8_SB(1, 0), b3, voffB); PG8_STAGE(PG8_SB(1, 1), b3 + hstep, voffB); PG8_STAGE(PG8_SA(1, 0), a3, voffA);
	s_add_i32 s0, s79, s48
	v_lshl_add_u64 v[182:183], s[44:45], 0, v[170:171]
	s_mov_b32 m0, s0
	ds_read_b128 v[200:203], v196 offset:16384
	ds_read_b128 v[204:207], v196 offset:17408
	ds_read_b128 v[208:211], v196 offset:18432
	ds_read_b128 v[212:215], v196 offset:19456
	ds_read_b128 v[216:219], v196 offset:20480
	ds_read_b128 v[220:223], v196 offset:21504
	ds_read_b128 v[224:227], v196 offset:22528
	ds_read_b128 v[228:231], v196 offset:23552
	global_load_lds_dwordx4 v[182:183], off
	s_add_i32 m0, s0, 0x2000
	s_add_u32 s4, s44, 0x20000
	v_lshl_add_u64 v[184:185], s[44:45], 0, v[166:167]
	s_addc_u32 s5, s45, 0
	s_add_i32 s0, s80, s48
	global_load_lds_dwordx4 v[184:185], off
	v_lshl_add_u64 v[186:187], s[4:5], 0, v[170:171]
	s_mov_b32 m0, s0
	v_lshl_add_u64 v[188:189], s[46:47], 0, v[168:169]
	global_load_lds_dwordx4 v[186:187], off
	v_lshl_add_u64 v[186:187], s[4:5], 0, v[166:167]
	s_add_i32 m0, s0, 0x2000
	s_nop 0
	global_load_lds_dwordx4 v[186:187], off
	v_lshl_add_u64 v[186:187], s[46:47], 0, v[172:173]
	s_mov_b32 m0, s41
	s_nop 0
	global_load_lds_dwordx4 v[186:187], off
	s_mov_b32 m0, s71
	s_nop 0
	global_load_lds_dwordx4 v[188:189], off
	s_waitcnt vmcnt(8)
	s_waitcnt lgkmcnt(0)
	s_barrier
	s_setprio 3
	s_waitcnt lgkmcnt(0)
	v_mfma_f32_16x16x128_f8f6f4 v[94:97], v[18:25], v[200:207], v[94:97]
	v_mfma_f32_16x16x128_f8f6f4 v[90:93], v[26:33], v[200:207], v[90:93]
	v_mfma_f32_16x16x128_f8f6f4 v[86:89], v[18:25], v[208:215], v[86:89]
	v_mfma_f32_16x16x128_f8f6f4 v[82:85], v[26:33], v[208:215], v[82:85]
	v_mfma_f32_16x16x128_f8f6f4 v[70:73], v[18:25], v[216:223], v[70:73]
	v_mfma_f32_16x16x128_f8f6f4 v[66:69], v[26:33], v[216:223], v[66:69]
	v_mfma_f32_16x16x128_f8f6f4 v[54:57], v[18:25], v[224:231], v[54:57]
	v_mfma_f32_16x16x128_f8f6f4 v[50:53], v[26:33], v[224:231], v[50:53]
	s_setprio 0
	s_setprio 3
	v_mfma_f32_16x16x128_f8f6f4 v[78:81], v[2:9], v[200:207], v[78:81]
	v_mfma_f32_16x16x128_f8f6f4 v[74:77], v[10:17], v[200:207], v[74:77]
	v_mfma_f32_16x16x128_f8f6f4 v[62:65], v[2:9], v[208:215], v[62:65]
	v_mfma_f32_16x16x128_f8f6f4 v[58:61], v[10:17], v[208:215], v[58:61]
	v_mfma_f32_16x16x128_f8f6f4 v[46:49], v[2:9], v[216:223], v[46:49]
	v_mfma_f32_16x16x128_f8f6f4 v[42:45], v[10:17], v[216:223], v[42:45]
	v_mfma_f32_16x16x128_f8f6f4 v[38:41], v[2:9], v[224:231], v[38:41]
	v_mfma_f32_16x16x128_f8f6f4 v[34:37], v[10:17], v[224:231], v[34:37]
	s_setprio 0
	s_barrier
	s_add_i32 s0, 0, 0x18000
	s_add_i32 s1, 0, 0x1c000
	v_add_u32_e32 v14, s0, v190
	v_add_u32_e32 v30, s1, v190
	ds_read_b128 v[2:5], v14
	ds_read_b128 v[6:9], v14 offset:1024
	ds_read_b128 v[10:13], v14 offset:2048
	ds_read_b128 v[14:17], v14 offset:3072
	ds_read_b128 v[18:21], v30
	ds_read_b128 v[22:25], v30 offset:1024
	ds_read_b128 v[26:29], v30 offset:2048
	ds_read_b128 v[30:33], v30 offset:3072
	s_add_u32 s4, s46, 0x20000
	s_addc_u32 s5, s47, 0
	s_mov_b32 m0, s72
	v_lshl_add_u64 v[232:233], s[4:5], 0, v[172:173]
	ds_read_b128 v[200:203], v196 offset:32768
	ds_read_b128 v[204:207], v196 offset:33792
	ds_read_b128 v[208:211], v196 offset:34816
	ds_read_b128 v[212:215], v196 offset:35840
	ds_read_b128 v[216:219], v196 offset:36864
	ds_read_b128 v[220:223], v196 offset:37888
	ds_read_b128 v[224:227], v196 offset:38912
	ds_read_b128 v[228:231], v196 offset:39936
	global_load_lds_dwordx4 v[232:233], off
	v_lshl_add_u64 v[232:233], s[4:5], 0, v[168:169]
	s_mov_b32 m0, s73
	s_nop 0
	global_load_lds_dwordx4 v[232:233], off
	s_waitcnt vmcnt(8)
	s_waitcnt lgkmcnt(0)
	s_barrier
; #define PG8_STAGE(bufoff, gbase, voff) do { _Pragma("unroll") for (int _i = 0; _i < 2; ++_i) \
;         __builtin_amdgcn_global_load_lds((const unsigned*)((const char*)(gbase) + (voff)[_i]), (PG8_LAS unsigned*)(lds + (bufoff) + ldsw + _i * 8192), 16, 0, 0); } while (0)
; #define PG8_LDA(dst, b, h) do { _Pragma("unroll") for (int m = 0; m < 4; ++m) Frag<F8>::load(dst[m], lds + PG8_SA(b, h) + aoff + m * 2048); } while (0)
; #define PG8_MMA(ai, bj, At, Bt) do { __builtin_amdgcn_s_setprio(3); _Pragma("unroll") for (int m = 0; m < 4; ++m) _Pragma("unroll") for (int n = 0; n < 2; ++n) Frag<F8>::mma(acc[ai][bj][m][n], Bt[n], At[m]); \
;         __builtin_amdgcn_s_setprio(0); } while (0)
; #define PG8_WAIT_V(n) asm volatile("s_waitcnt vmcnt(" #n ")" ::: "memory")
; #define PG8_WAIT_L(n) asm volatile("s_waitcnt lgkmcnt(" #n ")" ::: "memory")
; #define PG8_BAR __builtin_amdgcn_s_barrier()
; #define PG8_SCHED __builtin_amdgcn_sched_barrier(0)
; template <class Epi, class Sched, bool ALIGN_EPI = false, bool SP2 = false, bool F8 = false>
; __device__ __forceinline__ void gemm_phase(PG8_LAS unsigned char* lds, const Gemm g, const Sched& S, const Epi& E) {
;     ...
;             PG8_LDA(At, 1, 1); PG8_STAGE(PG8_SB(1, 0), b3, voffB); PG8_STAGE(PG8_SB(1, 1), b3 + hstep, voffB); PG8_STAGE(PG8_SA(1, 0), a3, voffA);
;             PG8_WAIT_V(8); PG8_WAIT_L(0); PG8_BAR; PG8_MMA(1, 0, At, B0); PG8_MMA(1, 1, At, B1); PG8_BAR; PG8_SCHED;
	s_setprio 3
	s_waitcnt lgkmcnt(0)
	v_mfma_f32_16x16x128_f8f6f4 v[158:161], v[2:9], v[200:207], v[158:161]
	v_mfma_f32_16x16x128_f8f6f4 v[154:157], v[10:17], v[200:207], v[154:157]
	v_mfma_f32_16x16x128_f8f6f4 v[150:153], v[2:9], v[208:215], v[150:153]
	v_mfma_f32_16x16x128_f8f6f4 v[142:145], v[10:17], v[208:215], v[142:145]
	v_mfma_f32_16x16x128_f8f6f4 v[130:133], v[2:9], v[216:223], v[130:133]
	v_mfma_f32_16x16x128_f8f6f4 v[122:125], v[10:17], v[216:223], v[122:125]
	v_mfma_f32_16x16x128_f8f6f4 v[118:121], v[2:9], v[224:231], v[118:121]
	v_mfma_f32_16x16x128_f8f6f4 v[110:113], v[10:17], v[224:231], v[110:113]
	s_setprio 0
	s_setprio 3
	v_mfma_f32_16x16x128_f8f6f4 v[146:149], v[18:25], v[200:207], v[146:149]
	v_mfma_f32_16x16x128_f8f6f4 v[138:141], v[26:33], v[200:207], v[138:141]
	v_mfma_f32_16x16x128_f8f6f4 v[134:137], v[18:25], v[208:215], v[134:137]
	v_mfma_f32_16x16x128_f8f6f4 v[126:129], v[26:33], v[208:215], v[126:129]
	v_mfma_f32_16x16x128_f8f6f4 v[114:117], v[18:25], v[216:223], v[114:117]
	v_mfma_f32_16x16x128_f8f6f4 v[106:109], v[26:33], v[216:223], v[106:109]
	v_mfma_f32_16x16x128_f8f6f4 v[102:105], v[18:25], v[224:231], v[102:105]
	v_mfma_f32_16x16x128_f8f6f4 v[98:101], v[26:33], v[224:231], v[98:101]
	s_setprio 0
	s_barrier
	s_add_i32 s0, s0, s48
	v_lshl_add_u64 v[182:183], v[182:183], 0, s[18:19]
	s_mov_b32 m0, s0
	ds_read_b128 v[200:203], v196 offset:49152
	ds_read_b128 v[204:207], v196 offset:50176
	ds_read_b128 v[208:211], v196 offset:51200
	ds_read_b128 v[212:215], v196 offset:52224
	ds_read_b128 v[216:219], v196 offset:53248
	ds_read_b128 v[220:223], v196 offset:54272
	ds_read_b128 v[224:227], v196 offset:55296
	ds_read_b128 v[228:231], v196 offset:56320
	global_load_lds_dwordx4 v[182:183], off
	s_add_i32 m0, s0, 0x2000
	s_add_u32 s4, s44, 0x20080
	v_lshl_add_u64 v[182:183], v[184:185], 0, s[18:19]
	s_addc_u32 s5, s45, 0
	s_add_i32 s0, s1, s48
	global_load_lds_dwordx4 v[182:183], off
	v_lshl_add_u64 v[182:183], s[4:5], 0, v[170:171]
	s_mov_b32 m0, s0
	s_nop 0
	global_load_lds_dwordx4 v[182:183], off
	v_lshl_add_u64 v[182:183], s[4:5], 0, v[166:167]
	s_add_i32 m0, s0, 0x2000
	s_nop 0
	global_load_lds_dwordx4 v[182:183], off
	v_lshl_add_u64 v[182:183], v[186:187], 0, s[18:19]
	s_mov_b32 m0, s74
	s_nop 0
	global_load_lds_dwordx4 v[182:183], off
	v_lshl_add_u64 v[182:183], v[188:189], 0, s[18:19]
	s_mov_b32 m0, s75
	s_nop 0
	global_load_lds_dwordx4 v[182:183], off
	s_waitcnt vmcnt(8)
	s_waitcnt lgkmcnt(0)
	s_barrier
	s_setprio 3
	s_waitcnt lgkmcnt(0)
	v_mfma_f32_16x16x128_f8f6f4 v[94:97], v[2:9], v[200:207], v[94:97]
	v_mfma_f32_16x16x128_f8f6f4 v[90:93], v[10:17], v[200:207], v[90:93]
	v_mfma_f32_16x16x128_f8f6f4 v[86:89], v[2:9], v[208:215], v[86:89]
	v_mfma_f32_16x16x128_f8f6f4 v[82:85], v[10:17], v[208:215], v[82:85]
	v_mfma_f32_16x16x128_f8f6f4 v[70:73], v[2:9], v[216:223], v[70:73]
	v_mfma_f32_16x16x128_f8f6f4 v[66:69], v[10:17], v[216:223], v[66:69]
	v_mfma_f32_16x16x128_f8f6f4 v[54:57], v[2:9], v[224:231], v[54:57]
	v_mfma_f32_16x16x128_f8f6f4 v[50:53], v[10:17], v[224:231], v[50:53]
	s_setprio 0
	s_setprio 3
	v_mfma_f32_16x16x128_f8f6f4 v[78:81], v[18:25], v[200:207], v[78:81]
	v_mfma_f32_16x16x128_f8f6f4 v[74:77], v[26:33], v[200:207], v[74:77]
	v_mfma_f32_16x16x128_f8f6f4 v[62:65], v[18:25], v[208:215], v[62:65]
	v_mfma_f32_16x16x128_f8f6f4 v[58:61], v[26:33], v[208:215], v[58:61]
	v_mfma_f32_16x16x128_f8f6f4 v[46:49], v[18:25], v[216:223], v[46:49]
	v_mfma_f32_16x16x128_f8f6f4 v[42:45], v[26:33], v[216:223], v[42:45]
	v_mfma_f32_16x16x128_f8f6f4 v[38:41], v[18:25], v[224:231], v[38:41]
	v_mfma_f32_16x16x128_f8f6f4 v[34:37], v[26:33], v[224:231], v[34:37]
	s_setprio 0
	s_barrier
	s_add_i32 s87, s87, 2
	s_add_u32 s42, s42, 0x100
	s_addc_u32 s43, s43, 0
	s_add_u32 s85, s85, 0x100
	s_addc_u32 s86, s86, 0
	s_cmp_gt_u32 s87, 5
	s_cbranch_scc0 .LBB0_802

; #define PG8_STAGE(bufoff, gbase, voff) do { _Pragma("unroll") for (int _i = 0; _i < 2; ++_i) \
;         __builtin_amdgcn_global_load_lds((const unsigned*)((const char*)(gbase) + (voff)[_i]), (PG8_LAS unsigned*)(lds + (bufoff) + ldsw + _i * 8192), 16, 0, 0); } while (0)
; #define PG8_LDA(dst, b, h) do { _Pragma("unroll") for (int m = 0; m < 4; ++m) Frag<F8>::load(dst[m], lds + PG8_SA(b, h) + aoff + m * 2048); } while (0)
; #define PG8_BAR __builtin_amdgcn_s_barrier()
; template <class Epi, class Sched, bool ALIGN_EPI = false, bool SP2 = false, bool F8 = false>
; __device__ __forceinline__ void gemm_phase(PG8_LAS unsigned char* lds, const Gemm g, const Sched& S, const Epi& E) {
;     ...
;         const bool has_next = S.next(ui + 1, nxt);
;         const char* nA = has_next ? (const char*)g.A + (size_t)nxt.pm * tstep + nxt.ko : cA; const char* nB = has_next ? (const char*)g.Bt + (size_t)nxt.pn * tstep + nxt.ko : cB;
;         for (int t = 0; t < nt; t += 2) {
;             const bool last = (t == nt - 2);
;             const char* a1 = cA + (size_t)(t + 1) * kstep;
;             const char* a2 = last ? nA : cA + (size_t)(t + 2) * kstep; const char* b2 = last ? nB : cB + (size_t)(t + 2) * kstep;
;             const char* a3 = a2 + kstep; const char* b3 = b2 + kstep;
;             if (last && has_next) S.a_ready(nxt);
;             if constexpr (SP2) {
;             PG8_LDB(B0, 0, 0); PG8_LDB(B1, 0, 1); PG8_SCHED; PG8_LDA(At, 0, 0); PG8_STAGE(PG8_SA(1, 1), a1 + hstep, voffA);
;             PG8_WAIT_V(8); PG8_WAIT_L(0); PG8_BAR; PG8_MMA(0, 0, At, B0); PG8_MMA(0, 1, At, B1); PG8_BAR; PG8_SCHED;
;             PG8_LDA(At, 0, 1); PG8_STAGE(PG8_SB(0, 0), b2, voffB); PG8_STAGE(PG8_SB(0, 1), b2 + hstep, voffB); PG8_STAGE(PG8_SA(0, 0), a2, voffA);
;             PG8_WAIT_V(8); PG8_WAIT_L(0); PG8_BAR; PG8_MMA(1, 0, At, B0); PG8_MMA(1, 1, At, B1); PG8_BAR; PG8_SCHED;
;             PG8_LDB(B0, 1, 0); PG8_LDB(B1, 1, 1); PG8_SCHED; PG8_LDA(At, 1, 0); PG8_STAGE(PG8_SA(0, 1), a2 + hstep, voffA);
;             PG8_WAIT_V(8); PG8_WAIT_L(0); PG8_BAR; PG8_MMA(0, 0, At, B0); PG8_MMA(0, 1, At, B1); PG8_BAR; PG8_SCHED;
;             PG8_LDA(At, 1, 1); PG8_STAGE(PG8_SB(1, 0), b3, voffB); PG8_STAGE(PG8_SB(1, 1), b3 + hstep, voffB); PG8_STAGE(PG8_SA(1, 0), a3, voffA);
;             PG8_WAIT_V(8); PG8_WAIT_L(0); PG8_BAR; PG8_MMA(1, 0, At, B0); PG8_MMA(1, 1, At, B1); PG8_BAR; PG8_SCHED;
.LBB0_1309:
	s_ashr_i32 s25, s24, 31
	s_lshl_b64 s[4:5], s[24:25], 18
	s_add_u32 s30, s48, s4
	s_addc_u32 s31, s49, s5
	s_and_b64 s[4:5], s[22:23], exec
	s_cselect_b32 s25, s31, s43
	s_cselect_b32 s77, s30, s42
	s_ashr_i32 s27, s26, 31
	s_lshl_b64 s[4:5], s[26:27], 18
	s_add_u32 s36, s50, s4
	s_addc_u32 s37, s51, s5
	s_and_b64 s[4:5], s[22:23], exec
	s_cselect_b32 s27, s37, s45
	s_cselect_b32 s78, s36, s44
	s_add_u32 s42, s42, 0x20080
	s_addc_u32 s43, s43, 0
	s_add_u32 s79, s44, 0x100
	s_addc_u32 s80, s45, 0
	s_mov_b32 s81, -2
	ds_read_b128 v[18:21], v186
	ds_read_b128 v[22:25], v186 offset:1024
	ds_read_b128 v[26:29], v186 offset:2048
	ds_read_b128 v[30:33], v186 offset:3072
	ds_read_b128 v[2:5], v187
	ds_read_b128 v[6:9], v187 offset:1024
	ds_read_b128 v[10:13], v187 offset:2048
	ds_read_b128 v[14:17], v187 offset:3072
	s_add_u32 s0, s42, 0xfffe0080
	s_addc_u32 s1, s43, -1
	s_cmp_eq_u32 s81, 4
	s_cselect_b32 s47, s25, s1
	s_cselect_b32 s46, s77, s0
	s_cselect_b32 s45, s27, s80
	s_cselect_b32 s44, s78, s79
	v_lshl_add_u64 v[214:215], s[42:43], 0, v[172:173]
	s_add_i32 m0, s39, 0xc000
	ds_read_b128 v[176:179], v188
	ds_read_b128 v[180:183], v188 offset:1024
	ds_read_b128 v[190:193], v188 offset:2048
	ds_read_b128 v[194:197], v188 offset:3072
	ds_read_b128 v[198:201], v188 offset:4096
	ds_read_b128 v[202:205], v188 offset:5120
	ds_read_b128 v[206:209], v188 offset:6144
	ds_read_b128 v[210:213], v188 offset:7168
	global_load_lds_dwordx4 v[214:215], off
	v_lshl_add_u64 v[214:215], s[42:43], 0, v[174:175]
	s_add_i32 m0, s39, 0xe000
	s_nop 0
	global_load_lds_dwordx4 v[214:215], off
	s_waitcnt vmcnt(8)
	s_waitcnt lgkmcnt(0)
	s_barrier
	s_setprio 3
	s_waitcnt lgkmcnt(0)
	v_mfma_f32_16x16x128_f8f6f4 v[158:161], v[18:25], v[176:183], 0
	v_mfma_f32_16x16x128_f8f6f4 v[150:153], v[26:33], v[176:183], 0
	v_mfma_f32_16x16x128_f8f6f4 v[142:145], v[18:25], v[190:197], 0
	v_mfma_f32_16x16x128_f8f6f4 v[134:137], v[26:33], v[190:197], 0
	v_mfma_f32_16x16x128_f8f6f4 v[126:129], v[18:25], v[198:205], 0
	v_mfma_f32_16x16x128_f8f6f4 v[118:121], v[26:33], v[198:205], 0
	v_mfma_f32_16x16x128_f8f6f4 v[110:113], v[18:25], v[206:213], 0
	v_mfma_f32_16x16x128_f8f6f4 v[102:105], v[26:33], v[206:213], 0
	s_setprio 0
	s_setprio 3
	v_mfma_f32_16x16x128_f8f6f4 v[154:157], v[2:9], v[176:183], 0
	v_mfma_f32_16x16x128_f8f6f4 v[146:149], v[10:17], v[176:183], 0
	v_mfma_f32_16x16x128_f8f6f4 v[138:141], v[2:9], v[190:197], 0
	v_mfma_f32_16x16x128_f8f6f4 v[130:133], v[10:17], v[190:197], 0
	v_mfma_f32_16x16x128_f8f6f4 v[122:125], v[2:9], v[198:205], 0
	v_mfma_f32_16x16x128_f8f6f4 v[114:117], v[10:17], v[198:205], 0
	v_mfma_f32_16x16x128_f8f6f4 v[106:109], v[2:9], v[206:213], 0
	v_mfma_f32_16x16x128_f8f6f4 v[98:101], v[10:17], v[206:213], 0
	s_setprio 0
	s_barrier
	s_add_i32 s0, s74, s52
	v_lshl_add_u64 v[176:177], s[44:45], 0, v[168:169]
	s_mov_b32 m0, s0
	ds_read_b128 v[190:193], v188 offset:16384
	ds_read_b128 v[194:197], v188 offset:17408
	ds_read_b128 v[198:201], v188 offset:18432
	ds_read_b128 v[202:205], v188 offset:19456
	ds_read_b128 v[206:209], v188 offset:20480
	ds_read_b128 v[210:213], v188 offset:21504
	ds_read_b128 v[214:217], v188 offset:22528
	ds_read_b128 v[218:221], v188 offset:23552
	global_load_lds_dwordx4 v[176:177], off
	s_add_i32 m0, s0, 0x2000
	s_add_u32 s4, s44, 0x20000
	v_lshl_add_u64 v[178:179], s[44:45], 0, v[164:165]
	s_addc_u32 s5, s45, 0
	s_add_i32 s0, s75, s52
	global_load_lds_dwordx4 v[178:179], off
	v_lshl_add_u64 v[180:181], s[4:5], 0, v[168:169]
	s_mov_b32 m0, s0
	v_lshl_add_u64 v[182:183], s[46:47], 0, v[166:167]
	global_load_lds_dwordx4 v[180:181], off
	v_lshl_add_u64 v[180:181], s[4:5], 0, v[164:165]
	s_add_i32 m0, s0, 0x2000
	s_nop 0
	global_load_lds_dwordx4 v[180:181], off
	v_lshl_add_u64 v[180:181], s[46:47], 0, v[170:171]
	s_mov_b32 m0, s39
	s_nop 0
	global_load_lds_dwordx4 v[180:181], off
	s_mov_b32 m0, s41
	s_nop 0
	global_load_lds_dwordx4 v[182:183], off
	s_waitcnt vmcnt(8)
	s_waitcnt lgkmcnt(0)
	s_barrier
	s_setprio 3
	s_waitcnt lgkmcnt(0)
	v_mfma_f32_16x16x128_f8f6f4 v[94:97], v[18:25], v[190:197], 0
	v_mfma_f32_16x16x128_f8f6f4 v[86:89], v[26:33], v[190:197], 0
	v_mfma_f32_16x16x128_f8f6f4 v[78:81], v[18:25], v[198:205], 0
	v_mfma_f32_16x16x128_f8f6f4 v[70:73], v[26:33], v[198:205], 0
	v_mfma_f32_16x16x128_f8f6f4 v[62:65], v[18:25], v[206:213], 0
	v_mfma_f32_16x16x128_f8f6f4 v[54:57], v[26:33], v[206:213], 0
	v_mfma_f32_16x16x128_f8f6f4 v[46:49], v[18:25], v[214:221], 0
	v_mfma_f32_16x16x128_f8f6f4 v[38:41], v[26:33], v[214:221], 0
	s_setprio 0
	s_setprio 3
	v_mfma_f32_16x16x128_f8f6f4 v[90:93], v[2:9], v[190:197], 0
	v_mfma_f32_16x16x128_f8f6f4 v[82:85], v[10:17], v[190:197], 0
	v_mfma_f32_16x16x128_f8f6f4 v[74:77], v[2:9], v[198:205], 0
	v_mfma_f32_16x16x128_f8f6f4 v[66:69], v[10:17], v[198:205], 0
	v_mfma_f32_16x16x128_f8f6f4 v[58:61], v[2:9], v[206:213], 0
	v_mfma_f32_16x16x128_f8f6f4 v[50:53], v[10:17], v[206:213], 0
	v_mfma_f32_16x16x128_f8f6f4 v[42:45], v[2:9], v[214:221], 0
	v_mfma_f32_16x16x128_f8f6f4 v[34:37], v[10:17], v[214:221], 0
	s_setprio 0
	s_barrier
	s_add_i32 s0, 0, 0x18000
	s_add_i32 s1, 0, 0x1c000
	v_add_u32_e32 v14, s0, v184
	v_add_u32_e32 v30, s1, v184
	ds_read_b128 v[2:5], v14
	ds_read_b128 v[6:9], v14 offset:1024
	ds_read_b128 v[10:13], v14 offset:2048
	ds_read_b128 v[14:17], v14 offset:3072
	ds_read_b128 v[18:21], v30
	ds_read_b128 v[22:25], v30 offset:1024
	ds_read_b128 v[26:29], v30 offset:2048
	ds_read_b128 v[30:33], v30 offset:3072
	s_add_u32 s4, s46, 0x20000
	s_addc_u32 s5, s47, 0
	s_mov_b32 m0, s58
	v_lshl_add_u64 v[222:223], s[4:5], 0, v[170:171]
	ds_read_b128 v[190:193], v188 offset:32768
	ds_read_b128 v[194:197], v188 offset:33792
	ds_read_b128 v[198:201], v188 offset:34816
	ds_read_b128 v[202:205], v188 offset:35840
	ds_read_b128 v[206:209], v188 offset:36864
	ds_read_b128 v[210:213], v188 offset:37888
	ds_read_b128 v[214:217], v188 offset:38912
	ds_read_b128 v[218:221], v188 offset:39936
	global_load_lds_dwordx4 v[222:223], off
	v_lshl_add_u64 v[222:223], s[4:5], 0, v[166:167]
	s_mov_b32 m0, s59
	s_nop 0
	global_load_lds_dwordx4 v[222:223], off
	s_waitcnt vmcnt(8)
	s_waitcnt lgkmcnt(0)
	s_barrier
; #define PG8_STAGE(bufoff, gbase, voff) do { _Pragma("unroll") for (int _i = 0; _i < 2; ++_i) \
;         __builtin_amdgcn_global_load_lds((const unsigned*)((const char*)(gbase) + (voff)[_i]), (PG8_LAS unsigned*)(lds + (bufoff) + ldsw + _i * 8192), 16, 0, 0); } while (0)
; #define PG8_LDA(dst, b, h) do { _Pragma("unroll") for (int m = 0; m < 4; ++m) Frag<F8>::load(dst[m], lds + PG8_SA(b, h) + aoff + m * 2048); } while (0)
; #define PG8_LDB(dst, b, h) do { _Pragma("unroll") for (int n = 0; n < 2; ++n) Frag<F8>::load(dst[n], lds + PG8_SB(b, h) + boff + n * 2048); } while (0)
; #define PG8_MMA(ai, bj, At, Bt) do { __builtin_amdgcn_s_setprio(3); _Pragma("unroll") for (int m = 0; m < 4; ++m) _Pragma("unroll") for (int n = 0; n < 2; ++n) Frag<F8>::mma(acc[ai][bj][m][n], Bt[n], At[m]); \
;         __builtin_amdgcn_s_setprio(0); } while (0)
; #define PG8_WAIT_V(n) asm volatile("s_waitcnt vmcnt(" #n ")" ::: "memory")
; #define PG8_WAIT_L(n) asm volatile("s_waitcnt lgkmcnt(" #n ")" ::: "memory")
; #define PG8_BAR __builtin_amdgcn_s_barrier()
; #define PG8_SCHED __builtin_amdgcn_sched_barrier(0)
; template <class Epi, class Sched, bool ALIGN_EPI = false, bool SP2 = false, bool F8 = false>
; __device__ __forceinline__ void gemm_phase(PG8_LAS unsigned char* lds, const Gemm g, const Sched& S, const Epi& E) {
;     ...
;             PG8_LDB(B0, 0, 0); PG8_LDB(B1, 0, 1); PG8_SCHED; PG8_LDA(At, 0, 0); PG8_STAGE(PG8_SA(1, 1), a1 + hstep, voffA);
;             PG8_WAIT_V(8); PG8_WAIT_L(0); PG8_BAR; PG8_MMA(0, 0, At, B0); PG8_MMA(0, 1, At, B1); PG8_BAR; PG8_SCHED;
;             PG8_LDA(At, 0, 1); PG8_STAGE(PG8_SB(0, 0), b2, voffB); PG8_STAGE(PG8_SB(0, 1), b2 + hstep, voffB); PG8_STAGE(PG8_SA(0, 0), a2, voffA);
;             PG8_WAIT_V(8); PG8_WAIT_L(0); PG8_BAR; PG8_MMA(1, 0, At, B0); PG8_MMA(1, 1, At, B1); PG8_BAR; PG8_SCHED;
;             PG8_LDB(B0, 1, 0); PG8_LDB(B1, 1, 1); PG8_SCHED; PG8_LDA(At, 1, 0); PG8_STAGE(PG8_SA(0, 1), a2 + hstep, voffA);
;             PG8_WAIT_V(8); PG8_WAIT_L(0); PG8_BAR; PG8_MMA(0, 0, At, B0); PG8_MMA(0, 1, At, B1); PG8_BAR; PG8_SCHED;
;             PG8_LDA(At, 1, 1); PG8_STAGE(PG8_SB(1, 0), b3, voffB); PG8_STAGE(PG8_SB(1, 1), b3 + hstep, voffB); PG8_STAGE(PG8_SA(1, 0), a3, voffA);
;             PG8_WAIT_V(8); PG8_WAIT_L(0); PG8_BAR; PG8_MMA(1, 0, At, B0); PG8_MMA(1, 1, At, B1); PG8_BAR; PG8_SCHED;
	s_setprio 3
	s_waitcnt lgkmcnt(0)
	v_mfma_f32_16x16x128_f8f6f4 v[158:161], v[2:9], v[190:197], v[158:161]
	v_mfma_f32_16x16x128_f8f6f4 v[150:153], v[10:17], v[190:197], v[150:153]
	v_mfma_f32_16x16x128_f8f6f4 v[142:145], v[2:9], v[198:205], v[142:145]
	v_mfma_f32_16x16x128_f8f6f4 v[134:137], v[10:17], v[198:205], v[134:137]
	v_mfma_f32_16x16x128_f8f6f4 v[126:129], v[2:9], v[206:213], v[126:129]
	v_mfma_f32_16x16x128_f8f6f4 v[118:121], v[10:17], v[206:213], v[118:121]
	v_mfma_f32_16x16x128_f8f6f4 v[110:113], v[2:9], v[214:221], v[110:113]
	v_mfma_f32_16x16x128_f8f6f4 v[102:105], v[10:17], v[214:221], v[102:105]
	s_setprio 0
	s_setprio 3
	v_mfma_f32_16x16x128_f8f6f4 v[154:157], v[18:25], v[190:197], v[154:157]
	v_mfma_f32_16x16x128_f8f6f4 v[146:149], v[26:33], v[190:197], v[146:149]
	v_mfma_f32_16x16x128_f8f6f4 v[138:141], v[18:25], v[198:205], v[138:141]
	v_mfma_f32_16x16x128_f8f6f4 v[130:133], v[26:33], v[198:205], v[130:133]
	v_mfma_f32_16x16x128_f8f6f4 v[122:125], v[18:25], v[206:213], v[122:125]
	v_mfma_f32_16x16x128_f8f6f4 v[114:117], v[26:33], v[206:213], v[114:117]
	v_mfma_f32_16x16x128_f8f6f4 v[106:109], v[18:25], v[214:221], v[106:109]
	v_mfma_f32_16x16x128_f8f6f4 v[98:101], v[26:33], v[214:221], v[98:101]
	s_setprio 0
	s_barrier
	s_add_i32 s0, s0, s52
	v_lshl_add_u64 v[176:177], v[176:177], 0, s[14:15]
	s_mov_b32 m0, s0
	ds_read_b128 v[190:193], v188 offset:49152
	ds_read_b128 v[194:197], v188 offset:50176
	ds_read_b128 v[198:201], v188 offset:51200
	ds_read_b128 v[202:205], v188 offset:52224
	ds_read_b128 v[206:209], v188 offset:53248
	ds_read_b128 v[210:213], v188 offset:54272
	ds_read_b128 v[214:217], v188 offset:55296
	ds_read_b128 v[218:221], v188 offset:56320
	global_load_lds_dwordx4 v[176:177], off
	s_add_i32 m0, s0, 0x2000
	s_add_u32 s4, s44, 0x20080
	v_lshl_add_u64 v[176:177], v[178:179], 0, s[14:15]
	s_addc_u32 s5, s45, 0
	s_add_i32 s0, s1, s52
	global_load_lds_dwordx4 v[176:177], off
	v_lshl_add_u64 v[176:177], s[4:5], 0, v[168:169]
	s_mov_b32 m0, s0
	s_nop 0
	global_load_lds_dwordx4 v[176:177], off
	v_lshl_add_u64 v[176:177], s[4:5], 0, v[164:165]
	s_add_i32 m0, s0, 0x2000
	s_nop 0
	global_load_lds_dwordx4 v[176:177], off
	v_lshl_add_u64 v[176:177], v[180:181], 0, s[14:15]
	s_mov_b32 m0, s60
	s_nop 0
	global_load_lds_dwordx4 v[176:177], off
	v_lshl_add_u64 v[176:177], v[182:183], 0, s[14:15]
	s_mov_b32 m0, s61
	s_nop 0
	global_load_lds_dwordx4 v[176:177], off
	s_waitcnt vmcnt(8)
	s_waitcnt lgkmcnt(0)
	s_barrier
	s_setprio 3
	s_waitcnt lgkmcnt(0)
	v_mfma_f32_16x16x128_f8f6f4 v[94:97], v[2:9], v[190:197], v[94:97]
	v_mfma_f32_16x16x128_f8f6f4 v[86:89], v[10:17], v[190:197], v[86:89]
	v_mfma_f32_16x16x128_f8f6f4 v[78:81], v[2:9], v[198:205], v[78:81]
	v_mfma_f32_16x16x128_f8f6f4 v[70:73], v[10:17], v[198:205], v[70:73]
	v_mfma_f32_16x16x128_f8f6f4 v[62:65], v[2:9], v[206:213], v[62:65]
	v_mfma_f32_16x16x128_f8f6f4 v[54:57], v[10:17], v[206:213], v[54:57]
	v_mfma_f32_16x16x128_f8f6f4 v[46:49], v[2:9], v[214:221], v[46:49]
	v_mfma_f32_16x16x128_f8f6f4 v[38:41], v[10:17], v[214:221], v[38:41]
	s_setprio 0
	s_setprio 3
	v_mfma_f32_16x16x128_f8f6f4 v[90:93], v[18:25], v[190:197], v[90:93]
	v_mfma_f32_16x16x128_f8f6f4 v[82:85], v[26:33], v[190:197], v[82:85]
	v_mfma_f32_16x16x128_f8f6f4 v[74:77], v[18:25], v[198:205], v[74:77]
	v_mfma_f32_16x16x128_f8f6f4 v[66:69], v[26:33], v[198:205], v[66:69]
	v_mfma_f32_16x16x128_f8f6f4 v[58:61], v[18:25], v[206:213], v[58:61]
	v_mfma_f32_16x16x128_f8f6f4 v[50:53], v[26:33], v[206:213], v[50:53]
	v_mfma_f32_16x16x128_f8f6f4 v[42:45], v[18:25], v[214:221], v[42:45]
	v_mfma_f32_16x16x128_f8f6f4 v[34:37], v[26:33], v[214:221], v[34:37]
	s_setprio 0
	s_barrier
	s_add_i32 s81, s81, 2
	s_add_u32 s42, s42, 0x100
	s_addc_u32 s43, s43, 0
	s_add_u32 s79, s79, 0x100
	s_addc_u32 s80, s80, 0
	s_cmp_gt_u32 s81, 5
	s_cbranch_scc1 .Lpeel_exit_3
.LBB0_1310:
	ds_read_b128 v[18:21], v186
	ds_read_b128 v[22:25], v186 offset:1024
	ds_read_b128 v[26:29], v186 offset:2048
	ds_read_b128 v[30:33], v186 offset:3072
	ds_read_b128 v[2:5], v187
	ds_read_b128 v[6:9], v187 offset:1024
	ds_read_b128 v[10:13], v187 offset:2048
	ds_read_b128 v[14:17], v187 offset:3072
	s_add_u32 s0, s42, 0xfffe0080
	s_addc_u32 s1, s43, -1
	s_cmp_eq_u32 s81, 4
	s_cselect_b32 s47, s25, s1
	s_cselect_b32 s46, s77, s0
	s_cselect_b32 s45, s27, s80
	s_cselect_b32 s44, s78, s79
	v_lshl_add_u64 v[214:215], s[42:43], 0, v[172:173]
	s_add_i32 m0, s39, 0xc000
	ds_read_b128 v[176:179], v188
	ds_read_b128 v[180:183], v188 offset:1024
	ds_read_b128 v[190:193], v188 offset:2048
	ds_read_b128 v[194:197], v188 offset:3072
	ds_read_b128 v[198:201], v188 offset:4096
	ds_read_b128 v[202:205], v188 offset:5120
	ds_read_b128 v[206:209], v188 offset:6144
	ds_read_b128 v[210:213], v188 offset:7168
	global_load_lds_dwordx4 v[214:215], off
	v_lshl_add_u64 v[214:215], s[42:43], 0, v[174:175]
	s_add_i32 m0, s39, 0xe000
	s_nop 0
	global_load_lds_dwordx4 v[214:215], off
	s_waitcnt vmcnt(8)
	s_waitcnt lgkmcnt(0)
	s_barrier
	s_setprio 3
	s_waitcnt lgkmcnt(0)
	v_mfma_f32_16x16x128_f8f6f4 v[158:161], v[18:25], v[176:183], v[158:161]
	v_mfma_f32_16x16x128_f8f6f4 v[150:153], v[26:33], v[176:183], v[150:153]
	v_mfma_f32_16x16x128_f8f6f4 v[142:145], v[18:25], v[190:197], v[142:145]
	v_mfma_f32_16x16x128_f8f6f4 v[134:137], v[26:33], v[190:197], v[134:137]
	v_mfma_f32_16x16x128_f8f6f4 v[126:129], v[18:25], v[198:205], v[126:129]
	v_mfma_f32_16x16x128_f8f6f4 v[118:121], v[26:33], v[198:205], v[118:121]
	v_mfma_f32_16x16x128_f8f6f4 v[110:113], v[18:25], v[206:213], v[110:113]
	v_mfma_f32_16x16x128_f8f6f4 v[102:105], v[26:33], v[206:213], v[102:105]
	s_setprio 0
	s_setprio 3
	v_mfma_f32_16x16x128_f8f6f4 v[154:157], v[2:9], v[176:183], v[154:157]
	v_mfma_f32_16x16x128_f8f6f4 v[146:149], v[10:17], v[176:183], v[146:149]
	v_mfma_f32_16x16x128_f8f6f4 v[138:141], v[2:9], v[190:197], v[138:141]
	v_mfma_f32_16x16x128_f8f6f4 v[130:133], v[10:17], v[190:197], v[130:133]
	v_mfma_f32_16x16x128_f8f6f4 v[122:125], v[2:9], v[198:205], v[122:125]
	v_mfma_f32_16x16x128_f8f6f4 v[114:117], v[10:17], v[198:205], v[114:117]
	v_mfma_f32_16x16x128_f8f6f4 v[106:109], v[2:9], v[206:213], v[106:109]
	v_mfma_f32_16x16x128_f8f6f4 v[98:101], v[10:17], v[206:213], v[98:101]
	s_setprio 0
	s_barrier
; #define PG8_STAGE(bufoff, gbase, voff) do { _Pragma("unroll") for (int _i = 0; _i < 2; ++_i) \
;         __builtin_amdgcn_global_load_lds((const unsigned*)((const char*)(gbase) + (voff)[_i]), (PG8_LAS unsigned*)(lds + (bufoff) + ldsw + _i * 8192), 16, 0, 0); } while (0)
; #define PG8_LDA(dst, b, h) do { _Pragma("unroll") for (int m = 0; m < 4; ++m) Frag<F8>::load(dst[m], lds + PG8_SA(b, h) + aoff + m * 2048); } while (0)
; #define PG8_LDB(dst, b, h) do { _Pragma("unroll") for (int n = 0; n < 2; ++n) Frag<F8>::load(dst[n], lds + PG8_SB(b, h) + boff + n * 2048); } while (0)
; #define PG8_MMA(ai, bj, At, Bt) do { __builtin_amdgcn_s_setprio(3); _Pragma("unroll") for (int m = 0; m < 4; ++m) _Pragma("unroll") for (int n = 0; n < 2; ++n) Frag<F8>::mma(acc[ai][bj][m][n], Bt[n], At[m]); \
;         __builtin_amdgcn_s_setprio(0); } while (0)
; #define PG8_WAIT_V(n) asm volatile("s_waitcnt vmcnt(" #n ")" ::: "memory")
; #define PG8_WAIT_L(n) asm volatile("s_waitcnt lgkmcnt(" #n ")" ::: "memory")
; #define PG8_BAR __builtin_amdgcn_s_barrier()
; #define PG8_SCHED __builtin_amdgcn_sched_barrier(0)
; template <class Epi, class Sched, bool ALIGN_EPI = false, bool SP2 = false, bool F8 = false>
; __device__ __forceinline__ void gemm_phase(PG8_LAS unsigned char* lds, const Gemm g, const Sched& S, const Epi& E) {
;     ...
;             PG8_LDB(B0, 1, 0); PG8_LDB(B1, 1, 1); PG8_SCHED; PG8_LDA(At, 1, 0); PG8_STAGE(PG8_SA(0, 1), a2 + hstep, voffA);
;             PG8_WAIT_V(8); PG8_WAIT_L(0); PG8_BAR; PG8_MMA(0, 0, At, B0); PG8_MMA(0, 1, At, B1); PG8_BAR; PG8_SCHED;
;             PG8_LDA(At, 1, 1); PG8_STAGE(PG8_SB(1, 0), b3, voffB); PG8_STAGE(PG8_SB(1, 1), b3 + hstep, voffB); PG8_STAGE(PG8_SA(1, 0), a3, voffA);
;             PG8_WAIT_V(8); PG8_WAIT_L(0); PG8_BAR; PG8_MMA(1, 0, At, B0); PG8_MMA(1, 1, At, B1); PG8_BAR; PG8_SCHED;
	s_add_i32 s0, s74, s52
	v_lshl_add_u64 v[176:177], s[44:45], 0, v[168:169]
	s_mov_b32 m0, s0
	ds_read_b128 v[190:193], v188 offset:16384
	ds_read_b128 v[194:197], v188 offset:17408
	ds_read_b128 v[198:201], v188 offset:18432
	ds_read_b128 v[202:205], v188 offset:19456
	ds_read_b128 v[206:209], v188 offset:20480
	ds_read_b128 v[210:213], v188 offset:21504
	ds_read_b128 v[214:217], v188 offset:22528
	ds_read_b128 v[218:221], v188 offset:23552
	global_load_lds_dwordx4 v[176:177], off
	s_add_i32 m0, s0, 0x2000
	s_add_u32 s4, s44, 0x20000
	v_lshl_add_u64 v[178:179], s[44:45], 0, v[164:165]
	s_addc_u32 s5, s45, 0
	s_add_i32 s0, s75, s52
	global_load_lds_dwordx4 v[178:179], off
	v_lshl_add_u64 v[180:181], s[4:5], 0, v[168:169]
	s_mov_b32 m0, s0
	v_lshl_add_u64 v[182:183], s[46:47], 0, v[166:167]
	global_load_lds_dwordx4 v[180:181], off
	v_lshl_add_u64 v[180:181], s[4:5], 0, v[164:165]
	s_add_i32 m0, s0, 0x2000
	s_nop 0
	global_load_lds_dwordx4 v[180:181], off
	v_lshl_add_u64 v[180:181], s[46:47], 0, v[170:171]
	s_mov_b32 m0, s39
	s_nop 0
	global_load_lds_dwordx4 v[180:181], off
	s_mov_b32 m0, s41
	s_nop 0
	global_load_lds_dwordx4 v[182:183], off
	s_waitcnt vmcnt(8)
	s_waitcnt lgkmcnt(0)
	s_barrier
	s_setprio 3
	s_waitcnt lgkmcnt(0)
	v_mfma_f32_16x16x128_f8f6f4 v[94:97], v[18:25], v[190:197], v[94:97]
	v_mfma_f32_16x16x128_f8f6f4 v[86:89], v[26:33], v[190:197], v[86:89]
	v_mfma_f32_16x16x128_f8f6f4 v[78:81], v[18:25], v[198:205], v[78:81]
	v_mfma_f32_16x16x128_f8f6f4 v[70:73], v[26:33], v[198:205], v[70:73]
	v_mfma_f32_16x16x128_f8f6f4 v[62:65], v[18:25], v[206:213], v[62:65]
	v_mfma_f32_16x16x128_f8f6f4 v[54:57], v[26:33], v[206:213], v[54:57]
	v_mfma_f32_16x16x128_f8f6f4 v[46:49], v[18:25], v[214:221], v[46:49]
	v_mfma_f32_16x16x128_f8f6f4 v[38:41], v[26:33], v[214:221], v[38:41]
	s_setprio 0
	s_setprio 3
	v_mfma_f32_16x16x128_f8f6f4 v[90:93], v[2:9], v[190:197], v[90:93]
	v_mfma_f32_16x16x128_f8f6f4 v[82:85], v[10:17], v[190:197], v[82:85]
	v_mfma_f32_16x16x128_f8f6f4 v[74:77], v[2:9], v[198:205], v[74:77]
	v_mfma_f32_16x16x128_f8f6f4 v[66:69], v[10:17], v[198:205], v[66:69]
	v_mfma_f32_16x16x128_f8f6f4 v[58:61], v[2:9], v[206:213], v[58:61]
	v_mfma_f32_16x16x128_f8f6f4 v[50:53], v[10:17], v[206:213], v[50:53]
	v_mfma_f32_16x16x128_f8f6f4 v[42:45], v[2:9], v[214:221], v[42:45]
	v_mfma_f32_16x16x128_f8f6f4 v[34:37], v[10:17], v[214:221], v[34:37]
	s_setprio 0
	s_barrier
	s_add_i32 s0, 0, 0x18000
	s_add_i32 s1, 0, 0x1c000
	v_add_u32_e32 v14, s0, v184
	v_add_u32_e32 v30, s1, v184
	ds_read_b128 v[2:5], v14
	ds_read_b128 v[6:9], v14 offset:1024
	ds_read_b128 v[10:13], v14 offset:2048
	ds_read_b128 v[14:17], v14 offset:3072
	ds_read_b128 v[18:21], v30
	ds_read_b128 v[22:25], v30 offset:1024
	ds_read_b128 v[26:29], v30 offset:2048
	ds_read_b128 v[30:33], v30 offset:3072
	s_add_u32 s4, s46, 0x20000
	s_addc_u32 s5, s47, 0
	s_mov_b32 m0, s58
	v_lshl_add_u64 v[222:223], s[4:5], 0, v[170:171]
	ds_read_b128 v[190:193], v188 offset:32768
	ds_read_b128 v[194:197], v188 offset:33792
	ds_read_b128 v[198:201], v188 offset:34816
	ds_read_b128 v[202:205], v188 offset:35840
	ds_read_b128 v[206:209], v188 offset:36864
	ds_read_b128 v[210:213], v188 offset:37888
	ds_read_b128 v[214:217], v188 offset:38912
	ds_read_b128 v[218:221], v188 offset:39936
	global_load_lds_dwordx4 v[222:223], off
	v_lshl_add_u64 v[222:223], s[4:5], 0, v[166:167]
	s_mov_b32 m0, s59
	s_nop 0
	global_load_lds_dwordx4 v[222:223], off
	s_waitcnt vmcnt(8)
	s_waitcnt lgkmcnt(0)
	s_barrier
; #define PG8_STAGE(bufoff, gbase, voff) do { _Pragma("unroll") for (int _i = 0; _i < 2; ++_i) \
;         __builtin_amdgcn_global_load_lds((const unsigned*)((const char*)(gbase) + (voff)[_i]), (PG8_LAS unsigned*)(lds + (bufoff) + ldsw + _i * 8192), 16, 0, 0); } while (0)
; #define PG8_LDA(dst, b, h) do { _Pragma("unroll") for (int m = 0; m < 4; ++m) Frag<F8>::load(dst[m], lds + PG8_SA(b, h) + aoff + m * 2048); } while (0)
; #define PG8_LDB(dst, b, h) do { _Pragma("unroll") for (int n = 0; n < 2; ++n) Frag<F8>::load(dst[n], lds + PG8_SB(b, h) + boff + n * 2048); } while (0)
; #define PG8_MMA(ai, bj, At, Bt) do { __builtin_amdgcn_s_setprio(3); _Pragma("unroll") for (int m = 0; m < 4; ++m) _Pragma("unroll") for (int n = 0; n < 2; ++n) Frag<F8>::mma(acc[ai][bj][m][n], Bt[n], At[m]); \
;         __builtin_amdgcn_s_setprio(0); } while (0)
; #define PG8_WAIT_V(n) asm volatile("s_waitcnt vmcnt(" #n ")" ::: "memory")
; #define PG8_WAIT_L(n) asm volatile("s_waitcnt lgkmcnt(" #n ")" ::: "memory")
; #define PG8_BAR __builtin_amdgcn_s_barrier()
; #define PG8_SCHED __builtin_amdgcn_sched_barrier(0)
; template <class Epi, class Sched, bool ALIGN_EPI = false, bool SP2 = false, bool F8 = false>
; __device__ __forceinline__ void gemm_phase(PG8_LAS unsigned char* lds, const Gemm g, const Sched& S, const Epi& E) {
;     ...
;             PG8_LDB(B0, 1, 0); PG8_LDB(B1, 1, 1); PG8_SCHED; PG8_LDA(At, 1, 0); PG8_STAGE(PG8_SA(0, 1), a2 + hstep, voffA);
;             PG8_WAIT_V(8); PG8_WAIT_L(0); PG8_BAR; PG8_MMA(0, 0, At, B0); PG8_MMA(0, 1, At, B1); PG8_BAR; PG8_SCHED;
;             PG8_LDA(At, 1, 1); PG8_STAGE(PG8_SB(1, 0), b3, voffB); PG8_STAGE(PG8_SB(1, 1), b3 + hstep, voffB); PG8_STAGE(PG8_SA(1, 0), a3, voffA);
;             PG8_WAIT_V(8); PG8_WAIT_L(0); PG8_BAR; PG8_MMA(1, 0, At, B0); PG8_MMA(1, 1, At, B1); PG8_BAR; PG8_SCHED;
	s_setprio 3
	s_waitcnt lgkmcnt(0)
	v_mfma_f32_16x16x128_f8f6f4 v[158:161], v[2:9], v[190:197], v[158:161]
	v_mfma_f32_16x16x128_f8f6f4 v[150:153], v[10:17], v[190:197], v[150:153]
	v_mfma_f32_16x16x128_f8f6f4 v[142:145], v[2:9], v[198:205], v[142:145]
	v_mfma_f32_16x16x128_f8f6f4 v[134:137], v[10:17], v[198:205], v[134:137]
	v_mfma_f32_16x16x128_f8f6f4 v[126:129], v[2:9], v[206:213], v[126:129]
	v_mfma_f32_16x16x128_f8f6f4 v[118:121], v[10:17], v[206:213], v[118:121]
	v_mfma_f32_16x16x128_f8f6f4 v[110:113], v[2:9], v[214:221], v[110:113]
	v_mfma_f32_16x16x128_f8f6f4 v[102:105], v[10:17], v[214:221], v[102:105]
	s_setprio 0
	s_setprio 3
	v_mfma_f32_16x16x128_f8f6f4 v[154:157], v[18:25], v[190:197], v[154:157]
	v_mfma_f32_16x16x128_f8f6f4 v[146:149], v[26:33], v[190:197], v[146:149]
	v_mfma_f32_16x16x128_f8f6f4 v[138:141], v[18:25], v[198:205], v[138:141]
	v_mfma_f32_16x16x128_f8f6f4 v[130:133], v[26:33], v[198:205], v[130:133]
	v_mfma_f32_16x16x128_f8f6f4 v[122:125], v[18:25], v[206:213], v[122:125]
	v_mfma_f32_16x16x128_f8f6f4 v[114:117], v[26:33], v[206:213], v[114:117]
	v_mfma_f32_16x16x128_f8f6f4 v[106:109], v[18:25], v[214:221], v[106:109]
	v_mfma_f32_16x16x128_f8f6f4 v[98:101], v[26:33], v[214:221], v[98:101]
	s_setprio 0
	s_barrier
	s_add_i32 s0, s0, s52
	v_lshl_add_u64 v[176:177], v[176:177], 0, s[14:15]
	s_mov_b32 m0, s0
	ds_read_b128 v[190:193], v188 offset:49152
	ds_read_b128 v[194:197], v188 offset:50176
	ds_read_b128 v[198:201], v188 offset:51200
	ds_read_b128 v[202:205], v188 offset:52224
	ds_read_b128 v[206:209], v188 offset:53248
	ds_read_b128 v[210:213], v188 offset:54272
	ds_read_b128 v[214:217], v188 offset:55296
	ds_read_b128 v[218:221], v188 offset:56320
	global_load_lds_dwordx4 v[176:177], off
	s_add_i32 m0, s0, 0x2000
	s_add_u32 s4, s44, 0x20080
	v_lshl_add_u64 v[176:177], v[178:179], 0, s[14:15]
	s_addc_u32 s5, s45, 0
	s_add_i32 s0, s1, s52
	global_load_lds_dwordx4 v[176:177], off
	v_lshl_add_u64 v[176:177], s[4:5], 0, v[168:169]
	s_mov_b32 m0, s0
	s_nop 0
	global_load_lds_dwordx4 v[176:177], off
	v_lshl_add_u64 v[176:177], s[4:5], 0, v[164:165]
	s_add_i32 m0, s0, 0x2000
	s_nop 0
	global_load_lds_dwordx4 v[176:177], off
	v_lshl_add_u64 v[176:177], v[180:181], 0, s[14:15]
	s_mov_b32 m0, s60
	s_nop 0
	global_load_lds_dwordx4 v[176:177], off
	v_lshl_add_u64 v[176:177], v[182:183], 0, s[14:15]
	s_mov_b32 m0, s61
	s_nop 0
	global_load_lds_dwordx4 v[176:177], off
	s_waitcnt vmcnt(8)
	s_waitcnt lgkmcnt(0)
	s_barrier
	s_setprio 3
	s_waitcnt lgkmcnt(0)
	v_mfma_f32_16x16x128_f8f6f4 v[94:97], v[2:9], v[190:197], v[94:97]
	v_mfma_f32_16x16x128_f8f6f4 v[86:89], v[10:17], v[190:197], v[86:89]
	v_mfma_f32_16x16x128_f8f6f4 v[78:81], v[2:9], v[198:205], v[78:81]
	v_mfma_f32_16x16x128_f8f6f4 v[70:73], v[10:17], v[198:205], v[70:73]
	v_mfma_f32_16x16x128_f8f6f4 v[62:65], v[2:9], v[206:213], v[62:65]
	v_mfma_f32_16x16x128_f8f6f4 v[54:57], v[10:17], v[206:213], v[54:57]
	v_mfma_f32_16x16x128_f8f6f4 v[46:49], v[2:9], v[214:221], v[46:49]
	v_mfma_f32_16x16x128_f8f6f4 v[38:41], v[10:17], v[214:221], v[38:41]
	s_setprio 0
	s_setprio 3
	v_mfma_f32_16x16x128_f8f6f4 v[90:93], v[18:25], v[190:197], v[90:93]
	v_mfma_f32_16x16x128_f8f6f4 v[82:85], v[26:33], v[190:197], v[82:85]
	v_mfma_f32_16x16x128_f8f6f4 v[74:77], v[18:25], v[198:205], v[74:77]
	v_mfma_f32_16x16x128_f8f6f4 v[66:69], v[26:33], v[198:205], v[66:69]
	v_mfma_f32_16x16x128_f8f6f4 v[58:61], v[18:25], v[206:213], v[58:61]
	v_mfma_f32_16x16x128_f8f6f4 v[50:53], v[26:33], v[206:213], v[50:53]
	v_mfma_f32_16x16x128_f8f6f4 v[42:45], v[18:25], v[214:221], v[42:45]
	v_mfma_f32_16x16x128_f8f6f4 v[34:37], v[26:33], v[214:221], v[34:37]
	s_setprio 0
	s_barrier
	s_add_i32 s81, s81, 2
	s_add_u32 s42, s42, 0x100
	s_addc_u32 s43, s43, 0
	s_add_u32 s79, s79, 0x100
	s_addc_u32 s80, s80, 0
	s_cmp_gt_u32 s81, 5
	s_cbranch_scc0 .LBB0_1310

; #define PG8_STAGE(bufoff, gbase, voff) do { _Pragma("unroll") for (int _i = 0; _i < 2; ++_i) \
;         __builtin_amdgcn_global_load_lds((const unsigned*)((const char*)(gbase) + (voff)[_i]), (PG8_LAS unsigned*)(lds + (bufoff) + ldsw + _i * 8192), 16, 0, 0); } while (0)
; #define PG8_LDA(dst, b, h) do { _Pragma("unroll") for (int m = 0; m < 4; ++m) Frag<F8>::load(dst[m], lds + PG8_SA(b, h) + aoff + m * 2048); } while (0)
; template <class Epi, class Sched, bool ALIGN_EPI = false, bool SP2 = false, bool F8 = false>
; __device__ __forceinline__ void gemm_phase(PG8_LAS unsigned char* lds, const Gemm g, const Sched& S, const Epi& E) {
;     ...
;     for (;;) {
;         const bool has_next = S.next(ui + 1, nxt);
;         const char* nA = has_next ? (const char*)g.A + (size_t)nxt.pm * tstep + nxt.ko : cA; const char* nB = has_next ? (const char*)g.Bt + (size_t)nxt.pn * tstep + nxt.ko : cB;
;         for (int t = 0; t < nt; t += 2) {
;             const bool last = (t == nt - 2);
;             const char* a1 = cA + (size_t)(t + 1) * kstep;
;             const char* a2 = last ? nA : cA + (size_t)(t + 2) * kstep; const char* b2 = last ? nB : cB + (size_t)(t + 2) * kstep;
;             const char* a3 = a2 + kstep; const char* b3 = b2 + kstep;
;             if (last && has_next) S.a_ready(nxt);
;             if constexpr (SP2) {
;             PG8_LDB(B0, 0, 0); PG8_LDB(B1, 0, 1); PG8_SCHED; PG8_LDA(At, 0, 0); PG8_STAGE(PG8_SA(1, 1), a1 + hstep, voffA);
;             PG8_WAIT_V(8); PG8_WAIT_L(0); PG8_BAR; PG8_MMA(0, 0, At, B0); PG8_MMA(0, 1, At, B1); PG8_BAR; PG8_SCHED;
;             PG8_LDA(At, 0, 1); PG8_STAGE(PG8_SB(0, 0), b2, voffB); PG8_STAGE(PG8_SB(0, 1), b2 + hstep, voffB); PG8_STAGE(PG8_SA(0, 0), a2, voffA);
;             PG8_WAIT_V(8); PG8_WAIT_L(0); PG8_BAR; PG8_MMA(1, 0, At, B0); PG8_MMA(1, 1, At, B1); PG8_BAR; PG8_SCHED;
;             PG8_LDB(B0, 1, 0); PG8_LDB(B1, 1, 1); PG8_SCHED; PG8_LDA(At, 1, 0); PG8_STAGE(PG8_SA(0, 1), a2 + hstep, voffA);
;             PG8_WAIT_V(8); PG8_WAIT_L(0); PG8_BAR; PG8_MMA(0, 0, At, B0); PG8_MMA(0, 1, At, B1); PG8_BAR; PG8_SCHED;
;             PG8_LDA(At, 1, 1); PG8_STAGE(PG8_SB(1, 0), b3, voffB); PG8_STAGE(PG8_SB(1, 1), b3 + hstep, voffB); PG8_STAGE(PG8_SA(1, 0), a3, voffA);
;             PG8_WAIT_V(8); PG8_WAIT_L(0); PG8_BAR; PG8_MMA(1, 0, At, B0); PG8_MMA(1, 1, At, B1); PG8_BAR; PG8_SCHED;
.LBB0_1391:
	v_lshl_add_u64 v[180:181], v[2:3], 0, s[24:25]
	s_mov_b32 s76, -2
	ds_read_b128 v[18:21], v192
	ds_read_b128 v[22:25], v192 offset:1024
	ds_read_b128 v[26:29], v192 offset:2048
	ds_read_b128 v[30:33], v192 offset:3072
	ds_read_b128 v[2:5], v193
	ds_read_b128 v[6:9], v193 offset:1024
	ds_read_b128 v[10:13], v193 offset:2048
	ds_read_b128 v[14:17], v193 offset:3072
	s_add_u32 s30, s36, 0x100
	s_addc_u32 s31, s37, 0
	s_cmp_eq_u32 s76, 24
	s_cselect_b64 vcc, -1, 0
	s_cselect_b32 s39, s27, s31
	s_cselect_b32 s38, s26, s30
	v_cndmask_b32_e32 v183, v181, v179, vcc
	v_cndmask_b32_e32 v182, v180, v178, vcc
	s_mov_b32 m0, s56
	v_lshl_add_u64 v[224:225], s[36:37], 0, v[174:175]
	ds_read_b128 v[184:187], v194
	ds_read_b128 v[188:191], v194 offset:1024
	ds_read_b128 v[200:203], v194 offset:2048
	ds_read_b128 v[204:207], v194 offset:3072
	ds_read_b128 v[208:211], v194 offset:4096
	ds_read_b128 v[212:215], v194 offset:5120
	ds_read_b128 v[216:219], v194 offset:6144
	ds_read_b128 v[220:223], v194 offset:7168
	global_load_lds_dwordx4 v[224:225], off
	v_lshl_add_u64 v[224:225], s[36:37], 0, v[176:177]
	s_mov_b32 m0, s57
	s_nop 0
	global_load_lds_dwordx4 v[224:225], off
	s_waitcnt vmcnt(8)
	s_waitcnt lgkmcnt(0)
	s_barrier
	s_setprio 3
	s_waitcnt lgkmcnt(0)
	v_mfma_f32_16x16x128_f8f6f4 v[158:161], v[18:25], v[184:191], 0
	v_mfma_f32_16x16x128_f8f6f4 v[154:157], v[26:33], v[184:191], 0
	v_mfma_f32_16x16x128_f8f6f4 v[142:145], v[18:25], v[200:207], 0
	v_mfma_f32_16x16x128_f8f6f4 v[138:141], v[26:33], v[200:207], 0
	v_mfma_f32_16x16x128_f8f6f4 v[126:129], v[18:25], v[208:215], 0
	v_mfma_f32_16x16x128_f8f6f4 v[122:125], v[26:33], v[208:215], 0
	v_mfma_f32_16x16x128_f8f6f4 v[110:113], v[18:25], v[216:223], 0
	v_mfma_f32_16x16x128_f8f6f4 v[106:109], v[26:33], v[216:223], 0
	s_setprio 0
	s_setprio 3
	v_mfma_f32_16x16x128_f8f6f4 v[150:153], v[2:9], v[184:191], 0
	v_mfma_f32_16x16x128_f8f6f4 v[146:149], v[10:17], v[184:191], 0
	v_mfma_f32_16x16x128_f8f6f4 v[134:137], v[2:9], v[200:207], 0
	v_mfma_f32_16x16x128_f8f6f4 v[130:133], v[10:17], v[200:207], 0
	v_mfma_f32_16x16x128_f8f6f4 v[118:121], v[2:9], v[208:215], 0
	v_mfma_f32_16x16x128_f8f6f4 v[114:117], v[10:17], v[208:215], 0
	v_mfma_f32_16x16x128_f8f6f4 v[102:105], v[2:9], v[216:223], 0
	v_mfma_f32_16x16x128_f8f6f4 v[98:101], v[10:17], v[216:223], 0
	s_setprio 0
	s_barrier
	s_mov_b32 m0, s58
	v_lshl_add_u64 v[184:185], v[182:183], 0, v[166:167]
	ds_read_b128 v[200:203], v194 offset:16384
	ds_read_b128 v[204:207], v194 offset:17408
	ds_read_b128 v[208:211], v194 offset:18432
	ds_read_b128 v[212:215], v194 offset:19456
	ds_read_b128 v[216:219], v194 offset:20480
	ds_read_b128 v[220:223], v194 offset:21504
	ds_read_b128 v[224:227], v194 offset:22528
	ds_read_b128 v[228:231], v194 offset:23552
	global_load_lds_dwordx4 v[184:185], off
	v_lshl_add_u64 v[186:187], v[182:183], 0, v[170:171]
	s_mov_b32 m0, s59
	v_lshl_add_u64 v[188:189], v[182:183], 0, s[10:11]
	global_load_lds_dwordx4 v[186:187], off
	v_lshl_add_u64 v[190:191], v[188:189], 0, v[166:167]
	s_mov_b32 m0, s60
	v_lshl_add_u64 v[188:189], v[188:189], 0, v[170:171]
	global_load_lds_dwordx4 v[190:191], off
	s_mov_b32 m0, s61
	v_lshl_add_u64 v[190:191], s[38:39], 0, v[168:169]
	global_load_lds_dwordx4 v[188:189], off
	v_lshl_add_u64 v[188:189], s[38:39], 0, v[164:165]
	s_mov_b32 m0, s45
	s_nop 0
	global_load_lds_dwordx4 v[188:189], off
	s_mov_b32 m0, s46
	s_nop 0
	global_load_lds_dwordx4 v[190:191], off
	s_waitcnt vmcnt(8)
	s_waitcnt lgkmcnt(0)
	s_barrier
	s_setprio 3
	s_waitcnt lgkmcnt(0)
	v_mfma_f32_16x16x128_f8f6f4 v[94:97], v[18:25], v[200:207], 0
	v_mfma_f32_16x16x128_f8f6f4 v[90:93], v[26:33], v[200:207], 0
	v_mfma_f32_16x16x128_f8f6f4 v[78:81], v[18:25], v[208:215], 0
	v_mfma_f32_16x16x128_f8f6f4 v[74:77], v[26:33], v[208:215], 0
	v_mfma_f32_16x16x128_f8f6f4 v[62:65], v[18:25], v[216:223], 0
	v_mfma_f32_16x16x128_f8f6f4 v[58:61], v[26:33], v[216:223], 0
	v_mfma_f32_16x16x128_f8f6f4 v[46:49], v[18:25], v[224:231], 0
	v_mfma_f32_16x16x128_f8f6f4 v[42:45], v[26:33], v[224:231], 0
	s_setprio 0
	s_setprio 3
	v_mfma_f32_16x16x128_f8f6f4 v[86:89], v[2:9], v[200:207], 0
	v_mfma_f32_16x16x128_f8f6f4 v[82:85], v[10:17], v[200:207], 0
	v_mfma_f32_16x16x128_f8f6f4 v[70:73], v[2:9], v[208:215], 0
	v_mfma_f32_16x16x128_f8f6f4 v[66:69], v[10:17], v[208:215], 0
	v_mfma_f32_16x16x128_f8f6f4 v[54:57], v[2:9], v[216:223], 0
	v_mfma_f32_16x16x128_f8f6f4 v[50:53], v[10:17], v[216:223], 0
	v_mfma_f32_16x16x128_f8f6f4 v[38:41], v[2:9], v[224:231], 0
	v_mfma_f32_16x16x128_f8f6f4 v[34:37], v[10:17], v[224:231], 0
	s_setprio 0
	s_barrier
	ds_read_b128 v[2:5], v196
	ds_read_b128 v[6:9], v196 offset:1024
	ds_read_b128 v[10:13], v196 offset:2048
	ds_read_b128 v[14:17], v196 offset:3072
	ds_read_b128 v[18:21], v197
	ds_read_b128 v[22:25], v197 offset:1024
	ds_read_b128 v[26:29], v197 offset:2048
	ds_read_b128 v[30:33], v197 offset:3072
	s_add_u32 s4, s38, 0x70000
	s_addc_u32 s5, s39, 0
	s_mov_b32 m0, s47
	v_lshl_add_u64 v[232:233], s[4:5], 0, v[164:165]
	ds_read_b128 v[200:203], v194 offset:32768
	ds_read_b128 v[204:207], v194 offset:33792
	ds_read_b128 v[208:211], v194 offset:34816
	ds_read_b128 v[212:215], v194 offset:35840
	ds_read_b128 v[216:219], v194 offset:36864
	ds_read_b128 v[220:223], v194 offset:37888
	ds_read_b128 v[224:227], v194 offset:38912
	ds_read_b128 v[228:231], v194 offset:39936
	global_load_lds_dwordx4 v[232:233], off
	v_lshl_add_u64 v[232:233], s[4:5], 0, v[168:169]
	s_mov_b32 m0, s48
	s_nop 0
	global_load_lds_dwordx4 v[232:233], off
	s_waitcnt vmcnt(8)
	s_waitcnt lgkmcnt(0)
	s_barrier
; #define PG8_STAGE(bufoff, gbase, voff) do { _Pragma("unroll") for (int _i = 0; _i < 2; ++_i) \
;         __builtin_amdgcn_global_load_lds((const unsigned*)((const char*)(gbase) + (voff)[_i]), (PG8_LAS unsigned*)(lds + (bufoff) + ldsw + _i * 8192), 16, 0, 0); } while (0)
; #define PG8_LDA(dst, b, h) do { _Pragma("unroll") for (int m = 0; m < 4; ++m) Frag<F8>::load(dst[m], lds + PG8_SA(b, h) + aoff + m * 2048); } while (0)
; #define PG8_LDB(dst, b, h) do { _Pragma("unroll") for (int n = 0; n < 2; ++n) Frag<F8>::load(dst[n], lds + PG8_SB(b, h) + boff + n * 2048); } while (0)
; #define PG8_MMA(ai, bj, At, Bt) do { __builtin_amdgcn_s_setprio(3); _Pragma("unroll") for (int m = 0; m < 4; ++m) _Pragma("unroll") for (int n = 0; n < 2; ++n) Frag<F8>::mma(acc[ai][bj][m][n], Bt[n], At[m]); \
;         __builtin_amdgcn_s_setprio(0); } while (0)
; #define PG8_WAIT_V(n) asm volatile("s_waitcnt vmcnt(" #n ")" ::: "memory")
; #define PG8_WAIT_L(n) asm volatile("s_waitcnt lgkmcnt(" #n ")" ::: "memory")
; #define PG8_BAR __builtin_amdgcn_s_barrier()
; #define PG8_SCHED __builtin_amdgcn_sched_barrier(0)
; template <class Epi, class Sched, bool ALIGN_EPI = false, bool SP2 = false, bool F8 = false>
; __device__ __forceinline__ void gemm_phase(PG8_LAS unsigned char* lds, const Gemm g, const Sched& S, const Epi& E) {
;     ...
;             PG8_LDB(B0, 0, 0); PG8_LDB(B1, 0, 1); PG8_SCHED; PG8_LDA(At, 0, 0); PG8_STAGE(PG8_SA(1, 1), a1 + hstep, voffA);
;             PG8_WAIT_V(8); PG8_WAIT_L(0); PG8_BAR; PG8_MMA(0, 0, At, B0); PG8_MMA(0, 1, At, B1); PG8_BAR; PG8_SCHED;
;             PG8_LDA(At, 0, 1); PG8_STAGE(PG8_SB(0, 0), b2, voffB); PG8_STAGE(PG8_SB(0, 1), b2 + hstep, voffB); PG8_STAGE(PG8_SA(0, 0), a2, voffA);
;             PG8_WAIT_V(8); PG8_WAIT_L(0); PG8_BAR; PG8_MMA(1, 0, At, B0); PG8_MMA(1, 1, At, B1); PG8_BAR; PG8_SCHED;
;             PG8_LDB(B0, 1, 0); PG8_LDB(B1, 1, 1); PG8_SCHED; PG8_LDA(At, 1, 0); PG8_STAGE(PG8_SA(0, 1), a2 + hstep, voffA);
;             PG8_WAIT_V(8); PG8_WAIT_L(0); PG8_BAR; PG8_MMA(0, 0, At, B0); PG8_MMA(0, 1, At, B1); PG8_BAR; PG8_SCHED;
;             PG8_LDA(At, 1, 1); PG8_STAGE(PG8_SB(1, 0), b3, voffB); PG8_STAGE(PG8_SB(1, 1), b3 + hstep, voffB); PG8_STAGE(PG8_SA(1, 0), a3, voffA);
;             PG8_WAIT_V(8); PG8_WAIT_L(0); PG8_BAR; PG8_MMA(1, 0, At, B0); PG8_MMA(1, 1, At, B1); PG8_BAR; PG8_SCHED;
	s_setprio 3
	s_waitcnt lgkmcnt(0)
	v_mfma_f32_16x16x128_f8f6f4 v[158:161], v[2:9], v[200:207], v[158:161]
	v_mfma_f32_16x16x128_f8f6f4 v[154:157], v[10:17], v[200:207], v[154:157]
	v_mfma_f32_16x16x128_f8f6f4 v[142:145], v[2:9], v[208:215], v[142:145]
	v_mfma_f32_16x16x128_f8f6f4 v[138:141], v[10:17], v[208:215], v[138:141]
	v_mfma_f32_16x16x128_f8f6f4 v[126:129], v[2:9], v[216:223], v[126:129]
	v_mfma_f32_16x16x128_f8f6f4 v[122:125], v[10:17], v[216:223], v[122:125]
	v_mfma_f32_16x16x128_f8f6f4 v[110:113], v[2:9], v[224:231], v[110:113]
	v_mfma_f32_16x16x128_f8f6f4 v[106:109], v[10:17], v[224:231], v[106:109]
	s_setprio 0
	s_setprio 3
	v_mfma_f32_16x16x128_f8f6f4 v[150:153], v[18:25], v[200:207], v[150:153]
	v_mfma_f32_16x16x128_f8f6f4 v[146:149], v[26:33], v[200:207], v[146:149]
	v_mfma_f32_16x16x128_f8f6f4 v[134:137], v[18:25], v[208:215], v[134:137]
	v_mfma_f32_16x16x128_f8f6f4 v[130:133], v[26:33], v[208:215], v[130:133]
	v_mfma_f32_16x16x128_f8f6f4 v[118:121], v[18:25], v[216:223], v[118:121]
	v_mfma_f32_16x16x128_f8f6f4 v[114:117], v[26:33], v[216:223], v[114:117]
	v_mfma_f32_16x16x128_f8f6f4 v[102:105], v[18:25], v[224:231], v[102:105]
	v_mfma_f32_16x16x128_f8f6f4 v[98:101], v[26:33], v[224:231], v[98:101]
	s_setprio 0
	s_barrier
	s_mov_b32 m0, s67
	v_lshl_add_u64 v[184:185], v[184:185], 0, s[18:19]
	ds_read_b128 v[200:203], v194 offset:49152
	ds_read_b128 v[204:207], v194 offset:50176
	ds_read_b128 v[208:211], v194 offset:51200
	ds_read_b128 v[212:215], v194 offset:52224
	ds_read_b128 v[216:219], v194 offset:53248
	ds_read_b128 v[220:223], v194 offset:54272
	ds_read_b128 v[224:227], v194 offset:55296
	ds_read_b128 v[228:231], v194 offset:56320
	global_load_lds_dwordx4 v[184:185], off
	v_lshl_add_u64 v[184:185], v[186:187], 0, s[18:19]
	s_mov_b32 m0, s70
	v_lshl_add_u64 v[182:183], v[182:183], 0, s[20:21]
	global_load_lds_dwordx4 v[184:185], off
	v_lshl_add_u64 v[184:185], v[182:183], 0, v[166:167]
	s_mov_b32 m0, s71
	v_lshl_add_u64 v[182:183], v[182:183], 0, v[170:171]
	global_load_lds_dwordx4 v[184:185], off
	s_mov_b32 m0, s72
	s_nop 0
	global_load_lds_dwordx4 v[182:183], off
	v_lshl_add_u64 v[182:183], v[188:189], 0, s[18:19]
	s_mov_b32 m0, s49
	s_nop 0
	global_load_lds_dwordx4 v[182:183], off
	v_lshl_add_u64 v[182:183], v[190:191], 0, s[18:19]
	s_mov_b32 m0, s50
	s_nop 0
	global_load_lds_dwordx4 v[182:183], off
	s_waitcnt vmcnt(8)
	s_waitcnt lgkmcnt(0)
	s_barrier
	s_setprio 3
	s_waitcnt lgkmcnt(0)
	v_mfma_f32_16x16x128_f8f6f4 v[94:97], v[2:9], v[200:207], v[94:97]
	v_mfma_f32_16x16x128_f8f6f4 v[90:93], v[10:17], v[200:207], v[90:93]
	v_mfma_f32_16x16x128_f8f6f4 v[78:81], v[2:9], v[208:215], v[78:81]
	v_mfma_f32_16x16x128_f8f6f4 v[74:77], v[10:17], v[208:215], v[74:77]
	v_mfma_f32_16x16x128_f8f6f4 v[62:65], v[2:9], v[216:223], v[62:65]
	v_mfma_f32_16x16x128_f8f6f4 v[58:61], v[10:17], v[216:223], v[58:61]
	v_mfma_f32_16x16x128_f8f6f4 v[46:49], v[2:9], v[224:231], v[46:49]
	v_mfma_f32_16x16x128_f8f6f4 v[42:45], v[10:17], v[224:231], v[42:45]
	s_setprio 0
	s_setprio 3
	v_mfma_f32_16x16x128_f8f6f4 v[86:89], v[18:25], v[200:207], v[86:89]
	v_mfma_f32_16x16x128_f8f6f4 v[82:85], v[26:33], v[200:207], v[82:85]
	v_mfma_f32_16x16x128_f8f6f4 v[70:73], v[18:25], v[208:215], v[70:73]
	v_mfma_f32_16x16x128_f8f6f4 v[66:69], v[26:33], v[208:215], v[66:69]
	v_mfma_f32_16x16x128_f8f6f4 v[54:57], v[18:25], v[216:223], v[54:57]
	v_mfma_f32_16x16x128_f8f6f4 v[50:53], v[26:33], v[216:223], v[50:53]
	v_mfma_f32_16x16x128_f8f6f4 v[38:41], v[18:25], v[224:231], v[38:41]
	v_mfma_f32_16x16x128_f8f6f4 v[34:37], v[26:33], v[224:231], v[34:37]
	s_setprio 0
	s_barrier
	s_add_i32 s76, s76, 2
	v_lshl_add_u64 v[180:181], v[180:181], 0, s[24:25]
	s_cmp_gt_u32 s76, 25
	s_mov_b64 s[36:37], s[30:31]
	s_cbranch_scc1 .Lpeel_exit_4
.LBB0_1392:
	ds_read_b128 v[18:21], v192
	ds_read_b128 v[22:25], v192 offset:1024
	ds_read_b128 v[26:29], v192 offset:2048
	ds_read_b128 v[30:33], v192 offset:3072
	ds_read_b128 v[2:5], v193
	ds_read_b128 v[6:9], v193 offset:1024
	ds_read_b128 v[10:13], v193 offset:2048
	ds_read_b128 v[14:17], v193 offset:3072
	s_add_u32 s30, s36, 0x100
	s_addc_u32 s31, s37, 0
	s_cmp_eq_u32 s76, 24
	s_cselect_b64 vcc, -1, 0
	s_cselect_b32 s39, s27, s31
	s_cselect_b32 s38, s26, s30
	v_cndmask_b32_e32 v183, v181, v179, vcc
	v_cndmask_b32_e32 v182, v180, v178, vcc
	s_mov_b32 m0, s56
	v_lshl_add_u64 v[224:225], s[36:37], 0, v[174:175]
	ds_read_b128 v[184:187], v194
	ds_read_b128 v[188:191], v194 offset:1024
	ds_read_b128 v[200:203], v194 offset:2048
	ds_read_b128 v[204:207], v194 offset:3072
	ds_read_b128 v[208:211], v194 offset:4096
	ds_read_b128 v[212:215], v194 offset:5120
	ds_read_b128 v[216:219], v194 offset:6144
	ds_read_b128 v[220:223], v194 offset:7168
	global_load_lds_dwordx4 v[224:225], off
	v_lshl_add_u64 v[224:225], s[36:37], 0, v[176:177]
	s_mov_b32 m0, s57
	s_nop 0
	global_load_lds_dwordx4 v[224:225], off
	s_waitcnt vmcnt(8)
	s_waitcnt lgkmcnt(0)
	s_barrier
	s_setprio 3
	s_waitcnt lgkmcnt(0)
	v_mfma_f32_16x16x128_f8f6f4 v[158:161], v[18:25], v[184:191], v[158:161]
	v_mfma_f32_16x16x128_f8f6f4 v[154:157], v[26:33], v[184:191], v[154:157]
	v_mfma_f32_16x16x128_f8f6f4 v[142:145], v[18:25], v[200:207], v[142:145]
	v_mfma_f32_16x16x128_f8f6f4 v[138:141], v[26:33], v[200:207], v[138:141]
	v_mfma_f32_16x16x128_f8f6f4 v[126:129], v[18:25], v[208:215], v[126:129]
	v_mfma_f32_16x16x128_f8f6f4 v[122:125], v[26:33], v[208:215], v[122:125]
	v_mfma_f32_16x16x128_f8f6f4 v[110:113], v[18:25], v[216:223], v[110:113]
	v_mfma_f32_16x16x128_f8f6f4 v[106:109], v[26:33], v[216:223], v[106:109]
	s_setprio 0
	s_setprio 3
	v_mfma_f32_16x16x128_f8f6f4 v[150:153], v[2:9], v[184:191], v[150:153]
	v_mfma_f32_16x16x128_f8f6f4 v[146:149], v[10:17], v[184:191], v[146:149]
	v_mfma_f32_16x16x128_f8f6f4 v[134:137], v[2:9], v[200:207], v[134:137]
	v_mfma_f32_16x16x128_f8f6f4 v[130:133], v[10:17], v[200:207], v[130:133]
	v_mfma_f32_16x16x128_f8f6f4 v[118:121], v[2:9], v[208:215], v[118:121]
	v_mfma_f32_16x16x128_f8f6f4 v[114:117], v[10:17], v[208:215], v[114:117]
	v_mfma_f32_16x16x128_f8f6f4 v[102:105], v[2:9], v[216:223], v[102:105]
	v_mfma_f32_16x16x128_f8f6f4 v[98:101], v[10:17], v[216:223], v[98:101]
	s_setprio 0
	s_barrier
; #define PG8_STAGE(bufoff, gbase, voff) do { _Pragma("unroll") for (int _i = 0; _i < 2; ++_i) \
;         __builtin_amdgcn_global_load_lds((const unsigned*)((const char*)(gbase) + (voff)[_i]), (PG8_LAS unsigned*)(lds + (bufoff) + ldsw + _i * 8192), 16, 0, 0); } while (0)
; #define PG8_LDA(dst, b, h) do { _Pragma("unroll") for (int m = 0; m < 4; ++m) Frag<F8>::load(dst[m], lds + PG8_SA(b, h) + aoff + m * 2048); } while (0)
; #define PG8_LDB(dst, b, h) do { _Pragma("unroll") for (int n = 0; n < 2; ++n) Frag<F8>::load(dst[n], lds + PG8_SB(b, h) + boff + n * 2048); } while (0)
; #define PG8_MMA(ai, bj, At, Bt) do { __builtin_amdgcn_s_setprio(3); _Pragma("unroll") for (int m = 0; m < 4; ++m) _Pragma("unroll") for (int n = 0; n < 2; ++n) Frag<F8>::mma(acc[ai][bj][m][n], Bt[n], At[m]); \
;         __builtin_amdgcn_s_setprio(0); } while (0)
; #define PG8_WAIT_V(n) asm volatile("s_waitcnt vmcnt(" #n ")" ::: "memory")
; #define PG8_WAIT_L(n) asm volatile("s_waitcnt lgkmcnt(" #n ")" ::: "memory")
; #define PG8_BAR __builtin_amdgcn_s_barrier()
; #define PG8_SCHED __builtin_amdgcn_sched_barrier(0)
; template <class Epi, class Sched, bool ALIGN_EPI = false, bool SP2 = false, bool F8 = false>
; __device__ __forceinline__ void gemm_phase(PG8_LAS unsigned char* lds, const Gemm g, const Sched& S, const Epi& E) {
;     ...
;             PG8_LDB(B0, 1, 0); PG8_LDB(B1, 1, 1); PG8_SCHED; PG8_LDA(At, 1, 0); PG8_STAGE(PG8_SA(0, 1), a2 + hstep, voffA);
;             PG8_WAIT_V(8); PG8_WAIT_L(0); PG8_BAR; PG8_MMA(0, 0, At, B0); PG8_MMA(0, 1, At, B1); PG8_BAR; PG8_SCHED;
;             PG8_LDA(At, 1, 1); PG8_STAGE(PG8_SB(1, 0), b3, voffB); PG8_STAGE(PG8_SB(1, 1), b3 + hstep, voffB); PG8_STAGE(PG8_SA(1, 0), a3, voffA);
	s_mov_b32 m0, s58
	v_lshl_add_u64 v[184:185], v[182:183], 0, v[166:167]
	ds_read_b128 v[200:203], v194 offset:16384
	ds_read_b128 v[204:207], v194 offset:17408
	ds_read_b128 v[208:211], v194 offset:18432
	ds_read_b128 v[212:215], v194 offset:19456
	ds_read_b128 v[216:219], v194 offset:20480
	ds_read_b128 v[220:223], v194 offset:21504
	ds_read_b128 v[224:227], v194 offset:22528
	ds_read_b128 v[228:231], v194 offset:23552
	global_load_lds_dwordx4 v[184:185], off
	v_lshl_add_u64 v[186:187], v[182:183], 0, v[170:171]
	s_mov_b32 m0, s59
	v_lshl_add_u64 v[188:189], v[182:183], 0, s[10:11]
	global_load_lds_dwordx4 v[186:187], off
	v_lshl_add_u64 v[190:191], v[188:189], 0, v[166:167]
	s_mov_b32 m0, s60
	v_lshl_add_u64 v[188:189], v[188:189], 0, v[170:171]
	global_load_lds_dwordx4 v[190:191], off
	s_mov_b32 m0, s61
	v_lshl_add_u64 v[190:191], s[38:39], 0, v[168:169]
	global_load_lds_dwordx4 v[188:189], off
	v_lshl_add_u64 v[188:189], s[38:39], 0, v[164:165]
	s_mov_b32 m0, s45
	s_nop 0
	global_load_lds_dwordx4 v[188:189], off
	s_mov_b32 m0, s46
	s_nop 0
	global_load_lds_dwordx4 v[190:191], off
	s_waitcnt vmcnt(8)
	s_waitcnt lgkmcnt(0)
	s_barrier
	s_setprio 3
	s_waitcnt lgkmcnt(0)
	v_mfma_f32_16x16x128_f8f6f4 v[94:97], v[18:25], v[200:207], v[94:97]
	v_mfma_f32_16x16x128_f8f6f4 v[90:93], v[26:33], v[200:207], v[90:93]
	v_mfma_f32_16x16x128_f8f6f4 v[78:81], v[18:25], v[208:215], v[78:81]
	v_mfma_f32_16x16x128_f8f6f4 v[74:77], v[26:33], v[208:215], v[74:77]
	v_mfma_f32_16x16x128_f8f6f4 v[62:65], v[18:25], v[216:223], v[62:65]
	v_mfma_f32_16x16x128_f8f6f4 v[58:61], v[26:33], v[216:223], v[58:61]
	v_mfma_f32_16x16x128_f8f6f4 v[46:49], v[18:25], v[224:231], v[46:49]
	v_mfma_f32_16x16x128_f8f6f4 v[42:45], v[26:33], v[224:231], v[42:45]
	s_setprio 0
	s_setprio 3
	v_mfma_f32_16x16x128_f8f6f4 v[86:89], v[2:9], v[200:207], v[86:89]
	v_mfma_f32_16x16x128_f8f6f4 v[82:85], v[10:17], v[200:207], v[82:85]
	v_mfma_f32_16x16x128_f8f6f4 v[70:73], v[2:9], v[208:215], v[70:73]
	v_mfma_f32_16x16x128_f8f6f4 v[66:69], v[10:17], v[208:215], v[66:69]
	v_mfma_f32_16x16x128_f8f6f4 v[54:57], v[2:9], v[216:223], v[54:57]
	v_mfma_f32_16x16x128_f8f6f4 v[50:53], v[10:17], v[216:223], v[50:53]
	v_mfma_f32_16x16x128_f8f6f4 v[38:41], v[2:9], v[224:231], v[38:41]
	v_mfma_f32_16x16x128_f8f6f4 v[34:37], v[10:17], v[224:231], v[34:37]
	s_setprio 0
	s_barrier
	ds_read_b128 v[2:5], v196
	ds_read_b128 v[6:9], v196 offset:1024
	ds_read_b128 v[10:13], v196 offset:2048
	ds_read_b128 v[14:17], v196 offset:3072
	ds_read_b128 v[18:21], v197
	ds_read_b128 v[22:25], v197 offset:1024
	ds_read_b128 v[26:29], v197 offset:2048
	ds_read_b128 v[30:33], v197 offset:3072
	s_add_u32 s4, s38, 0x70000
	s_addc_u32 s5, s39, 0
	s_mov_b32 m0, s47
	v_lshl_add_u64 v[232:233], s[4:5], 0, v[164:165]
	ds_read_b128 v[200:203], v194 offset:32768
	ds_read_b128 v[204:207], v194 offset:33792
	ds_read_b128 v[208:211], v194 offset:34816
	ds_read_b128 v[212:215], v194 offset:35840
	ds_read_b128 v[216:219], v194 offset:36864
	ds_read_b128 v[220:223], v194 offset:37888
	ds_read_b128 v[224:227], v194 offset:38912
	ds_read_b128 v[228:231], v194 offset:39936
	global_load_lds_dwordx4 v[232:233], off
	v_lshl_add_u64 v[232:233], s[4:5], 0, v[168:169]
	s_mov_b32 m0, s48
	s_nop 0
	global_load_lds_dwordx4 v[232:233], off
	s_waitcnt vmcnt(8)
	s_waitcnt lgkmcnt(0)
	s_barrier
; #define PG8_STAGE(bufoff, gbase, voff) do { _Pragma("unroll") for (int _i = 0; _i < 2; ++_i) \
;         __builtin_amdgcn_global_load_lds((const unsigned*)((const char*)(gbase) + (voff)[_i]), (PG8_LAS unsigned*)(lds + (bufoff) + ldsw + _i * 8192), 16, 0, 0); } while (0)
; #define PG8_LDA(dst, b, h) do { _Pragma("unroll") for (int m = 0; m < 4; ++m) Frag<F8>::load(dst[m], lds + PG8_SA(b, h) + aoff + m * 2048); } while (0)
; #define PG8_MMA(ai, bj, At, Bt) do { __builtin_amdgcn_s_setprio(3); _Pragma("unroll") for (int m = 0; m < 4; ++m) _Pragma("unroll") for (int n = 0; n < 2; ++n) Frag<F8>::mma(acc[ai][bj][m][n], Bt[n], At[m]); \
;         __builtin_amdgcn_s_setprio(0); } while (0)
; #define PG8_WAIT_V(n) asm volatile("s_waitcnt vmcnt(" #n ")" ::: "memory")
; #define PG8_WAIT_L(n) asm volatile("s_waitcnt lgkmcnt(" #n ")" ::: "memory")
; #define PG8_BAR __builtin_amdgcn_s_barrier()
; #define PG8_SCHED __builtin_amdgcn_sched_barrier(0)
; template <class Epi, class Sched, bool ALIGN_EPI = false, bool SP2 = false, bool F8 = false>
; __device__ __forceinline__ void gemm_phase(PG8_LAS unsigned char* lds, const Gemm g, const Sched& S, const Epi& E) {
;     ...
;             PG8_LDA(At, 1, 1); PG8_STAGE(PG8_SB(1, 0), b3, voffB); PG8_STAGE(PG8_SB(1, 1), b3 + hstep, voffB); PG8_STAGE(PG8_SA(1, 0), a3, voffA);
;             PG8_WAIT_V(8); PG8_WAIT_L(0); PG8_BAR; PG8_MMA(1, 0, At, B0); PG8_MMA(1, 1, At, B1); PG8_BAR; PG8_SCHED;
	s_setprio 3
	s_waitcnt lgkmcnt(0)
	v_mfma_f32_16x16x128_f8f6f4 v[158:161], v[2:9], v[200:207], v[158:161]
	v_mfma_f32_16x16x128_f8f6f4 v[154:157], v[10:17], v[200:207], v[154:157]
	v_mfma_f32_16x16x128_f8f6f4 v[142:145], v[2:9], v[208:215], v[142:145]
	v_mfma_f32_16x16x128_f8f6f4 v[138:141], v[10:17], v[208:215], v[138:141]
	v_mfma_f32_16x16x128_f8f6f4 v[126:129], v[2:9], v[216:223], v[126:129]
	v_mfma_f32_16x16x128_f8f6f4 v[122:125], v[10:17], v[216:223], v[122:125]
	v_mfma_f32_16x16x128_f8f6f4 v[110:113], v[2:9], v[224:231], v[110:113]
	v_mfma_f32_16x16x128_f8f6f4 v[106:109], v[10:17], v[224:231], v[106:109]
	s_setprio 0
	s_setprio 3
	v_mfma_f32_16x16x128_f8f6f4 v[150:153], v[18:25], v[200:207], v[150:153]
	v_mfma_f32_16x16x128_f8f6f4 v[146:149], v[26:33], v[200:207], v[146:149]
	v_mfma_f32_16x16x128_f8f6f4 v[134:137], v[18:25], v[208:215], v[134:137]
	v_mfma_f32_16x16x128_f8f6f4 v[130:133], v[26:33], v[208:215], v[130:133]
	v_mfma_f32_16x16x128_f8f6f4 v[118:121], v[18:25], v[216:223], v[118:121]
	v_mfma_f32_16x16x128_f8f6f4 v[114:117], v[26:33], v[216:223], v[114:117]
	v_mfma_f32_16x16x128_f8f6f4 v[102:105], v[18:25], v[224:231], v[102:105]
	v_mfma_f32_16x16x128_f8f6f4 v[98:101], v[26:33], v[224:231], v[98:101]
	s_setprio 0
	s_barrier
	s_mov_b32 m0, s67
	v_lshl_add_u64 v[184:185], v[184:185], 0, s[18:19]
	ds_read_b128 v[200:203], v194 offset:49152
	ds_read_b128 v[204:207], v194 offset:50176
	ds_read_b128 v[208:211], v194 offset:51200
	ds_read_b128 v[212:215], v194 offset:52224
	ds_read_b128 v[216:219], v194 offset:53248
	ds_read_b128 v[220:223], v194 offset:54272
	ds_read_b128 v[224:227], v194 offset:55296
	ds_read_b128 v[228:231], v194 offset:56320
	global_load_lds_dwordx4 v[184:185], off
	v_lshl_add_u64 v[184:185], v[186:187], 0, s[18:19]
	s_mov_b32 m0, s70
	v_lshl_add_u64 v[182:183], v[182:183], 0, s[20:21]
	global_load_lds_dwordx4 v[184:185], off
	v_lshl_add_u64 v[184:185], v[182:183], 0, v[166:167]
	s_mov_b32 m0, s71
	v_lshl_add_u64 v[182:183], v[182:183], 0, v[170:171]
	global_load_lds_dwordx4 v[184:185], off
	s_mov_b32 m0, s72
	s_nop 0
	global_load_lds_dwordx4 v[182:183], off
	v_lshl_add_u64 v[182:183], v[188:189], 0, s[18:19]
	s_mov_b32 m0, s49
	s_nop 0
	global_load_lds_dwordx4 v[182:183], off
	v_lshl_add_u64 v[182:183], v[190:191], 0, s[18:19]
	s_mov_b32 m0, s50
	s_nop 0
	global_load_lds_dwordx4 v[182:183], off
	s_waitcnt vmcnt(8)
	s_waitcnt lgkmcnt(0)
	s_barrier
	s_setprio 3
	s_waitcnt lgkmcnt(0)
	v_mfma_f32_16x16x128_f8f6f4 v[94:97], v[2:9], v[200:207], v[94:97]
	v_mfma_f32_16x16x128_f8f6f4 v[90:93], v[10:17], v[200:207], v[90:93]
	v_mfma_f32_16x16x128_f8f6f4 v[78:81], v[2:9], v[208:215], v[78:81]
	v_mfma_f32_16x16x128_f8f6f4 v[74:77], v[10:17], v[208:215], v[74:77]
	v_mfma_f32_16x16x128_f8f6f4 v[62:65], v[2:9], v[216:223], v[62:65]
	v_mfma_f32_16x16x128_f8f6f4 v[58:61], v[10:17], v[216:223], v[58:61]
	v_mfma_f32_16x16x128_f8f6f4 v[46:49], v[2:9], v[224:231], v[46:49]
	v_mfma_f32_16x16x128_f8f6f4 v[42:45], v[10:17], v[224:231], v[42:45]
	s_setprio 0
	s_setprio 3
	v_mfma_f32_16x16x128_f8f6f4 v[86:89], v[18:25], v[200:207], v[86:89]
	v_mfma_f32_16x16x128_f8f6f4 v[82:85], v[26:33], v[200:207], v[82:85]
	v_mfma_f32_16x16x128_f8f6f4 v[70:73], v[18:25], v[208:215], v[70:73]
	v_mfma_f32_16x16x128_f8f6f4 v[66:69], v[26:33], v[208:215], v[66:69]
	v_mfma_f32_16x16x128_f8f6f4 v[54:57], v[18:25], v[216:223], v[54:57]
	v_mfma_f32_16x16x128_f8f6f4 v[50:53], v[26:33], v[216:223], v[50:53]
	v_mfma_f32_16x16x128_f8f6f4 v[38:41], v[18:25], v[224:231], v[38:41]
	v_mfma_f32_16x16x128_f8f6f4 v[34:37], v[26:33], v[224:231], v[34:37]
	s_setprio 0
	s_barrier
	s_add_i32 s76, s76, 2
	v_lshl_add_u64 v[180:181], v[180:181], 0, s[24:25]
	s_cmp_gt_u32 s76, 25
	s_mov_b64 s[36:37], s[30:31]
	s_cbranch_scc0 .LBB0_1392

; #define PG8_STAGE(bufoff, gbase, voff) do { _Pragma("unroll") for (int _i = 0; _i < 2; ++_i) \
;         __builtin_amdgcn_global_load_lds((const unsigned*)((const char*)(gbase) + (voff)[_i]), (PG8_LAS unsigned*)(lds + (bufoff) + ldsw + _i * 8192), 16, 0, 0); } while (0)
; #define PG8_LDA(dst, b, h) do { _Pragma("unroll") for (int m = 0; m < 4; ++m) Frag<F8>::load(dst[m], lds + PG8_SA(b, h) + aoff + m * 2048); } while (0)
; #define PG8_LDB(dst, b, h) do { _Pragma("unroll") for (int n = 0; n < 2; ++n) Frag<F8>::load(dst[n], lds + PG8_SB(b, h) + boff + n * 2048); } while (0)
; #define PG8_MMA(ai, bj, At, Bt) do { __builtin_amdgcn_s_setprio(3); _Pragma("unroll") for (int m = 0; m < 4; ++m) _Pragma("unroll") for (int n = 0; n < 2; ++n) Frag<F8>::mma(acc[ai][bj][m][n], Bt[n], At[m]); \
;         __builtin_amdgcn_s_setprio(0); } while (0)
; #define PG8_WAIT_V(n) asm volatile("s_waitcnt vmcnt(" #n ")" ::: "memory")
; #define PG8_BAR __builtin_amdgcn_s_barrier()
; template <class Epi, class Sched, bool ALIGN_EPI = false, bool SP2 = false, bool F8 = false>
; __device__ __forceinline__ void gemm_phase(PG8_LAS unsigned char* lds, const Gemm g, const Sched& S, const Epi& E) {
;     ...
;     for (int a = 0; a < 2; ++a)
; #pragma unroll
;         for (int b = 0; b < 2; ++b)
; #pragma unroll
;             for (int m = 0; m < 4; ++m)
; #pragma unroll
;                 for (int n = 0; n < 2; ++n) acc[a][b][m][n] = (f32x4){0.f, 0.f, 0.f, 0.f};
;     }
;     typename Frag<F8>::A At[4]; typename Frag<F8>::A B0[2], B1[2];
;     const char* cA = (const char*)g.A + (size_t)cur.pm * tstep + cur.ko; const char* cB = (const char*)g.Bt + (size_t)cur.pn * tstep + cur.ko;
;     S.a_ready(cur);
;     if constexpr (SP2) {
;         PG8_STAGE(PG8_SB(0, 0), cB, voffB); PG8_STAGE(PG8_SB(0, 1), cB + hstep, voffB); PG8_STAGE(PG8_SA(0, 0), cA, voffA); PG8_STAGE(PG8_SA(0, 1), cA + hstep, voffA);
;         if (wr == 1) PG8_BAR;
;         PG8_WAIT_V(2); PG8_BAR;
;         PG8_STAGE(PG8_SB(1, 0), cB + kstep, voffB); PG8_STAGE(PG8_SA(1, 0), cA + kstep, voffA); PG8_STAGE(PG8_SB(1, 1), cB + hstep + kstep, voffB);
;         PG8_WAIT_V(6); PG8_BAR;
;     ...
;             PG8_LDB(B0, 0, 0); PG8_LDB(B1, 0, 1); PG8_SCHED; PG8_LDA(At, 0, 0); PG8_STAGE(PG8_SA(1, 1), a1 + hstep, voffA);
;             PG8_WAIT_V(8); PG8_WAIT_L(0); PG8_BAR; PG8_MMA(0, 0, At, B0); PG8_MMA(0, 1, At, B1); PG8_BAR; PG8_SCHED;
.LBB0_1418:
	s_lshl_b32 s1, s15, 5
	s_add_i32 s15, 0, 0x18000
	s_and_b32 s27, s1, 0x60
	s_add_i32 s30, s15, s14
	s_mov_b64 s[8:9], 0x80
	s_lshl_b32 s0, s22, 13
	s_lshl_b32 s1, s27, 7
	v_lshl_add_u64 v[130:131], v[154:155], 0, s[8:9]
	s_mov_b32 m0, s30
	s_add_i32 s36, s30, 0x2000
	s_add_i32 s31, s4, 0x8000
	s_add_i32 s37, s4, 0xa000
	s_waitcnt vmcnt(2)
	s_barrier
	global_load_lds_dwordx4 v[130:131], off
	v_lshl_add_u64 v[132:133], v[156:157], 0, s[8:9]
	s_mov_b32 m0, s36
	v_lshl_add_u64 v[128:129], v[148:149], 0, s[8:9]
	v_lshl_add_u64 v[134:135], v[146:147], 0, s[8:9]
	s_add_u32 s8, s6, 0x70080
	global_load_lds_dwordx4 v[132:133], off
	s_mov_b32 m0, s31
	s_addc_u32 s9, s7, 0
	s_add_i32 s16, 0, 0x1c000
	global_load_lds_dwordx4 v[128:129], off
	s_mov_b32 m0, s37
	s_add_i32 s38, s16, s14
	global_load_lds_dwordx4 v[134:135], off
	v_lshl_add_u64 v[136:137], s[8:9], 0, v[158:159]
	s_mov_b32 m0, s38
	s_add_i32 s39, s38, 0x2000
	global_load_lds_dwordx4 v[136:137], off
	v_lshl_add_u64 v[138:139], s[8:9], 0, v[144:145]
	s_mov_b32 m0, s39
	v_and_b32_e32 v160, 15, v0
	global_load_lds_dwordx4 v[138:139], off
	v_bfe_u32 v161, v0, 4, 2
	v_lshlrev_b32_e32 v1, 6, v160
	v_lshlrev_b32_e32 v0, 2, v0
	v_lshl_or_b32 v1, v161, 4, v1
	v_and_b32_e32 v0, 32, v0
	v_bitop3_b32 v2, v1, s0, v0 bitop3:0xde
	v_bitop3_b32 v0, v1, s1, v0 bitop3:0xde
	s_add_i32 s42, 0, 0x10000
	s_add_i32 s44, 0, 0x14000
	v_add_u32_e32 v168, s42, v0
	s_add_u32 s20, s10, 0x70080
	s_waitcnt vmcnt(6)
	s_barrier
	v_add_u32_e32 v167, s44, v0
	s_addc_u32 s21, s11, 0
	s_add_i32 s42, s42, s14
	ds_read_b128 v[96:99], v168
	ds_read_b128 v[100:103], v168 offset:1024
	ds_read_b128 v[104:107], v168 offset:2048
	ds_read_b128 v[108:111], v168 offset:3072
	ds_read_b128 v[170:173], v167
	ds_read_b128 v[174:177], v167 offset:1024
	ds_read_b128 v[178:181], v167 offset:2048
	ds_read_b128 v[182:185], v167 offset:3072
	s_add_i32 s46, s4, 0xc000
	s_add_i32 s45, s4, 0xe000
	s_add_i32 s41, s42, 0x2000
	s_add_u32 s18, s6, 0x70100
	s_addc_u32 s19, s7, 0
	s_add_i32 s44, s44, s14
	s_add_i32 s43, s44, 0x2000
	v_add_u32_e32 v165, s16, v0
	s_add_u32 s16, s10, 0x70100
	s_addc_u32 s17, s11, 0
	s_add_u32 s14, s6, 0x70180
	v_add_u32_e32 v166, s15, v0
	s_addc_u32 s15, s7, 0
	s_add_u32 s6, s10, 0x70180
	s_mov_b32 s3, 0x8000
	s_mov_b32 s26, 0xc000
	s_addc_u32 s7, s11, 0
	s_mov_b32 s8, 0
	v_add_u32_e32 v163, 0, v2
	s_cmpk_gt_u32 s47, 0xff
	s_mov_b32 m0, s46
	v_lshl_add_u64 v[0:1], s[20:21], 0, v[158:159]
	ds_read_b128 v[36:39], v163
	ds_read_b128 v[40:43], v163 offset:1024
	ds_read_b128 v[44:47], v163 offset:2048
	ds_read_b128 v[48:51], v163 offset:3072
	ds_read_b128 v[68:71], v163 offset:4096
	ds_read_b128 v[72:75], v163 offset:5120
	ds_read_b128 v[76:79], v163 offset:6144
	ds_read_b128 v[80:83], v163 offset:7168
	global_load_lds_dwordx4 v[0:1], off
	v_lshl_add_u64 v[0:1], s[20:21], 0, v[144:145]
	s_mov_b32 m0, s45
	s_nop 0
	global_load_lds_dwordx4 v[0:1], off
	s_waitcnt vmcnt(8)
	s_waitcnt lgkmcnt(0)
	s_barrier
	s_setprio 3
	s_mov_b32 s9, s8
	s_mov_b32 s10, s8
	s_mov_b32 s11, s8
	v_mov_b64_e32 v[0:1], s[8:9]
	v_mov_b64_e32 v[30:31], s[10:11]
	v_mov_b64_e32 v[34:35], s[10:11]
	v_mov_b64_e32 v[22:23], s[10:11]
	v_mov_b64_e32 v[26:27], s[10:11]
	v_mov_b64_e32 v[14:15], s[10:11]
	v_mov_b64_e32 v[18:19], s[10:11]
	v_mov_b64_e32 v[4:5], s[8:9]
	v_mov_b64_e32 v[8:9], s[8:9]
	v_mov_b64_e32 v[2:3], s[10:11]
	v_mov_b64_e32 v[28:29], s[8:9]
	v_mov_b64_e32 v[32:33], s[8:9]
	v_mov_b64_e32 v[20:21], s[8:9]
	v_mov_b64_e32 v[24:25], s[8:9]
	v_mov_b64_e32 v[12:13], s[8:9]
	v_mov_b64_e32 v[16:17], s[8:9]
	v_mov_b64_e32 v[6:7], s[10:11]
	v_mov_b64_e32 v[10:11], s[10:11]
	v_mov_b32_e32 v164, 0x7f7f7f7f
	s_waitcnt lgkmcnt(0)
	v_mfma_f32_16x16x128_f8f6f4 v[28:31], v[96:103], v[36:43], v[28:31]
	v_mfma_f32_16x16x128_f8f6f4 v[32:35], v[104:111], v[36:43], v[32:35]
	v_mfma_f32_16x16x128_f8f6f4 v[20:23], v[96:103], v[44:51], v[20:23]
	v_mfma_f32_16x16x128_f8f6f4 v[24:27], v[104:111], v[44:51], v[24:27]
	v_mfma_f32_16x16x128_f8f6f4 v[12:15], v[96:103], v[68:75], v[12:15]
	v_mfma_f32_16x16x128_f8f6f4 v[16:19], v[104:111], v[68:75], v[16:19]
	v_mfma_f32_16x16x128_f8f6f4 v[4:7], v[96:103], v[76:83], v[4:7]
	v_mfma_f32_16x16x128_f8f6f4 v[8:11], v[104:111], v[76:83], v[8:11]
	s_setprio 0
	s_setprio 3
	v_mov_b64_e32 v[62:63], s[10:11]
	v_mov_b64_e32 v[66:67], s[10:11]
	v_mov_b64_e32 v[54:55], s[10:11]
	v_mov_b64_e32 v[58:59], s[10:11]
	v_mov_b64_e32 v[60:61], s[8:9]
	v_mov_b64_e32 v[64:65], s[8:9]
	v_mov_b64_e32 v[52:53], s[8:9]
	v_mov_b64_e32 v[56:57], s[8:9]
	v_mfma_f32_16x16x128_f8f6f4 v[60:63], v[170:177], v[36:43], v[60:63]
	v_mfma_f32_16x16x128_f8f6f4 v[64:67], v[178:185], v[36:43], v[64:67]
	v_mfma_f32_16x16x128_f8f6f4 v[52:55], v[170:177], v[44:51], v[52:55]
	v_mfma_f32_16x16x128_f8f6f4 v[56:59], v[178:185], v[44:51], v[56:59]
	v_mov_b64_e32 v[46:47], s[10:11]
	v_mov_b64_e32 v[50:51], s[10:11]
	v_mov_b64_e32 v[38:39], s[10:11]
	v_mov_b64_e32 v[42:43], s[10:11]
	v_mov_b64_e32 v[44:45], s[8:9]
	v_mov_b64_e32 v[48:49], s[8:9]
	v_mov_b64_e32 v[36:37], s[8:9]
	v_mov_b64_e32 v[40:41], s[8:9]
	v_mfma_f32_16x16x128_f8f6f4 v[44:47], v[170:177], v[68:75], v[44:47]
	v_mfma_f32_16x16x128_f8f6f4 v[48:51], v[178:185], v[68:75], v[48:51]
	v_mfma_f32_16x16x128_f8f6f4 v[36:39], v[170:177], v[76:83], v[36:39]
	v_mfma_f32_16x16x128_f8f6f4 v[40:43], v[178:185], v[76:83], v[40:43]
	s_setprio 0
	s_barrier
; #define PG8_STAGE(bufoff, gbase, voff) do { _Pragma("unroll") for (int _i = 0; _i < 2; ++_i) \
;         __builtin_amdgcn_global_load_lds((const unsigned*)((const char*)(gbase) + (voff)[_i]), (PG8_LAS unsigned*)(lds + (bufoff) + ldsw + _i * 8192), 16, 0, 0); } while (0)
; #define PG8_LDA(dst, b, h) do { _Pragma("unroll") for (int m = 0; m < 4; ++m) Frag<F8>::load(dst[m], lds + PG8_SA(b, h) + aoff + m * 2048); } while (0)
; #define PG8_LDB(dst, b, h) do { _Pragma("unroll") for (int n = 0; n < 2; ++n) Frag<F8>::load(dst[n], lds + PG8_SB(b, h) + boff + n * 2048); } while (0)
; #define PG8_MMA(ai, bj, At, Bt) do { __builtin_amdgcn_s_setprio(3); _Pragma("unroll") for (int m = 0; m < 4; ++m) _Pragma("unroll") for (int n = 0; n < 2; ++n) Frag<F8>::mma(acc[ai][bj][m][n], Bt[n], At[m]); \
;         __builtin_amdgcn_s_setprio(0); } while (0)
; #define PG8_WAIT_V(n) asm volatile("s_waitcnt vmcnt(" #n ")" ::: "memory")
; #define PG8_WAIT_L(n) asm volatile("s_waitcnt lgkmcnt(" #n ")" ::: "memory")
; #define PG8_BAR __builtin_amdgcn_s_barrier()
; #define PG8_SCHED __builtin_amdgcn_sched_barrier(0)
; template <class Epi, class Sched, bool ALIGN_EPI = false, bool SP2 = false, bool F8 = false>
; __device__ __forceinline__ void gemm_phase(PG8_LAS unsigned char* lds, const Gemm g, const Sched& S, const Epi& E) {
;     ...
;             PG8_WAIT_V(8); PG8_WAIT_L(0); PG8_BAR; PG8_MMA(0, 0, At, B0); PG8_MMA(0, 1, At, B1); PG8_BAR; PG8_SCHED;
;             PG8_LDA(At, 0, 1); PG8_STAGE(PG8_SB(0, 0), b2, voffB); PG8_STAGE(PG8_SB(0, 1), b2 + hstep, voffB); PG8_STAGE(PG8_SA(0, 0), a2, voffA);
;             PG8_WAIT_V(8); PG8_WAIT_L(0); PG8_BAR; PG8_MMA(1, 0, At, B0); PG8_MMA(1, 1, At, B1); PG8_BAR; PG8_SCHED;
;             PG8_LDB(B0, 1, 0); PG8_LDB(B1, 1, 1); PG8_SCHED; PG8_LDA(At, 1, 0); PG8_STAGE(PG8_SA(0, 1), a2 + hstep, voffA);
;             PG8_WAIT_V(8); PG8_WAIT_L(0); PG8_BAR; PG8_MMA(0, 0, At, B0); PG8_MMA(0, 1, At, B1); PG8_BAR; PG8_SCHED;
	s_mov_b64 s[8:9], 0x100
	s_mov_b32 m0, s42
	v_lshl_add_u64 v[68:69], v[154:155], 0, s[8:9]
	ds_read_b128 v[186:189], v163 offset:16384
	ds_read_b128 v[190:193], v163 offset:17408
	ds_read_b128 v[194:197], v163 offset:18432
	ds_read_b128 v[198:201], v163 offset:19456
	ds_read_b128 v[202:205], v163 offset:20480
	ds_read_b128 v[206:209], v163 offset:21504
	ds_read_b128 v[210:213], v163 offset:22528
	ds_read_b128 v[214:217], v163 offset:23552
	global_load_lds_dwordx4 v[68:69], off
	v_lshl_add_u64 v[68:69], v[156:157], 0, s[8:9]
	s_mov_b32 m0, s41
	s_nop 0
	global_load_lds_dwordx4 v[68:69], off
	v_lshl_add_u64 v[68:69], s[18:19], 0, v[158:159]
	s_mov_b32 m0, s44
	s_nop 0
	global_load_lds_dwordx4 v[68:69], off
	v_lshl_add_u64 v[68:69], s[18:19], 0, v[144:145]
	s_mov_b32 m0, s43
	s_nop 0
	global_load_lds_dwordx4 v[68:69], off
	v_lshl_add_u64 v[68:69], v[148:149], 0, s[8:9]
	s_mov_b32 m0, s4
	s_nop 0
	global_load_lds_dwordx4 v[68:69], off
	v_lshl_add_u64 v[68:69], v[146:147], 0, s[8:9]
	s_mov_b32 m0, s5
	s_nop 0
	global_load_lds_dwordx4 v[68:69], off
	s_waitcnt vmcnt(8)
	s_waitcnt lgkmcnt(0)
	s_barrier
	s_setprio 3
	v_mov_b64_e32 v[70:71], v[2:3]
	v_mov_b64_e32 v[86:87], v[2:3]
	v_mov_b64_e32 v[74:75], v[2:3]
	v_mov_b64_e32 v[90:91], v[2:3]
	v_mov_b64_e32 v[78:79], v[2:3]
	v_mov_b64_e32 v[94:95], v[2:3]
	v_mov_b64_e32 v[82:83], v[2:3]
	v_mov_b64_e32 v[68:69], v[0:1]
	v_mov_b64_e32 v[84:85], v[0:1]
	v_mov_b64_e32 v[72:73], v[0:1]
	v_mov_b64_e32 v[88:89], v[0:1]
	v_mov_b64_e32 v[76:77], v[0:1]
	v_mov_b64_e32 v[92:93], v[0:1]
	v_mov_b64_e32 v[80:81], v[0:1]
	s_waitcnt lgkmcnt(0)
	v_mfma_f32_16x16x128_f8f6f4 v[68:71], v[96:103], v[186:193], v[68:71]
	v_mfma_f32_16x16x128_f8f6f4 v[84:87], v[104:111], v[186:193], v[84:87]
	v_mfma_f32_16x16x128_f8f6f4 v[72:75], v[96:103], v[194:201], v[72:75]
	v_mfma_f32_16x16x128_f8f6f4 v[88:91], v[104:111], v[194:201], v[88:91]
	v_mfma_f32_16x16x128_f8f6f4 v[76:79], v[96:103], v[202:209], v[76:79]
	v_mfma_f32_16x16x128_f8f6f4 v[92:95], v[104:111], v[202:209], v[92:95]
	v_mfma_f32_16x16x128_f8f6f4 v[80:83], v[96:103], v[210:217], v[80:83]
	v_mov_b64_e32 v[98:99], v[2:3]
	v_mov_b64_e32 v[96:97], v[0:1]
	v_mfma_f32_16x16x128_f8f6f4 v[96:99], v[104:111], v[210:217], v[96:99]
	s_setprio 0
	s_setprio 3
	v_mov_b64_e32 v[118:119], v[2:3]
	v_mov_b64_e32 v[126:127], v[2:3]
	v_mov_b64_e32 v[110:111], v[2:3]
	v_mov_b64_e32 v[122:123], v[2:3]
	v_mov_b64_e32 v[106:107], v[2:3]
	v_mov_b64_e32 v[114:115], v[2:3]
	v_mov_b64_e32 v[102:103], v[2:3]
	v_mov_b64_e32 v[116:117], v[0:1]
	v_mov_b64_e32 v[124:125], v[0:1]
	v_mov_b64_e32 v[108:109], v[0:1]
	v_mov_b64_e32 v[120:121], v[0:1]
	v_mov_b64_e32 v[104:105], v[0:1]
	v_mov_b64_e32 v[112:113], v[0:1]
	v_mov_b64_e32 v[100:101], v[0:1]
	v_mfma_f32_16x16x128_f8f6f4 v[116:119], v[170:177], v[186:193], v[116:119]
	v_mfma_f32_16x16x128_f8f6f4 v[124:127], v[178:185], v[186:193], v[124:127]
	v_mfma_f32_16x16x128_f8f6f4 v[108:111], v[170:177], v[194:201], v[108:111]
	v_mfma_f32_16x16x128_f8f6f4 v[120:123], v[178:185], v[194:201], v[120:123]
	v_mfma_f32_16x16x128_f8f6f4 v[104:107], v[170:177], v[202:209], v[104:107]
	v_mfma_f32_16x16x128_f8f6f4 v[112:115], v[178:185], v[202:209], v[112:115]
	v_mfma_f32_16x16x128_f8f6f4 v[100:103], v[170:177], v[210:217], v[100:103]
	v_mfma_f32_16x16x128_f8f6f4 v[0:3], v[178:185], v[210:217], v[0:3]
	s_setprio 0
	s_barrier
	ds_read_b128 v[170:173], v166
	ds_read_b128 v[174:177], v166 offset:1024
	ds_read_b128 v[178:181], v166 offset:2048
	ds_read_b128 v[182:185], v166 offset:3072
	ds_read_b128 v[186:189], v165
	ds_read_b128 v[190:193], v165 offset:1024
	ds_read_b128 v[194:197], v165 offset:2048
	ds_read_b128 v[198:201], v165 offset:3072
	s_mov_b32 m0, s33
	v_lshl_add_u64 v[234:235], s[16:17], 0, v[158:159]
	ds_read_b128 v[202:205], v163 offset:32768
	ds_read_b128 v[206:209], v163 offset:33792
	ds_read_b128 v[210:213], v163 offset:34816
	ds_read_b128 v[214:217], v163 offset:35840
	ds_read_b128 v[218:221], v163 offset:36864
	ds_read_b128 v[222:225], v163 offset:37888
	ds_read_b128 v[226:229], v163 offset:38912
	ds_read_b128 v[230:233], v163 offset:39936
	global_load_lds_dwordx4 v[234:235], off
	v_lshl_add_u64 v[234:235], s[16:17], 0, v[144:145]
	s_mov_b32 m0, s40
	s_nop 0
	global_load_lds_dwordx4 v[234:235], off
	s_waitcnt vmcnt(8)
	s_waitcnt lgkmcnt(0)
	s_barrier
	s_setprio 3
	s_waitcnt lgkmcnt(0)
	v_mfma_f32_16x16x128_f8f6f4 v[28:31], v[170:177], v[202:209], v[28:31]
	v_mfma_f32_16x16x128_f8f6f4 v[32:35], v[178:185], v[202:209], v[32:35]
	v_mfma_f32_16x16x128_f8f6f4 v[20:23], v[170:177], v[210:217], v[20:23]
	v_mfma_f32_16x16x128_f8f6f4 v[24:27], v[178:185], v[210:217], v[24:27]
	v_mfma_f32_16x16x128_f8f6f4 v[12:15], v[170:177], v[218:225], v[12:15]
	v_mfma_f32_16x16x128_f8f6f4 v[16:19], v[178:185], v[218:225], v[16:19]
	v_mfma_f32_16x16x128_f8f6f4 v[4:7], v[170:177], v[226:233], v[4:7]
	v_mfma_f32_16x16x128_f8f6f4 v[8:11], v[178:185], v[226:233], v[8:11]
	s_setprio 0
	s_setprio 3
	v_mfma_f32_16x16x128_f8f6f4 v[60:63], v[186:193], v[202:209], v[60:63]
	v_mfma_f32_16x16x128_f8f6f4 v[64:67], v[194:201], v[202:209], v[64:67]
	v_mfma_f32_16x16x128_f8f6f4 v[52:55], v[186:193], v[210:217], v[52:55]
	v_mfma_f32_16x16x128_f8f6f4 v[56:59], v[194:201], v[210:217], v[56:59]
	v_mfma_f32_16x16x128_f8f6f4 v[44:47], v[186:193], v[218:225], v[44:47]
	v_mfma_f32_16x16x128_f8f6f4 v[48:51], v[194:201], v[218:225], v[48:51]
	v_mfma_f32_16x16x128_f8f6f4 v[36:39], v[186:193], v[226:233], v[36:39]
	v_mfma_f32_16x16x128_f8f6f4 v[40:43], v[194:201], v[226:233], v[40:43]
	s_setprio 0
	s_barrier
; #define PG8_STAGE(bufoff, gbase, voff) do { _Pragma("unroll") for (int _i = 0; _i < 2; ++_i) \
;         __builtin_amdgcn_global_load_lds((const unsigned*)((const char*)(gbase) + (voff)[_i]), (PG8_LAS unsigned*)(lds + (bufoff) + ldsw + _i * 8192), 16, 0, 0); } while (0)
; #define PG8_LDA(dst, b, h) do { _Pragma("unroll") for (int m = 0; m < 4; ++m) Frag<F8>::load(dst[m], lds + PG8_SA(b, h) + aoff + m * 2048); } while (0)
; #define PG8_MMA(ai, bj, At, Bt) do { __builtin_amdgcn_s_setprio(3); _Pragma("unroll") for (int m = 0; m < 4; ++m) _Pragma("unroll") for (int n = 0; n < 2; ++n) Frag<F8>::mma(acc[ai][bj][m][n], Bt[n], At[m]); \
;         __builtin_amdgcn_s_setprio(0); } while (0)
; #define PG8_WAIT_V(n) asm volatile("s_waitcnt vmcnt(" #n ")" ::: "memory")
; #define PG8_WAIT_L(n) asm volatile("s_waitcnt lgkmcnt(" #n ")" ::: "memory")
; #define PG8_BAR __builtin_amdgcn_s_barrier()
; #define PG8_SCHED __builtin_amdgcn_sched_barrier(0)
; template <class Epi, class Sched, bool ALIGN_EPI = false, bool SP2 = false, bool F8 = false>
; __device__ __forceinline__ void gemm_phase(PG8_LAS unsigned char* lds, const Gemm g, const Sched& S, const Epi& E) {
;     ...
;             PG8_WAIT_V(8); PG8_WAIT_L(0); PG8_BAR; PG8_MMA(0, 0, At, B0); PG8_MMA(0, 1, At, B1); PG8_BAR; PG8_SCHED;
;             PG8_LDA(At, 1, 1); PG8_STAGE(PG8_SB(1, 0), b3, voffB); PG8_STAGE(PG8_SB(1, 1), b3 + hstep, voffB); PG8_STAGE(PG8_SA(1, 0), a3, voffA);
;             PG8_WAIT_V(8); PG8_WAIT_L(0); PG8_BAR; PG8_MMA(1, 0, At, B0); PG8_MMA(1, 1, At, B1); PG8_BAR; PG8_SCHED;
	s_mov_b64 s[8:9], 0x180
	s_mov_b32 m0, s30
	v_lshl_add_u64 v[234:235], v[154:155], 0, s[8:9]
	ds_read_b128 v[202:205], v163 offset:49152
	ds_read_b128 v[206:209], v163 offset:50176
	ds_read_b128 v[210:213], v163 offset:51200
	ds_read_b128 v[214:217], v163 offset:52224
	ds_read_b128 v[218:221], v163 offset:53248
	ds_read_b128 v[222:225], v163 offset:54272
	ds_read_b128 v[226:229], v163 offset:55296
	ds_read_b128 v[230:233], v163 offset:56320
	global_load_lds_dwordx4 v[234:235], off
	v_lshl_add_u64 v[234:235], v[156:157], 0, s[8:9]
	s_mov_b32 m0, s36
	s_nop 0
	global_load_lds_dwordx4 v[234:235], off
	v_lshl_add_u64 v[234:235], s[14:15], 0, v[158:159]
	s_mov_b32 m0, s38
	s_nop 0
	global_load_lds_dwordx4 v[234:235], off
	v_lshl_add_u64 v[234:235], s[14:15], 0, v[144:145]
	s_mov_b32 m0, s39
	s_nop 0
	global_load_lds_dwordx4 v[234:235], off
	v_lshl_add_u64 v[234:235], v[148:149], 0, s[8:9]
	s_mov_b32 m0, s31
	s_nop 0
	global_load_lds_dwordx4 v[234:235], off
	v_lshl_add_u64 v[234:235], v[146:147], 0, s[8:9]
	s_mov_b32 m0, s37
	s_nop 0
	global_load_lds_dwordx4 v[234:235], off
	s_waitcnt vmcnt(8)
	s_waitcnt lgkmcnt(0)
	s_barrier
	s_setprio 3
	s_waitcnt lgkmcnt(0)
	v_mfma_f32_16x16x128_f8f6f4 v[68:71], v[170:177], v[202:209], v[68:71]
	v_mfma_f32_16x16x128_f8f6f4 v[84:87], v[178:185], v[202:209], v[84:87]
	v_mfma_f32_16x16x128_f8f6f4 v[72:75], v[170:177], v[210:217], v[72:75]
	v_mfma_f32_16x16x128_f8f6f4 v[88:91], v[178:185], v[210:217], v[88:91]
	v_mfma_f32_16x16x128_f8f6f4 v[76:79], v[170:177], v[218:225], v[76:79]
	v_mfma_f32_16x16x128_f8f6f4 v[92:95], v[178:185], v[218:225], v[92:95]
	v_mfma_f32_16x16x128_f8f6f4 v[80:83], v[170:177], v[226:233], v[80:83]
	v_mfma_f32_16x16x128_f8f6f4 v[96:99], v[178:185], v[226:233], v[96:99]
	s_setprio 0
	s_setprio 3
	v_mfma_f32_16x16x128_f8f6f4 v[116:119], v[186:193], v[202:209], v[116:119]
	v_mfma_f32_16x16x128_f8f6f4 v[124:127], v[194:201], v[202:209], v[124:127]
	v_mfma_f32_16x16x128_f8f6f4 v[108:111], v[186:193], v[210:217], v[108:111]
	v_mfma_f32_16x16x128_f8f6f4 v[120:123], v[194:201], v[210:217], v[120:123]
	v_mfma_f32_16x16x128_f8f6f4 v[104:107], v[186:193], v[218:225], v[104:107]
	v_mfma_f32_16x16x128_f8f6f4 v[112:115], v[194:201], v[218:225], v[112:115]
	v_mfma_f32_16x16x128_f8f6f4 v[100:103], v[186:193], v[226:233], v[100:103]
	v_mfma_f32_16x16x128_f8f6f4 v[0:3], v[194:201], v[226:233], v[0:3]
	s_setprio 0
	s_barrier
	ds_read_b128 v[170:173], v168
	ds_read_b128 v[174:177], v168 offset:1024
	ds_read_b128 v[178:181], v168 offset:2048
	ds_read_b128 v[182:185], v168 offset:3072
	ds_read_b128 v[186:189], v167
	ds_read_b128 v[190:193], v167 offset:1024
	ds_read_b128 v[194:197], v167 offset:2048
	ds_read_b128 v[198:201], v167 offset:3072
	s_mov_b32 m0, s46
	v_lshl_add_u64 v[158:159], s[6:7], 0, v[158:159]
	ds_read_b128 v[202:205], v163
	ds_read_b128 v[206:209], v163 offset:1024
	ds_read_b128 v[210:213], v163 offset:2048
	ds_read_b128 v[214:217], v163 offset:3072
	ds_read_b128 v[218:221], v163 offset:4096
	ds_read_b128 v[222:225], v163 offset:5120
	ds_read_b128 v[226:229], v163 offset:6144
	ds_read_b128 v[230:233], v163 offset:7168
	global_load_lds_dwordx4 v[158:159], off
	v_lshl_add_u64 v[144:145], s[6:7], 0, v[144:145]
	s_mov_b32 m0, s45
	s_nop 0
	global_load_lds_dwordx4 v[144:145], off
	s_waitcnt vmcnt(8)
	s_waitcnt lgkmcnt(0)
	s_barrier
	s_setprio 3
	s_waitcnt lgkmcnt(0)
	v_mfma_f32_16x16x128_f8f6f4 v[28:31], v[170:177], v[202:209], v[28:31]
	v_mfma_f32_16x16x128_f8f6f4 v[32:35], v[178:185], v[202:209], v[32:35]
	v_mfma_f32_16x16x128_f8f6f4 v[20:23], v[170:177], v[210:217], v[20:23]
	v_mfma_f32_16x16x128_f8f6f4 v[24:27], v[178:185], v[210:217], v[24:27]
	v_mfma_f32_16x16x128_f8f6f4 v[12:15], v[170:177], v[218:225], v[12:15]
	v_mfma_f32_16x16x128_f8f6f4 v[16:19], v[178:185], v[218:225], v[16:19]
	v_mfma_f32_16x16x128_f8f6f4 v[4:7], v[170:177], v[226:233], v[4:7]
	v_mfma_f32_16x16x128_f8f6f4 v[8:11], v[178:185], v[226:233], v[8:11]
	s_setprio 0
	s_setprio 3
	v_mfma_f32_16x16x128_f8f6f4 v[60:63], v[186:193], v[202:209], v[60:63]
	v_mfma_f32_16x16x128_f8f6f4 v[64:67], v[194:201], v[202:209], v[64:67]
	v_mfma_f32_16x16x128_f8f6f4 v[52:55], v[186:193], v[210:217], v[52:55]
	v_mfma_f32_16x16x128_f8f6f4 v[56:59], v[194:201], v[210:217], v[56:59]
	v_mfma_f32_16x16x128_f8f6f4 v[44:47], v[186:193], v[218:225], v[44:47]
	v_mfma_f32_16x16x128_f8f6f4 v[48:51], v[194:201], v[218:225], v[48:51]
	v_mfma_f32_16x16x128_f8f6f4 v[36:39], v[186:193], v[226:233], v[36:39]
	v_mfma_f32_16x16x128_f8f6f4 v[40:43], v[194:201], v[226:233], v[40:43]
	s_setprio 0
	s_barrier
	s_mov_b32 m0, s42
	ds_read_b128 v[202:205], v163 offset:16384
	ds_read_b128 v[206:209], v163 offset:17408
	ds_read_b128 v[210:213], v163 offset:18432
	ds_read_b128 v[214:217], v163 offset:19456
	ds_read_b128 v[218:221], v163 offset:20480
	ds_read_b128 v[222:225], v163 offset:21504
	ds_read_b128 v[226:229], v163 offset:22528
	ds_read_b128 v[230:233], v163 offset:23552
	global_load_lds_dwordx4 v[154:155], off
	s_mov_b32 m0, s41
	s_nop 0
	global_load_lds_dwordx4 v[156:157], off
	s_mov_b32 m0, s44
	s_nop 0
	global_load_lds_dwordx4 v[152:153], off
	s_mov_b32 m0, s43
	s_nop 0
	global_load_lds_dwordx4 v[150:151], off
	s_mov_b32 m0, s4
	s_nop 0
	global_load_lds_dwordx4 v[148:149], off
	s_mov_b32 m0, s5
	s_nop 0
	global_load_lds_dwordx4 v[146:147], off
	s_waitcnt vmcnt(8)
	s_waitcnt lgkmcnt(0)
	s_barrier
; #define PG8_STAGE(bufoff, gbase, voff) do { _Pragma("unroll") for (int _i = 0; _i < 2; ++_i) \
;         __builtin_amdgcn_global_load_lds((const unsigned*)((const char*)(gbase) + (voff)[_i]), (PG8_LAS unsigned*)(lds + (bufoff) + ldsw + _i * 8192), 16, 0, 0); } while (0)
; #define PG8_LDA(dst, b, h) do { _Pragma("unroll") for (int m = 0; m < 4; ++m) Frag<F8>::load(dst[m], lds + PG8_SA(b, h) + aoff + m * 2048); } while (0)
; #define PG8_MMA(ai, bj, At, Bt) do { __builtin_amdgcn_s_setprio(3); _Pragma("unroll") for (int m = 0; m < 4; ++m) _Pragma("unroll") for (int n = 0; n < 2; ++n) Frag<F8>::mma(acc[ai][bj][m][n], Bt[n], At[m]); \
;         __builtin_amdgcn_s_setprio(0); } while (0)
; #define PG8_WAIT_V(n) asm volatile("s_waitcnt vmcnt(" #n ")" ::: "memory")
; #define PG8_WAIT_L(n) asm volatile("s_waitcnt lgkmcnt(" #n ")" ::: "memory")
; #define PG8_BAR __builtin_amdgcn_s_barrier()
; #define PG8_SCHED __builtin_amdgcn_sched_barrier(0)
; template <class Epi, class Sched, bool ALIGN_EPI = false, bool SP2 = false, bool F8 = false>
; __device__ __forceinline__ void gemm_phase(PG8_LAS unsigned char* lds, const Gemm g, const Sched& S, const Epi& E) {
;     ...
;             PG8_LDA(At, 1, 1); PG8_STAGE(PG8_SB(1, 0), b3, voffB); PG8_STAGE(PG8_SB(1, 1), b3 + hstep, voffB); PG8_STAGE(PG8_SA(1, 0), a3, voffA);
;             PG8_WAIT_V(8); PG8_WAIT_L(0); PG8_BAR; PG8_MMA(1, 0, At, B0); PG8_MMA(1, 1, At, B1); PG8_BAR; PG8_SCHED;
;     ...
;     PG8_WAIT_V(0);
;     if constexpr (!ALIGN_EPI) { if (wr == 0) PG8_BAR; }
	s_setprio 3
	s_waitcnt lgkmcnt(0)
	v_mfma_f32_16x16x128_f8f6f4 v[68:71], v[170:177], v[202:209], v[68:71]
	v_mfma_f32_16x16x128_f8f6f4 v[84:87], v[178:185], v[202:209], v[84:87]
	v_mfma_f32_16x16x128_f8f6f4 v[72:75], v[170:177], v[210:217], v[72:75]
	v_mfma_f32_16x16x128_f8f6f4 v[88:91], v[178:185], v[210:217], v[88:91]
	v_mfma_f32_16x16x128_f8f6f4 v[76:79], v[170:177], v[218:225], v[76:79]
	v_mfma_f32_16x16x128_f8f6f4 v[92:95], v[178:185], v[218:225], v[92:95]
	v_mfma_f32_16x16x128_f8f6f4 v[80:83], v[170:177], v[226:233], v[80:83]
	v_mfma_f32_16x16x128_f8f6f4 v[96:99], v[178:185], v[226:233], v[96:99]
	s_setprio 0
	s_setprio 3
	v_mfma_f32_16x16x128_f8f6f4 v[116:119], v[186:193], v[202:209], v[116:119]
	v_mfma_f32_16x16x128_f8f6f4 v[124:127], v[194:201], v[202:209], v[124:127]
	v_mfma_f32_16x16x128_f8f6f4 v[108:111], v[186:193], v[210:217], v[108:111]
	v_mfma_f32_16x16x128_f8f6f4 v[120:123], v[194:201], v[210:217], v[120:123]
	v_mfma_f32_16x16x128_f8f6f4 v[104:107], v[186:193], v[218:225], v[104:107]
	v_mfma_f32_16x16x128_f8f6f4 v[112:115], v[194:201], v[218:225], v[112:115]
	v_mfma_f32_16x16x128_f8f6f4 v[100:103], v[186:193], v[226:233], v[100:103]
	v_mfma_f32_16x16x128_f8f6f4 v[0:3], v[194:201], v[226:233], v[0:3]
	s_setprio 0
	s_barrier
	ds_read_b128 v[144:147], v166
	ds_read_b128 v[148:151], v166 offset:1024
	ds_read_b128 v[152:155], v166 offset:2048
	ds_read_b128 v[156:159], v166 offset:3072
	ds_read_b128 v[166:169], v165
	ds_read_b128 v[170:173], v165 offset:1024
	ds_read_b128 v[174:177], v165 offset:2048
	ds_read_b128 v[178:181], v165 offset:3072
	s_mov_b32 m0, s33
	ds_read_b128 v[182:185], v163 offset:32768
	ds_read_b128 v[186:189], v163 offset:33792
	ds_read_b128 v[190:193], v163 offset:34816
	ds_read_b128 v[194:197], v163 offset:35840
	ds_read_b128 v[198:201], v163 offset:36864
	ds_read_b128 v[202:205], v163 offset:37888
	ds_read_b128 v[206:209], v163 offset:38912
	ds_read_b128 v[210:213], v163 offset:39936
	global_load_lds_dwordx4 v[140:141], off
	s_mov_b32 m0, s40
	s_nop 0
	global_load_lds_dwordx4 v[142:143], off
	s_waitcnt vmcnt(8)
	s_waitcnt lgkmcnt(0)
	s_barrier
	s_setprio 3
	s_waitcnt lgkmcnt(0)
	v_mfma_f32_16x16x128_f8f6f4 v[28:31], v[144:151], v[182:189], v[28:31]
	v_mfma_f32_16x16x128_f8f6f4 v[32:35], v[152:159], v[182:189], v[32:35]
	v_mfma_f32_16x16x128_f8f6f4 v[20:23], v[144:151], v[190:197], v[20:23]
	v_mfma_f32_16x16x128_f8f6f4 v[24:27], v[152:159], v[190:197], v[24:27]
	v_mfma_f32_16x16x128_f8f6f4 v[12:15], v[144:151], v[198:205], v[12:15]
	v_mfma_f32_16x16x128_f8f6f4 v[16:19], v[152:159], v[198:205], v[16:19]
	v_mfma_f32_16x16x128_f8f6f4 v[4:7], v[144:151], v[206:213], v[4:7]
	v_mfma_f32_16x16x128_f8f6f4 v[8:11], v[152:159], v[206:213], v[8:11]
	s_setprio 0
	s_setprio 3
	v_mfma_f32_16x16x128_f8f6f4 v[60:63], v[166:173], v[182:189], v[60:63]
	v_mfma_f32_16x16x128_f8f6f4 v[64:67], v[174:181], v[182:189], v[64:67]
	v_mfma_f32_16x16x128_f8f6f4 v[52:55], v[166:173], v[190:197], v[52:55]
	v_mfma_f32_16x16x128_f8f6f4 v[56:59], v[174:181], v[190:197], v[56:59]
	v_mfma_f32_16x16x128_f8f6f4 v[44:47], v[166:173], v[198:205], v[44:47]
	v_mfma_f32_16x16x128_f8f6f4 v[48:51], v[174:181], v[198:205], v[48:51]
	v_mfma_f32_16x16x128_f8f6f4 v[36:39], v[166:173], v[206:213], v[36:39]
	v_mfma_f32_16x16x128_f8f6f4 v[40:43], v[174:181], v[206:213], v[40:43]
	s_setprio 0
	s_barrier
	s_mov_b32 m0, s30
	ds_read_b128 v[182:185], v163 offset:49152
	ds_read_b128 v[186:189], v163 offset:50176
	ds_read_b128 v[190:193], v163 offset:51200
	ds_read_b128 v[194:197], v163 offset:52224
	ds_read_b128 v[198:201], v163 offset:53248
	ds_read_b128 v[202:205], v163 offset:54272
	ds_read_b128 v[206:209], v163 offset:55296
	ds_read_b128 v[210:213], v163 offset:56320
	global_load_lds_dwordx4 v[130:131], off
	s_mov_b32 m0, s36
	s_nop 0
	global_load_lds_dwordx4 v[132:133], off
	s_mov_b32 m0, s38
	s_nop 0
	global_load_lds_dwordx4 v[136:137], off
	s_mov_b32 m0, s39
	s_nop 0
	global_load_lds_dwordx4 v[138:139], off
	s_mov_b32 m0, s31
	s_nop 0
	global_load_lds_dwordx4 v[128:129], off
	s_mov_b32 m0, s37
	s_nop 0
	global_load_lds_dwordx4 v[134:135], off
	s_waitcnt vmcnt(8)
	s_waitcnt lgkmcnt(0)
	s_barrier
	s_setprio 3
	s_waitcnt lgkmcnt(0)
	v_mfma_f32_16x16x128_f8f6f4 v[68:71], v[144:151], v[182:189], v[68:71]
	v_mfma_f32_16x16x128_f8f6f4 v[84:87], v[152:159], v[182:189], v[84:87]
	v_mfma_f32_16x16x128_f8f6f4 v[72:75], v[144:151], v[190:197], v[72:75]
	v_mfma_f32_16x16x128_f8f6f4 v[88:91], v[152:159], v[190:197], v[88:91]
	v_mfma_f32_16x16x128_f8f6f4 v[76:79], v[144:151], v[198:205], v[76:79]
	v_mfma_f32_16x16x128_f8f6f4 v[92:95], v[152:159], v[198:205], v[92:95]
	v_mfma_f32_16x16x128_f8f6f4 v[80:83], v[144:151], v[206:213], v[80:83]
	v_mfma_f32_16x16x128_f8f6f4 v[96:99], v[152:159], v[206:213], v[96:99]
	s_setprio 0
	s_setprio 3
	v_mfma_f32_16x16x128_f8f6f4 v[116:119], v[166:173], v[182:189], v[116:119]
	v_mfma_f32_16x16x128_f8f6f4 v[124:127], v[174:181], v[182:189], v[124:127]
	v_mfma_f32_16x16x128_f8f6f4 v[108:111], v[166:173], v[190:197], v[108:111]
	v_mfma_f32_16x16x128_f8f6f4 v[120:123], v[174:181], v[190:197], v[120:123]
	v_mfma_f32_16x16x128_f8f6f4 v[104:107], v[166:173], v[198:205], v[104:107]
	v_mfma_f32_16x16x128_f8f6f4 v[112:115], v[174:181], v[198:205], v[112:115]
	v_mfma_f32_16x16x128_f8f6f4 v[100:103], v[166:173], v[206:213], v[100:103]
	v_mfma_f32_16x16x128_f8f6f4 v[0:3], v[174:181], v[206:213], v[0:3]
	s_setprio 0
	s_barrier
	s_cbranch_scc1 .LBB0_1420
	s_barrier
